# bundle: diff-attn softmax adds into LDS wait windows, q-load/DMA overlap at unit start, GEMM first 3 MFMAs before barrier, nt loads in mla_fin, P0 adaLN 16 loads in flight, moe_gu index table via LDS-
# speedup vs baseline: 1.0123x; 1.0063x over previous
; #define LAS __attribute__((address_space(3)))
; __device__ __forceinline__ void p0_prologue(Frame& F, const InPtrs& A) {
;     ...
;             const int layer = it / 24, cb = it % 24, col = cb * 256 + 4 * F.lane, kbase = F.wave * 128;
;             const float* W = A[I_ADAW] + (size_t)layer * 1024 * 6144 + col;
;             f32x4 acc[9];
; #pragma unroll
;             for (int r = 0; r < 9; ++r) acc[r] = (f32x4){0.f, 0.f, 0.f, 0.f};
; #pragma unroll 4
;             for (int k = 0; k < 128; ++k) { const f32x4 w = *(const f32x4*)(W + (size_t)(kbase + k) * 6144);
; #pragma unroll
;                 for (int r = 0; r < 9; ++r) acc[r] += w * sv[r * 1024 + kbase + k]; }
; #pragma unroll
;             for (int r = 0; r < 9; ++r) *(LAS f32x4*)(red + (F.wave * 9 + r) * 256 + 4 * F.lane) = acc[r];
.LBB0_22:
	v_lshl_add_u64 v[44:45], v[42:43], 0, s[6:7]
	global_load_dwordx4 v[52:55], v[44:45], off
	v_add_co_u32_e32 v140, vcc, s18, v44
	s_nop 1
	v_addc_co_u32_e32 v141, vcc, 0, v45, vcc
	global_load_dwordx4 v[94:97], v[140:141], off
	v_add_co_u32_e32 v142, vcc, s35, v44
	s_nop 1
	v_addc_co_u32_e32 v143, vcc, 0, v45, vcc
	global_load_dwordx4 v[98:101], v[142:143], off
	v_add_co_u32_e32 v144, vcc, s36, v44
	s_nop 1
	v_addc_co_u32_e32 v145, vcc, 0, v45, vcc
	global_load_dwordx4 v[102:105], v[144:145], off
	s_add_u32 s6, s6, 0x18000
	s_addc_u32 s7, s7, 0
	v_lshl_add_u64 v[44:45], v[42:43], 0, s[6:7]
	global_load_dwordx4 v[160:163], v[44:45], off
	v_add_co_u32_e32 v140, vcc, s18, v44
	s_nop 1
	v_addc_co_u32_e32 v141, vcc, 0, v45, vcc
	global_load_dwordx4 v[164:167], v[140:141], off
	v_add_co_u32_e32 v142, vcc, s35, v44
	s_nop 1
	v_addc_co_u32_e32 v143, vcc, 0, v45, vcc
	global_load_dwordx4 v[168:171], v[142:143], off
	v_add_co_u32_e32 v144, vcc, s36, v44
	s_nop 1
	v_addc_co_u32_e32 v145, vcc, 0, v45, vcc
	global_load_dwordx4 v[172:175], v[144:145], off
	s_add_u32 s6, s6, 0x18000
	s_addc_u32 s7, s7, 0
	v_lshl_add_u64 v[44:45], v[42:43], 0, s[6:7]
	global_load_dwordx4 v[176:179], v[44:45], off
	v_add_co_u32_e32 v140, vcc, s18, v44
	s_nop 1
	v_addc_co_u32_e32 v141, vcc, 0, v45, vcc
	global_load_dwordx4 v[180:183], v[140:141], off
	v_add_co_u32_e32 v142, vcc, s35, v44
	s_nop 1
	v_addc_co_u32_e32 v143, vcc, 0, v45, vcc
	global_load_dwordx4 v[184:187], v[142:143], off
	v_add_co_u32_e32 v144, vcc, s36, v44
	s_nop 1
	v_addc_co_u32_e32 v145, vcc, 0, v45, vcc
	global_load_dwordx4 v[192:195], v[144:145], off
	s_add_u32 s6, s6, 0x18000
	s_addc_u32 s7, s7, 0
	v_lshl_add_u64 v[44:45], v[42:43], 0, s[6:7]
	global_load_dwordx4 v[196:199], v[44:45], off
	v_add_co_u32_e32 v140, vcc, s18, v44
	s_nop 1
	v_addc_co_u32_e32 v141, vcc, 0, v45, vcc
	global_load_dwordx4 v[200:203], v[140:141], off
	v_add_co_u32_e32 v142, vcc, s35, v44
	s_nop 1
	v_addc_co_u32_e32 v143, vcc, 0, v45, vcc
	global_load_dwordx4 v[204:207], v[142:143], off
	v_add_co_u32_e32 v144, vcc, s36, v44
	s_nop 1
	v_addc_co_u32_e32 v145, vcc, 0, v45, vcc
	global_load_dwordx4 v[208:211], v[144:145], off
	s_add_u32 s6, s6, 0x18000
	s_addc_u32 s7, s7, 0
	v_mov_b32_e32 v40, s8
	ds_read_b128 v[56:59], v40
	ds_read_b128 v[60:63], v40 offset:32768
	ds_read_b128 v[66:69], v40 offset:4096
	ds_read_b128 v[70:73], v40 offset:8192
	ds_read_b128 v[74:77], v40 offset:12288
	ds_read_b128 v[78:81], v40 offset:16384
	ds_read_b128 v[82:85], v40 offset:20480
	ds_read_b128 v[86:89], v40 offset:24576
	ds_read_b128 v[90:93], v40 offset:28672
	s_add_i32 s8, s8, 16
	s_waitcnt lgkmcnt(8)
	v_mov_b32_e32 v40, v59
	s_waitcnt lgkmcnt(6)
	v_mov_b32_e32 v44, v69
	s_waitcnt lgkmcnt(5)
	v_mov_b32_e32 v64, v73
	s_waitcnt lgkmcnt(4)
	v_mov_b32_e32 v106, v77
	s_waitcnt lgkmcnt(3)
	v_mov_b32_e32 v108, v81
	s_waitcnt lgkmcnt(2)
	v_mov_b32_e32 v110, v85
	s_waitcnt lgkmcnt(1)
	v_mov_b32_e32 v112, v89
	s_waitcnt lgkmcnt(0)
	v_mov_b32_e32 v114, v93
	v_mov_b32_e32 v116, v63
	s_waitcnt vmcnt(15)
	v_pk_fma_f32 v[34:35], v[54:55], v[56:57], v[34:35] op_sel_hi:[1,0,1]
	v_pk_fma_f32 v[32:33], v[52:53], v[56:57], v[32:33] op_sel_hi:[1,0,1]
	v_pk_fma_f32 v[30:31], v[54:55], v[66:67], v[30:31] op_sel_hi:[1,0,1]
	v_pk_fma_f32 v[28:29], v[52:53], v[66:67], v[28:29] op_sel_hi:[1,0,1]
	v_pk_fma_f32 v[26:27], v[54:55], v[70:71], v[26:27] op_sel_hi:[1,0,1]
	v_pk_fma_f32 v[24:25], v[52:53], v[70:71], v[24:25] op_sel_hi:[1,0,1]
	v_pk_fma_f32 v[22:23], v[54:55], v[74:75], v[22:23] op_sel_hi:[1,0,1]
	v_pk_fma_f32 v[20:21], v[52:53], v[74:75], v[20:21] op_sel_hi:[1,0,1]
	v_pk_fma_f32 v[18:19], v[54:55], v[78:79], v[18:19] op_sel_hi:[1,0,1]
	v_pk_fma_f32 v[16:17], v[52:53], v[78:79], v[16:17] op_sel_hi:[1,0,1]
	v_pk_fma_f32 v[14:15], v[54:55], v[82:83], v[14:15] op_sel_hi:[1,0,1]
	v_pk_fma_f32 v[12:13], v[52:53], v[82:83], v[12:13] op_sel_hi:[1,0,1]
	v_pk_fma_f32 v[10:11], v[54:55], v[86:87], v[10:11] op_sel_hi:[1,0,1]
	v_pk_fma_f32 v[8:9], v[52:53], v[86:87], v[8:9] op_sel_hi:[1,0,1]
	v_pk_fma_f32 v[6:7], v[54:55], v[90:91], v[6:7] op_sel_hi:[1,0,1]
	v_pk_fma_f32 v[4:5], v[52:53], v[90:91], v[4:5] op_sel_hi:[1,0,1]
	v_pk_fma_f32 v[2:3], v[54:55], v[60:61], v[2:3] op_sel_hi:[1,0,1]
	v_pk_fma_f32 v[0:1], v[52:53], v[60:61], v[0:1] op_sel_hi:[1,0,1]
	s_waitcnt vmcnt(14)
	v_pk_fma_f32 v[32:33], v[94:95], v[56:57], v[32:33] op_sel:[0,1,0]
	v_pk_fma_f32 v[34:35], v[96:97], v[56:57], v[34:35] op_sel:[0,1,0]
	v_pk_fma_f32 v[28:29], v[94:95], v[66:67], v[28:29] op_sel:[0,1,0]
	v_pk_fma_f32 v[30:31], v[96:97], v[66:67], v[30:31] op_sel:[0,1,0]
	v_pk_fma_f32 v[24:25], v[94:95], v[70:71], v[24:25] op_sel:[0,1,0]
	v_pk_fma_f32 v[26:27], v[96:97], v[70:71], v[26:27] op_sel:[0,1,0]
	v_pk_fma_f32 v[20:21], v[94:95], v[74:75], v[20:21] op_sel:[0,1,0]
	v_pk_fma_f32 v[22:23], v[96:97], v[74:75], v[22:23] op_sel:[0,1,0]
	v_pk_fma_f32 v[16:17], v[94:95], v[78:79], v[16:17] op_sel:[0,1,0]
	v_pk_fma_f32 v[18:19], v[96:97], v[78:79], v[18:19] op_sel:[0,1,0]
	v_pk_fma_f32 v[12:13], v[94:95], v[82:83], v[12:13] op_sel:[0,1,0]
	v_pk_fma_f32 v[14:15], v[96:97], v[82:83], v[14:15] op_sel:[0,1,0]
	v_pk_fma_f32 v[8:9], v[94:95], v[86:87], v[8:9] op_sel:[0,1,0]
	v_pk_fma_f32 v[10:11], v[96:97], v[86:87], v[10:11] op_sel:[0,1,0]
	v_pk_fma_f32 v[4:5], v[94:95], v[90:91], v[4:5] op_sel:[0,1,0]
	v_pk_fma_f32 v[6:7], v[96:97], v[90:91], v[6:7] op_sel:[0,1,0]
	v_pk_fma_f32 v[0:1], v[94:95], v[60:61], v[0:1] op_sel:[0,1,0]
	v_pk_fma_f32 v[2:3], v[96:97], v[60:61], v[2:3] op_sel:[0,1,0]
	s_waitcnt vmcnt(13)
; #define LAS __attribute__((address_space(3)))
; __device__ __forceinline__ void p0_prologue(Frame& F, const InPtrs& A) {
;     ...
;             const int layer = it / 24, cb = it % 24, col = cb * 256 + 4 * F.lane, kbase = F.wave * 128;
;             const float* W = A[I_ADAW] + (size_t)layer * 1024 * 6144 + col;
;             f32x4 acc[9];
; #pragma unroll
;             for (int r = 0; r < 9; ++r) acc[r] = (f32x4){0.f, 0.f, 0.f, 0.f};
; #pragma unroll 4
;             for (int k = 0; k < 128; ++k) { const f32x4 w = *(const f32x4*)(W + (size_t)(kbase + k) * 6144);
; #pragma unroll
;                 for (int r = 0; r < 9; ++r) acc[r] += w * sv[r * 1024 + kbase + k]; }
; #pragma unroll
;             for (int r = 0; r < 9; ++r) *(LAS f32x4*)(red + (F.wave * 9 + r) * 256 + 4 * F.lane) = acc[r];
	v_pk_fma_f32 v[34:35], v[100:101], v[58:59], v[34:35] op_sel_hi:[1,0,1]
	v_pk_fma_f32 v[32:33], v[98:99], v[58:59], v[32:33] op_sel_hi:[1,0,1]
	v_pk_fma_f32 v[30:31], v[100:101], v[68:69], v[30:31] op_sel_hi:[1,0,1]
	v_pk_fma_f32 v[28:29], v[98:99], v[68:69], v[28:29] op_sel_hi:[1,0,1]
	v_pk_fma_f32 v[26:27], v[100:101], v[72:73], v[26:27] op_sel_hi:[1,0,1]
	v_pk_fma_f32 v[24:25], v[98:99], v[72:73], v[24:25] op_sel_hi:[1,0,1]
	v_pk_fma_f32 v[22:23], v[100:101], v[76:77], v[22:23] op_sel_hi:[1,0,1]
	v_pk_fma_f32 v[20:21], v[98:99], v[76:77], v[20:21] op_sel_hi:[1,0,1]
	v_pk_fma_f32 v[18:19], v[100:101], v[80:81], v[18:19] op_sel_hi:[1,0,1]
	v_pk_fma_f32 v[16:17], v[98:99], v[80:81], v[16:17] op_sel_hi:[1,0,1]
	v_pk_fma_f32 v[14:15], v[100:101], v[84:85], v[14:15] op_sel_hi:[1,0,1]
	v_pk_fma_f32 v[12:13], v[98:99], v[84:85], v[12:13] op_sel_hi:[1,0,1]
	v_pk_fma_f32 v[10:11], v[100:101], v[88:89], v[10:11] op_sel_hi:[1,0,1]
	v_pk_fma_f32 v[8:9], v[98:99], v[88:89], v[8:9] op_sel_hi:[1,0,1]
	v_pk_fma_f32 v[6:7], v[100:101], v[92:93], v[6:7] op_sel_hi:[1,0,1]
	v_pk_fma_f32 v[4:5], v[98:99], v[92:93], v[4:5] op_sel_hi:[1,0,1]
	v_pk_fma_f32 v[2:3], v[100:101], v[62:63], v[2:3] op_sel_hi:[1,0,1]
	v_pk_fma_f32 v[0:1], v[98:99], v[62:63], v[0:1] op_sel_hi:[1,0,1]
	s_waitcnt vmcnt(12)
	v_pk_fma_f32 v[34:35], v[104:105], v[40:41], v[34:35] op_sel_hi:[1,0,1]
	v_pk_fma_f32 v[32:33], v[102:103], v[40:41], v[32:33] op_sel_hi:[1,0,1]
	v_pk_fma_f32 v[30:31], v[104:105], v[44:45], v[30:31] op_sel_hi:[1,0,1]
	v_pk_fma_f32 v[28:29], v[102:103], v[44:45], v[28:29] op_sel_hi:[1,0,1]
	v_pk_fma_f32 v[26:27], v[104:105], v[64:65], v[26:27] op_sel_hi:[1,0,1]
	v_pk_fma_f32 v[24:25], v[102:103], v[64:65], v[24:25] op_sel_hi:[1,0,1]
	v_pk_fma_f32 v[22:23], v[104:105], v[106:107], v[22:23] op_sel_hi:[1,0,1]
	v_pk_fma_f32 v[20:21], v[102:103], v[106:107], v[20:21] op_sel_hi:[1,0,1]
	v_pk_fma_f32 v[18:19], v[104:105], v[108:109], v[18:19] op_sel_hi:[1,0,1]
	v_pk_fma_f32 v[16:17], v[102:103], v[108:109], v[16:17] op_sel_hi:[1,0,1]
	v_pk_fma_f32 v[14:15], v[104:105], v[110:111], v[14:15] op_sel_hi:[1,0,1]
	v_pk_fma_f32 v[12:13], v[102:103], v[110:111], v[12:13] op_sel_hi:[1,0,1]
	v_pk_fma_f32 v[10:11], v[104:105], v[112:113], v[10:11] op_sel_hi:[1,0,1]
	v_pk_fma_f32 v[8:9], v[102:103], v[112:113], v[8:9] op_sel_hi:[1,0,1]
	v_pk_fma_f32 v[6:7], v[104:105], v[114:115], v[6:7] op_sel_hi:[1,0,1]
	v_pk_fma_f32 v[4:5], v[102:103], v[114:115], v[4:5] op_sel_hi:[1,0,1]
	v_pk_fma_f32 v[2:3], v[104:105], v[116:117], v[2:3] op_sel_hi:[1,0,1]
	v_pk_fma_f32 v[0:1], v[102:103], v[116:117], v[0:1] op_sel_hi:[1,0,1]
	v_mov_b32_e32 v40, s8
	ds_read_b128 v[56:59], v40
	ds_read_b128 v[60:63], v40 offset:32768
	ds_read_b128 v[66:69], v40 offset:4096
	ds_read_b128 v[70:73], v40 offset:8192
	ds_read_b128 v[74:77], v40 offset:12288
	ds_read_b128 v[78:81], v40 offset:16384
	ds_read_b128 v[82:85], v40 offset:20480
	ds_read_b128 v[86:89], v40 offset:24576
	ds_read_b128 v[90:93], v40 offset:28672
	s_add_i32 s8, s8, 16
	s_waitcnt lgkmcnt(8)
	v_mov_b32_e32 v40, v59
	s_waitcnt lgkmcnt(6)
	v_mov_b32_e32 v44, v69
	s_waitcnt lgkmcnt(5)
	v_mov_b32_e32 v64, v73
	s_waitcnt lgkmcnt(4)
	v_mov_b32_e32 v106, v77
	s_waitcnt lgkmcnt(3)
	v_mov_b32_e32 v108, v81
	s_waitcnt lgkmcnt(2)
	v_mov_b32_e32 v110, v85
	s_waitcnt lgkmcnt(1)
	v_mov_b32_e32 v112, v89
	s_waitcnt lgkmcnt(0)
	v_mov_b32_e32 v114, v93
	v_mov_b32_e32 v116, v63
	s_waitcnt vmcnt(11)
	v_pk_fma_f32 v[34:35], v[162:163], v[56:57], v[34:35] op_sel_hi:[1,0,1]
	v_pk_fma_f32 v[32:33], v[160:161], v[56:57], v[32:33] op_sel_hi:[1,0,1]
	v_pk_fma_f32 v[30:31], v[162:163], v[66:67], v[30:31] op_sel_hi:[1,0,1]
	v_pk_fma_f32 v[28:29], v[160:161], v[66:67], v[28:29] op_sel_hi:[1,0,1]
	v_pk_fma_f32 v[26:27], v[162:163], v[70:71], v[26:27] op_sel_hi:[1,0,1]
	v_pk_fma_f32 v[24:25], v[160:161], v[70:71], v[24:25] op_sel_hi:[1,0,1]
	v_pk_fma_f32 v[22:23], v[162:163], v[74:75], v[22:23] op_sel_hi:[1,0,1]
	v_pk_fma_f32 v[20:21], v[160:161], v[74:75], v[20:21] op_sel_hi:[1,0,1]
	v_pk_fma_f32 v[18:19], v[162:163], v[78:79], v[18:19] op_sel_hi:[1,0,1]
	v_pk_fma_f32 v[16:17], v[160:161], v[78:79], v[16:17] op_sel_hi:[1,0,1]
	v_pk_fma_f32 v[14:15], v[162:163], v[82:83], v[14:15] op_sel_hi:[1,0,1]
	v_pk_fma_f32 v[12:13], v[160:161], v[82:83], v[12:13] op_sel_hi:[1,0,1]
	v_pk_fma_f32 v[10:11], v[162:163], v[86:87], v[10:11] op_sel_hi:[1,0,1]
	v_pk_fma_f32 v[8:9], v[160:161], v[86:87], v[8:9] op_sel_hi:[1,0,1]
	v_pk_fma_f32 v[6:7], v[162:163], v[90:91], v[6:7] op_sel_hi:[1,0,1]
	v_pk_fma_f32 v[4:5], v[160:161], v[90:91], v[4:5] op_sel_hi:[1,0,1]
	v_pk_fma_f32 v[2:3], v[162:163], v[60:61], v[2:3] op_sel_hi:[1,0,1]
	v_pk_fma_f32 v[0:1], v[160:161], v[60:61], v[0:1] op_sel_hi:[1,0,1]
	s_waitcnt vmcnt(10)
	v_pk_fma_f32 v[32:33], v[164:165], v[56:57], v[32:33] op_sel:[0,1,0]
	v_pk_fma_f32 v[34:35], v[166:167], v[56:57], v[34:35] op_sel:[0,1,0]
	v_pk_fma_f32 v[28:29], v[164:165], v[66:67], v[28:29] op_sel:[0,1,0]
	v_pk_fma_f32 v[30:31], v[166:167], v[66:67], v[30:31] op_sel:[0,1,0]
	v_pk_fma_f32 v[24:25], v[164:165], v[70:71], v[24:25] op_sel:[0,1,0]
	v_pk_fma_f32 v[26:27], v[166:167], v[70:71], v[26:27] op_sel:[0,1,0]
	v_pk_fma_f32 v[20:21], v[164:165], v[74:75], v[20:21] op_sel:[0,1,0]
	v_pk_fma_f32 v[22:23], v[166:167], v[74:75], v[22:23] op_sel:[0,1,0]
	v_pk_fma_f32 v[16:17], v[164:165], v[78:79], v[16:17] op_sel:[0,1,0]
	v_pk_fma_f32 v[18:19], v[166:167], v[78:79], v[18:19] op_sel:[0,1,0]
	v_pk_fma_f32 v[12:13], v[164:165], v[82:83], v[12:13] op_sel:[0,1,0]
	v_pk_fma_f32 v[14:15], v[166:167], v[82:83], v[14:15] op_sel:[0,1,0]
	v_pk_fma_f32 v[8:9], v[164:165], v[86:87], v[8:9] op_sel:[0,1,0]
	v_pk_fma_f32 v[10:11], v[166:167], v[86:87], v[10:11] op_sel:[0,1,0]
	v_pk_fma_f32 v[4:5], v[164:165], v[90:91], v[4:5] op_sel:[0,1,0]
	v_pk_fma_f32 v[6:7], v[166:167], v[90:91], v[6:7] op_sel:[0,1,0]
	v_pk_fma_f32 v[0:1], v[164:165], v[60:61], v[0:1] op_sel:[0,1,0]
	v_pk_fma_f32 v[2:3], v[166:167], v[60:61], v[2:3] op_sel:[0,1,0]
	s_waitcnt vmcnt(9)
; __device__ __forceinline__ void p0_prologue(Frame& F, const InPtrs& A) {
;     ...
;             const int layer = it / 24, cb = it % 24, col = cb * 256 + 4 * F.lane, kbase = F.wave * 128;
;             const float* W = A[I_ADAW] + (size_t)layer * 1024 * 6144 + col;
;             f32x4 acc[9];
; #pragma unroll
;             for (int r = 0; r < 9; ++r) acc[r] = (f32x4){0.f, 0.f, 0.f, 0.f};
; #pragma unroll 4
;             for (int k = 0; k < 128; ++k) { const f32x4 w = *(const f32x4*)(W + (size_t)(kbase + k) * 6144);
; #pragma unroll
;                 for (int r = 0; r < 9; ++r) acc[r] += w * sv[r * 1024 + kbase + k]; }
	v_pk_fma_f32 v[34:35], v[170:171], v[58:59], v[34:35] op_sel_hi:[1,0,1]
	v_pk_fma_f32 v[32:33], v[168:169], v[58:59], v[32:33] op_sel_hi:[1,0,1]
	v_pk_fma_f32 v[30:31], v[170:171], v[68:69], v[30:31] op_sel_hi:[1,0,1]
	v_pk_fma_f32 v[28:29], v[168:169], v[68:69], v[28:29] op_sel_hi:[1,0,1]
	v_pk_fma_f32 v[26:27], v[170:171], v[72:73], v[26:27] op_sel_hi:[1,0,1]
	v_pk_fma_f32 v[24:25], v[168:169], v[72:73], v[24:25] op_sel_hi:[1,0,1]
	v_pk_fma_f32 v[22:23], v[170:171], v[76:77], v[22:23] op_sel_hi:[1,0,1]
	v_pk_fma_f32 v[20:21], v[168:169], v[76:77], v[20:21] op_sel_hi:[1,0,1]
	v_pk_fma_f32 v[18:19], v[170:171], v[80:81], v[18:19] op_sel_hi:[1,0,1]
	v_pk_fma_f32 v[16:17], v[168:169], v[80:81], v[16:17] op_sel_hi:[1,0,1]
	v_pk_fma_f32 v[14:15], v[170:171], v[84:85], v[14:15] op_sel_hi:[1,0,1]
	v_pk_fma_f32 v[12:13], v[168:169], v[84:85], v[12:13] op_sel_hi:[1,0,1]
	v_pk_fma_f32 v[10:11], v[170:171], v[88:89], v[10:11] op_sel_hi:[1,0,1]
	v_pk_fma_f32 v[8:9], v[168:169], v[88:89], v[8:9] op_sel_hi:[1,0,1]
	v_pk_fma_f32 v[6:7], v[170:171], v[92:93], v[6:7] op_sel_hi:[1,0,1]
	v_pk_fma_f32 v[4:5], v[168:169], v[92:93], v[4:5] op_sel_hi:[1,0,1]
	v_pk_fma_f32 v[2:3], v[170:171], v[62:63], v[2:3] op_sel_hi:[1,0,1]
	v_pk_fma_f32 v[0:1], v[168:169], v[62:63], v[0:1] op_sel_hi:[1,0,1]
	s_waitcnt vmcnt(8)
	v_pk_fma_f32 v[34:35], v[174:175], v[40:41], v[34:35] op_sel_hi:[1,0,1]
	v_pk_fma_f32 v[32:33], v[172:173], v[40:41], v[32:33] op_sel_hi:[1,0,1]
	v_pk_fma_f32 v[30:31], v[174:175], v[44:45], v[30:31] op_sel_hi:[1,0,1]
	v_pk_fma_f32 v[28:29], v[172:173], v[44:45], v[28:29] op_sel_hi:[1,0,1]
	v_pk_fma_f32 v[26:27], v[174:175], v[64:65], v[26:27] op_sel_hi:[1,0,1]
	v_pk_fma_f32 v[24:25], v[172:173], v[64:65], v[24:25] op_sel_hi:[1,0,1]
	v_pk_fma_f32 v[22:23], v[174:175], v[106:107], v[22:23] op_sel_hi:[1,0,1]
	v_pk_fma_f32 v[20:21], v[172:173], v[106:107], v[20:21] op_sel_hi:[1,0,1]
	v_pk_fma_f32 v[18:19], v[174:175], v[108:109], v[18:19] op_sel_hi:[1,0,1]
	v_pk_fma_f32 v[16:17], v[172:173], v[108:109], v[16:17] op_sel_hi:[1,0,1]
	v_pk_fma_f32 v[14:15], v[174:175], v[110:111], v[14:15] op_sel_hi:[1,0,1]
	v_pk_fma_f32 v[12:13], v[172:173], v[110:111], v[12:13] op_sel_hi:[1,0,1]
	v_pk_fma_f32 v[10:11], v[174:175], v[112:113], v[10:11] op_sel_hi:[1,0,1]
	v_pk_fma_f32 v[8:9], v[172:173], v[112:113], v[8:9] op_sel_hi:[1,0,1]
	v_pk_fma_f32 v[6:7], v[174:175], v[114:115], v[6:7] op_sel_hi:[1,0,1]
	v_pk_fma_f32 v[4:5], v[172:173], v[114:115], v[4:5] op_sel_hi:[1,0,1]
	v_pk_fma_f32 v[2:3], v[174:175], v[116:117], v[2:3] op_sel_hi:[1,0,1]
	v_pk_fma_f32 v[0:1], v[172:173], v[116:117], v[0:1] op_sel_hi:[1,0,1]
	v_mov_b32_e32 v40, s8
	ds_read_b128 v[56:59], v40
	ds_read_b128 v[60:63], v40 offset:32768
	ds_read_b128 v[66:69], v40 offset:4096
	ds_read_b128 v[70:73], v40 offset:8192
	ds_read_b128 v[74:77], v40 offset:12288
	ds_read_b128 v[78:81], v40 offset:16384
	ds_read_b128 v[82:85], v40 offset:20480
	ds_read_b128 v[86:89], v40 offset:24576
	ds_read_b128 v[90:93], v40 offset:28672
	s_add_i32 s8, s8, 16
	s_waitcnt lgkmcnt(8)
	v_mov_b32_e32 v40, v59
	s_waitcnt lgkmcnt(6)
	v_mov_b32_e32 v44, v69
	s_waitcnt lgkmcnt(5)
	v_mov_b32_e32 v64, v73
	s_waitcnt lgkmcnt(4)
	v_mov_b32_e32 v106, v77
	s_waitcnt lgkmcnt(3)
	v_mov_b32_e32 v108, v81
	s_waitcnt lgkmcnt(2)
	v_mov_b32_e32 v110, v85
	s_waitcnt lgkmcnt(1)
	v_mov_b32_e32 v112, v89
	s_waitcnt lgkmcnt(0)
	v_mov_b32_e32 v114, v93
	v_mov_b32_e32 v116, v63
	s_waitcnt vmcnt(7)
	v_pk_fma_f32 v[34:35], v[178:179], v[56:57], v[34:35] op_sel_hi:[1,0,1]
	v_pk_fma_f32 v[32:33], v[176:177], v[56:57], v[32:33] op_sel_hi:[1,0,1]
	v_pk_fma_f32 v[30:31], v[178:179], v[66:67], v[30:31] op_sel_hi:[1,0,1]
	v_pk_fma_f32 v[28:29], v[176:177], v[66:67], v[28:29] op_sel_hi:[1,0,1]
	v_pk_fma_f32 v[26:27], v[178:179], v[70:71], v[26:27] op_sel_hi:[1,0,1]
	v_pk_fma_f32 v[24:25], v[176:177], v[70:71], v[24:25] op_sel_hi:[1,0,1]
	v_pk_fma_f32 v[22:23], v[178:179], v[74:75], v[22:23] op_sel_hi:[1,0,1]
	v_pk_fma_f32 v[20:21], v[176:177], v[74:75], v[20:21] op_sel_hi:[1,0,1]
	v_pk_fma_f32 v[18:19], v[178:179], v[78:79], v[18:19] op_sel_hi:[1,0,1]
	v_pk_fma_f32 v[16:17], v[176:177], v[78:79], v[16:17] op_sel_hi:[1,0,1]
	v_pk_fma_f32 v[14:15], v[178:179], v[82:83], v[14:15] op_sel_hi:[1,0,1]
	v_pk_fma_f32 v[12:13], v[176:177], v[82:83], v[12:13] op_sel_hi:[1,0,1]
	v_pk_fma_f32 v[10:11], v[178:179], v[86:87], v[10:11] op_sel_hi:[1,0,1]
	v_pk_fma_f32 v[8:9], v[176:177], v[86:87], v[8:9] op_sel_hi:[1,0,1]
	v_pk_fma_f32 v[6:7], v[178:179], v[90:91], v[6:7] op_sel_hi:[1,0,1]
	v_pk_fma_f32 v[4:5], v[176:177], v[90:91], v[4:5] op_sel_hi:[1,0,1]
	v_pk_fma_f32 v[2:3], v[178:179], v[60:61], v[2:3] op_sel_hi:[1,0,1]
	v_pk_fma_f32 v[0:1], v[176:177], v[60:61], v[0:1] op_sel_hi:[1,0,1]
	s_waitcnt vmcnt(6)
	v_pk_fma_f32 v[32:33], v[180:181], v[56:57], v[32:33] op_sel:[0,1,0]
	v_pk_fma_f32 v[34:35], v[182:183], v[56:57], v[34:35] op_sel:[0,1,0]
	v_pk_fma_f32 v[28:29], v[180:181], v[66:67], v[28:29] op_sel:[0,1,0]
	v_pk_fma_f32 v[30:31], v[182:183], v[66:67], v[30:31] op_sel:[0,1,0]
	v_pk_fma_f32 v[24:25], v[180:181], v[70:71], v[24:25] op_sel:[0,1,0]
	v_pk_fma_f32 v[26:27], v[182:183], v[70:71], v[26:27] op_sel:[0,1,0]
	v_pk_fma_f32 v[20:21], v[180:181], v[74:75], v[20:21] op_sel:[0,1,0]
	v_pk_fma_f32 v[22:23], v[182:183], v[74:75], v[22:23] op_sel:[0,1,0]
	v_pk_fma_f32 v[16:17], v[180:181], v[78:79], v[16:17] op_sel:[0,1,0]
	v_pk_fma_f32 v[18:19], v[182:183], v[78:79], v[18:19] op_sel:[0,1,0]
	v_pk_fma_f32 v[12:13], v[180:181], v[82:83], v[12:13] op_sel:[0,1,0]
	v_pk_fma_f32 v[14:15], v[182:183], v[82:83], v[14:15] op_sel:[0,1,0]
	v_pk_fma_f32 v[8:9], v[180:181], v[86:87], v[8:9] op_sel:[0,1,0]
	v_pk_fma_f32 v[10:11], v[182:183], v[86:87], v[10:11] op_sel:[0,1,0]
	v_pk_fma_f32 v[4:5], v[180:181], v[90:91], v[4:5] op_sel:[0,1,0]
	v_pk_fma_f32 v[6:7], v[182:183], v[90:91], v[6:7] op_sel:[0,1,0]
	v_pk_fma_f32 v[0:1], v[180:181], v[60:61], v[0:1] op_sel:[0,1,0]
	v_pk_fma_f32 v[2:3], v[182:183], v[60:61], v[2:3] op_sel:[0,1,0]
	s_waitcnt vmcnt(5)
; __device__ __forceinline__ void p0_prologue(Frame& F, const InPtrs& A) {
;     ...
;             const int layer = it / 24, cb = it % 24, col = cb * 256 + 4 * F.lane, kbase = F.wave * 128;
;             const float* W = A[I_ADAW] + (size_t)layer * 1024 * 6144 + col;
;             f32x4 acc[9];
; #pragma unroll
;             for (int r = 0; r < 9; ++r) acc[r] = (f32x4){0.f, 0.f, 0.f, 0.f};
; #pragma unroll 4
;             for (int k = 0; k < 128; ++k) { const f32x4 w = *(const f32x4*)(W + (size_t)(kbase + k) * 6144);
; #pragma unroll
;                 for (int r = 0; r < 9; ++r) acc[r] += w * sv[r * 1024 + kbase + k]; }
	v_pk_fma_f32 v[34:35], v[186:187], v[58:59], v[34:35] op_sel_hi:[1,0,1]
	v_pk_fma_f32 v[32:33], v[184:185], v[58:59], v[32:33] op_sel_hi:[1,0,1]
	v_pk_fma_f32 v[30:31], v[186:187], v[68:69], v[30:31] op_sel_hi:[1,0,1]
	v_pk_fma_f32 v[28:29], v[184:185], v[68:69], v[28:29] op_sel_hi:[1,0,1]
	v_pk_fma_f32 v[26:27], v[186:187], v[72:73], v[26:27] op_sel_hi:[1,0,1]
	v_pk_fma_f32 v[24:25], v[184:185], v[72:73], v[24:25] op_sel_hi:[1,0,1]
	v_pk_fma_f32 v[22:23], v[186:187], v[76:77], v[22:23] op_sel_hi:[1,0,1]
	v_pk_fma_f32 v[20:21], v[184:185], v[76:77], v[20:21] op_sel_hi:[1,0,1]
	v_pk_fma_f32 v[18:19], v[186:187], v[80:81], v[18:19] op_sel_hi:[1,0,1]
	v_pk_fma_f32 v[16:17], v[184:185], v[80:81], v[16:17] op_sel_hi:[1,0,1]
	v_pk_fma_f32 v[14:15], v[186:187], v[84:85], v[14:15] op_sel_hi:[1,0,1]
	v_pk_fma_f32 v[12:13], v[184:185], v[84:85], v[12:13] op_sel_hi:[1,0,1]
	v_pk_fma_f32 v[10:11], v[186:187], v[88:89], v[10:11] op_sel_hi:[1,0,1]
	v_pk_fma_f32 v[8:9], v[184:185], v[88:89], v[8:9] op_sel_hi:[1,0,1]
	v_pk_fma_f32 v[6:7], v[186:187], v[92:93], v[6:7] op_sel_hi:[1,0,1]
	v_pk_fma_f32 v[4:5], v[184:185], v[92:93], v[4:5] op_sel_hi:[1,0,1]
	v_pk_fma_f32 v[2:3], v[186:187], v[62:63], v[2:3] op_sel_hi:[1,0,1]
	v_pk_fma_f32 v[0:1], v[184:185], v[62:63], v[0:1] op_sel_hi:[1,0,1]
	s_waitcnt vmcnt(4)
	v_pk_fma_f32 v[34:35], v[194:195], v[40:41], v[34:35] op_sel_hi:[1,0,1]
	v_pk_fma_f32 v[32:33], v[192:193], v[40:41], v[32:33] op_sel_hi:[1,0,1]
	v_pk_fma_f32 v[30:31], v[194:195], v[44:45], v[30:31] op_sel_hi:[1,0,1]
	v_pk_fma_f32 v[28:29], v[192:193], v[44:45], v[28:29] op_sel_hi:[1,0,1]
	v_pk_fma_f32 v[26:27], v[194:195], v[64:65], v[26:27] op_sel_hi:[1,0,1]
	v_pk_fma_f32 v[24:25], v[192:193], v[64:65], v[24:25] op_sel_hi:[1,0,1]
	v_pk_fma_f32 v[22:23], v[194:195], v[106:107], v[22:23] op_sel_hi:[1,0,1]
	v_pk_fma_f32 v[20:21], v[192:193], v[106:107], v[20:21] op_sel_hi:[1,0,1]
	v_pk_fma_f32 v[18:19], v[194:195], v[108:109], v[18:19] op_sel_hi:[1,0,1]
	v_pk_fma_f32 v[16:17], v[192:193], v[108:109], v[16:17] op_sel_hi:[1,0,1]
	v_pk_fma_f32 v[14:15], v[194:195], v[110:111], v[14:15] op_sel_hi:[1,0,1]
	v_pk_fma_f32 v[12:13], v[192:193], v[110:111], v[12:13] op_sel_hi:[1,0,1]
	v_pk_fma_f32 v[10:11], v[194:195], v[112:113], v[10:11] op_sel_hi:[1,0,1]
	v_pk_fma_f32 v[8:9], v[192:193], v[112:113], v[8:9] op_sel_hi:[1,0,1]
	v_pk_fma_f32 v[6:7], v[194:195], v[114:115], v[6:7] op_sel_hi:[1,0,1]
	v_pk_fma_f32 v[4:5], v[192:193], v[114:115], v[4:5] op_sel_hi:[1,0,1]
	v_pk_fma_f32 v[2:3], v[194:195], v[116:117], v[2:3] op_sel_hi:[1,0,1]
	v_pk_fma_f32 v[0:1], v[192:193], v[116:117], v[0:1] op_sel_hi:[1,0,1]
	v_mov_b32_e32 v40, s8
	ds_read_b128 v[56:59], v40
	ds_read_b128 v[60:63], v40 offset:32768
	ds_read_b128 v[66:69], v40 offset:4096
	ds_read_b128 v[70:73], v40 offset:8192
	ds_read_b128 v[74:77], v40 offset:12288
	ds_read_b128 v[78:81], v40 offset:16384
	ds_read_b128 v[82:85], v40 offset:20480
	ds_read_b128 v[86:89], v40 offset:24576
	ds_read_b128 v[90:93], v40 offset:28672
	s_add_i32 s8, s8, 16
	s_waitcnt lgkmcnt(8)
	v_mov_b32_e32 v40, v59
	s_waitcnt lgkmcnt(6)
	v_mov_b32_e32 v44, v69
	s_waitcnt lgkmcnt(5)
	v_mov_b32_e32 v64, v73
	s_waitcnt lgkmcnt(4)
	v_mov_b32_e32 v106, v77
	s_waitcnt lgkmcnt(3)
	v_mov_b32_e32 v108, v81
	s_waitcnt lgkmcnt(2)
	v_mov_b32_e32 v110, v85
	s_waitcnt lgkmcnt(1)
	v_mov_b32_e32 v112, v89
	s_waitcnt lgkmcnt(0)
	v_mov_b32_e32 v114, v93
	v_mov_b32_e32 v116, v63
	s_waitcnt vmcnt(3)
	v_pk_fma_f32 v[34:35], v[198:199], v[56:57], v[34:35] op_sel_hi:[1,0,1]
	v_pk_fma_f32 v[32:33], v[196:197], v[56:57], v[32:33] op_sel_hi:[1,0,1]
	v_pk_fma_f32 v[30:31], v[198:199], v[66:67], v[30:31] op_sel_hi:[1,0,1]
	v_pk_fma_f32 v[28:29], v[196:197], v[66:67], v[28:29] op_sel_hi:[1,0,1]
	v_pk_fma_f32 v[26:27], v[198:199], v[70:71], v[26:27] op_sel_hi:[1,0,1]
	v_pk_fma_f32 v[24:25], v[196:197], v[70:71], v[24:25] op_sel_hi:[1,0,1]
	v_pk_fma_f32 v[22:23], v[198:199], v[74:75], v[22:23] op_sel_hi:[1,0,1]
	v_pk_fma_f32 v[20:21], v[196:197], v[74:75], v[20:21] op_sel_hi:[1,0,1]
	v_pk_fma_f32 v[18:19], v[198:199], v[78:79], v[18:19] op_sel_hi:[1,0,1]
	v_pk_fma_f32 v[16:17], v[196:197], v[78:79], v[16:17] op_sel_hi:[1,0,1]
	v_pk_fma_f32 v[14:15], v[198:199], v[82:83], v[14:15] op_sel_hi:[1,0,1]
	v_pk_fma_f32 v[12:13], v[196:197], v[82:83], v[12:13] op_sel_hi:[1,0,1]
	v_pk_fma_f32 v[10:11], v[198:199], v[86:87], v[10:11] op_sel_hi:[1,0,1]
	v_pk_fma_f32 v[8:9], v[196:197], v[86:87], v[8:9] op_sel_hi:[1,0,1]
	v_pk_fma_f32 v[6:7], v[198:199], v[90:91], v[6:7] op_sel_hi:[1,0,1]
	v_pk_fma_f32 v[4:5], v[196:197], v[90:91], v[4:5] op_sel_hi:[1,0,1]
	v_pk_fma_f32 v[2:3], v[198:199], v[60:61], v[2:3] op_sel_hi:[1,0,1]
	v_pk_fma_f32 v[0:1], v[196:197], v[60:61], v[0:1] op_sel_hi:[1,0,1]
	s_waitcnt vmcnt(2)
; #define LAS __attribute__((address_space(3)))
; __device__ __forceinline__ void p0_prologue(Frame& F, const InPtrs& A) {
;     ...
;             for (int k = 0; k < 128; ++k) { const f32x4 w = *(const f32x4*)(W + (size_t)(kbase + k) * 6144);
; #pragma unroll
;                 for (int r = 0; r < 9; ++r) acc[r] += w * sv[r * 1024 + kbase + k]; }
; #pragma unroll
;             for (int r = 0; r < 9; ++r) *(LAS f32x4*)(red + (F.wave * 9 + r) * 256 + 4 * F.lane) = acc[r];
;             __syncthreads();
;             float* MODp = (float*)(F.ws + WS_MOD) + (size_t)layer * 9 * 6144;
;             for (int o = F.tid; o < 9 * 256; o += NTHREADS) { const int r = o >> 8, cc = o & 255; float s = 0.f;
; #pragma unroll
;                 for (int w = 0; w < 8; ++w) s += red[(w * 9 + r) * 256 + cc];
;                 MODp[r * 6144 + cb * 256 + cc] = s + A[I_ADAB][layer * 6144 + cb * 256 + cc]; }
	v_pk_fma_f32 v[32:33], v[200:201], v[56:57], v[32:33] op_sel:[0,1,0]
	v_pk_fma_f32 v[34:35], v[202:203], v[56:57], v[34:35] op_sel:[0,1,0]
	v_pk_fma_f32 v[28:29], v[200:201], v[66:67], v[28:29] op_sel:[0,1,0]
	v_pk_fma_f32 v[30:31], v[202:203], v[66:67], v[30:31] op_sel:[0,1,0]
	v_pk_fma_f32 v[24:25], v[200:201], v[70:71], v[24:25] op_sel:[0,1,0]
	v_pk_fma_f32 v[26:27], v[202:203], v[70:71], v[26:27] op_sel:[0,1,0]
	v_pk_fma_f32 v[20:21], v[200:201], v[74:75], v[20:21] op_sel:[0,1,0]
	v_pk_fma_f32 v[22:23], v[202:203], v[74:75], v[22:23] op_sel:[0,1,0]
	v_pk_fma_f32 v[16:17], v[200:201], v[78:79], v[16:17] op_sel:[0,1,0]
	v_pk_fma_f32 v[18:19], v[202:203], v[78:79], v[18:19] op_sel:[0,1,0]
	v_pk_fma_f32 v[12:13], v[200:201], v[82:83], v[12:13] op_sel:[0,1,0]
	v_pk_fma_f32 v[14:15], v[202:203], v[82:83], v[14:15] op_sel:[0,1,0]
	v_pk_fma_f32 v[8:9], v[200:201], v[86:87], v[8:9] op_sel:[0,1,0]
	v_pk_fma_f32 v[10:11], v[202:203], v[86:87], v[10:11] op_sel:[0,1,0]
	v_pk_fma_f32 v[4:5], v[200:201], v[90:91], v[4:5] op_sel:[0,1,0]
	v_pk_fma_f32 v[6:7], v[202:203], v[90:91], v[6:7] op_sel:[0,1,0]
	v_pk_fma_f32 v[0:1], v[200:201], v[60:61], v[0:1] op_sel:[0,1,0]
	v_pk_fma_f32 v[2:3], v[202:203], v[60:61], v[2:3] op_sel:[0,1,0]
	s_waitcnt vmcnt(1)
	v_pk_fma_f32 v[34:35], v[206:207], v[58:59], v[34:35] op_sel_hi:[1,0,1]
	v_pk_fma_f32 v[32:33], v[204:205], v[58:59], v[32:33] op_sel_hi:[1,0,1]
	v_pk_fma_f32 v[30:31], v[206:207], v[68:69], v[30:31] op_sel_hi:[1,0,1]
	v_pk_fma_f32 v[28:29], v[204:205], v[68:69], v[28:29] op_sel_hi:[1,0,1]
	v_pk_fma_f32 v[26:27], v[206:207], v[72:73], v[26:27] op_sel_hi:[1,0,1]
	v_pk_fma_f32 v[24:25], v[204:205], v[72:73], v[24:25] op_sel_hi:[1,0,1]
	v_pk_fma_f32 v[22:23], v[206:207], v[76:77], v[22:23] op_sel_hi:[1,0,1]
	v_pk_fma_f32 v[20:21], v[204:205], v[76:77], v[20:21] op_sel_hi:[1,0,1]
	v_pk_fma_f32 v[18:19], v[206:207], v[80:81], v[18:19] op_sel_hi:[1,0,1]
	v_pk_fma_f32 v[16:17], v[204:205], v[80:81], v[16:17] op_sel_hi:[1,0,1]
	v_pk_fma_f32 v[14:15], v[206:207], v[84:85], v[14:15] op_sel_hi:[1,0,1]
	v_pk_fma_f32 v[12:13], v[204:205], v[84:85], v[12:13] op_sel_hi:[1,0,1]
	v_pk_fma_f32 v[10:11], v[206:207], v[88:89], v[10:11] op_sel_hi:[1,0,1]
	v_pk_fma_f32 v[8:9], v[204:205], v[88:89], v[8:9] op_sel_hi:[1,0,1]
	v_pk_fma_f32 v[6:7], v[206:207], v[92:93], v[6:7] op_sel_hi:[1,0,1]
	v_pk_fma_f32 v[4:5], v[204:205], v[92:93], v[4:5] op_sel_hi:[1,0,1]
	v_pk_fma_f32 v[2:3], v[206:207], v[62:63], v[2:3] op_sel_hi:[1,0,1]
	v_pk_fma_f32 v[0:1], v[204:205], v[62:63], v[0:1] op_sel_hi:[1,0,1]
	s_waitcnt vmcnt(0)
	v_pk_fma_f32 v[34:35], v[210:211], v[40:41], v[34:35] op_sel_hi:[1,0,1]
	v_pk_fma_f32 v[32:33], v[208:209], v[40:41], v[32:33] op_sel_hi:[1,0,1]
	v_pk_fma_f32 v[30:31], v[210:211], v[44:45], v[30:31] op_sel_hi:[1,0,1]
	v_pk_fma_f32 v[28:29], v[208:209], v[44:45], v[28:29] op_sel_hi:[1,0,1]
	v_pk_fma_f32 v[26:27], v[210:211], v[64:65], v[26:27] op_sel_hi:[1,0,1]
	v_pk_fma_f32 v[24:25], v[208:209], v[64:65], v[24:25] op_sel_hi:[1,0,1]
	v_pk_fma_f32 v[22:23], v[210:211], v[106:107], v[22:23] op_sel_hi:[1,0,1]
	v_pk_fma_f32 v[20:21], v[208:209], v[106:107], v[20:21] op_sel_hi:[1,0,1]
	v_pk_fma_f32 v[18:19], v[210:211], v[108:109], v[18:19] op_sel_hi:[1,0,1]
	v_pk_fma_f32 v[16:17], v[208:209], v[108:109], v[16:17] op_sel_hi:[1,0,1]
	v_pk_fma_f32 v[14:15], v[210:211], v[110:111], v[14:15] op_sel_hi:[1,0,1]
	v_pk_fma_f32 v[12:13], v[208:209], v[110:111], v[12:13] op_sel_hi:[1,0,1]
	v_pk_fma_f32 v[10:11], v[210:211], v[112:113], v[10:11] op_sel_hi:[1,0,1]
	v_pk_fma_f32 v[8:9], v[208:209], v[112:113], v[8:9] op_sel_hi:[1,0,1]
	v_pk_fma_f32 v[6:7], v[210:211], v[114:115], v[6:7] op_sel_hi:[1,0,1]
	v_pk_fma_f32 v[4:5], v[208:209], v[114:115], v[4:5] op_sel_hi:[1,0,1]
	v_pk_fma_f32 v[2:3], v[210:211], v[116:117], v[2:3] op_sel_hi:[1,0,1]
	v_pk_fma_f32 v[0:1], v[208:209], v[116:117], v[0:1] op_sel_hi:[1,0,1]
	s_cmp_lg_u32 s6, 0x300000
	s_cbranch_scc1 .LBB0_22
	ds_write_b128 v51, v[32:35] offset:36864
	ds_write_b128 v51, v[28:31] offset:37888
	ds_write_b128 v51, v[24:27] offset:38912
	ds_write_b128 v51, v[20:23] offset:39936
	ds_write_b128 v51, v[16:19] offset:40960
	ds_write_b128 v51, v[12:15] offset:41984
	ds_write_b128 v51, v[8:11] offset:43008
	ds_write_b128 v51, v[4:7] offset:44032
	ds_write_b128 v51, v[0:3] offset:45056
	s_waitcnt lgkmcnt(0)
	s_barrier
	s_and_saveexec_b64 s[6:7], s[0:1]
	s_cbranch_execz .LBB0_11
	s_mul_i32 s8, s10, 0x36000
	s_mul_hi_i32 s9, s10, 0x36000
	s_add_u32 s8, s13, s8
	s_mul_i32 s10, s10, 24
	s_addc_u32 s9, s16, s9
	s_sub_i32 s10, s40, s10
	s_lshl_b32 s10, s10, 8
	s_add_i32 s11, s11, s10
	v_or_b32_e32 v0, s11, v47
	v_ashrrev_i32_e32 v1, 31, v0
	v_or_b32_e32 v2, s10, v47
	s_mov_b64 s[10:11], 0
	v_mov_b32_e32 v3, v36

; #define PG8_STAGE(bufoff, gbase, voff) do { _Pragma("unroll") for (int _i = 0; _i < 2; ++_i) \
;         __builtin_amdgcn_global_load_lds((const unsigned*)((const char*)(gbase) + (voff)[_i]), (PG8_LAS unsigned*)(lds + (bufoff) + ldsw + _i * 8192), 16, 0, 0); } while (0)
; #define PG8_LDA(dst, b, h) do { _Pragma("unroll") for (int m = 0; m < 4; ++m) _Pragma("unroll") for (int k = 0; k < 2; ++k) dst[m][k] = *(const PG8_LAS bf16x8*)(lds + PG8_SA(b, h) + aoff + m * 2048 + k * 1024); } while (0)
; #define PG8_LDB(dst, b, h) do { _Pragma("unroll") for (int n = 0; n < 2; ++n) _Pragma("unroll") for (int k = 0; k < 2; ++k) dst[n][k] = *(const PG8_LAS bf16x8*)(lds + PG8_SB(b, h) + boff + n * 2048 + k * 1024); } while (0)
; #define PG8_WAIT_V(n) asm volatile("s_waitcnt vmcnt(" #n ")" ::: "memory")
; #define PG8_WAIT_L(n) asm volatile("s_waitcnt lgkmcnt(" #n ")" ::: "memory")
; #define PG8_BAR __builtin_amdgcn_s_barrier()
; #define PG8_SCHED __builtin_amdgcn_sched_barrier(0)
; template <class Epi, class Sched, bool ALIGN_EPI = false, bool SP2 = false, bool GATHER = false>
; __device__ __forceinline__ void gemm_phase(PG8_LAS unsigned char* lds, const Gemm g, const Sched& S, const Epi& E, int tid_in, const int* rowsrc = nullptr, PG8_LAS int* idx_lds = nullptr) {
;     ...
;             PG8_LDB(B0, 0, 0); PG8_LDB(B1, 0, 1); PG8_SCHED; PG8_LDA(At, 0, 0); PG8_STAGE(PG8_SA(1, 1), a1 + hstepA, PG8_OA(1));
;             PG8_WAIT_V(8); PG8_WAIT_L(0); PG8_BAR; PG8_MMA(0, 0, At, B0); PG8_MMA(0, 1, At, B1); PG8_BAR; PG8_SCHED;
;             PG8_LDA(At, 0, 1); PG8_STAGE(PG8_SB(0, 0), b2, voffB); PG8_STAGE(PG8_SB(0, 1), b2 + hstep, voffB); PG8_STAGE(PG8_SA(0, 0), a2, PG8_OS(0));
;             PG8_WAIT_V(8); PG8_WAIT_L(0); PG8_BAR; PG8_MMA(1, 0, At, B0); PG8_MMA(1, 1, At, B1); PG8_BAR; PG8_SCHED;
;             PG8_LDB(B0, 1, 0); PG8_LDB(B1, 1, 1); PG8_SCHED; PG8_LDA(At, 1, 0); PG8_STAGE(PG8_SA(0, 1), a2 + hstepA, PG8_OS(1));
;             PG8_WAIT_V(8); PG8_WAIT_L(0); PG8_BAR; PG8_MMA(0, 0, At, B0); PG8_MMA(0, 1, At, B1); PG8_BAR; PG8_SCHED;
;             PG8_LDA(At, 1, 1); PG8_STAGE(PG8_SB(1, 0), b3, voffB); PG8_STAGE(PG8_SB(1, 1), b3 + hstep, voffB); PG8_STAGE(PG8_SA(1, 0), a3, PG8_OS(0));
;             PG8_WAIT_V(8); PG8_WAIT_L(0); PG8_BAR; PG8_MMA(1, 0, At, B0); PG8_MMA(1, 1, At, B1); PG8_BAR; PG8_SCHED;
.LBB0_390:
	s_add_u32 s20, s18, 0xfffc0080
	s_addc_u32 s21, s19, -1
	s_add_i32 s52, 0, 0x10000
	s_cmp_eq_u32 s51, 12
	s_cselect_b32 s23, s13, s21
	s_cselect_b32 s22, s47, s20
	v_add_u32_e32 v144, s52, v149
	s_cselect_b32 s21, s9, s50
	s_cselect_b32 s20, s48, s49
	s_add_i32 s54, 0, 0x14000
	ds_read_b128 v[140:143], v144
	ds_read_b128 v[152:155], v144 offset:1024
	ds_read_b128 v[156:159], v144 offset:2048
	ds_read_b128 v[160:163], v144 offset:3072
	v_add_u32_e32 v144, s54, v149
	ds_read_b128 v[164:167], v144
	ds_read_b128 v[168:171], v144 offset:1024
	ds_read_b128 v[172:175], v144 offset:2048
	ds_read_b128 v[176:179], v144 offset:3072
	v_lshl_add_u64 v[144:145], s[18:19], 0, v[136:137]
	s_add_i32 m0, s29, 0xc000
	ds_read_b128 v[180:183], v151
	ds_read_b128 v[184:187], v151 offset:1024
	ds_read_b128 v[188:191], v151 offset:2048
	ds_read_b128 v[192:195], v151 offset:3072
	ds_read_b128 v[196:199], v151 offset:4096
	ds_read_b128 v[200:203], v151 offset:5120
	ds_read_b128 v[204:207], v151 offset:6144
	ds_read_b128 v[208:211], v151 offset:7168
	global_load_lds_dwordx4 v[144:145], off
	v_lshl_add_u64 v[144:145], s[18:19], 0, v[138:139]
	s_add_i32 m0, s29, 0xe000
	s_nop 0
	global_load_lds_dwordx4 v[144:145], off
	s_waitcnt vmcnt(8)
	s_waitcnt lgkmcnt(0)
	v_mfma_f32_16x16x32_bf16 v[126:129], v[140:143], v[180:183], v[126:129]
	v_mfma_f32_16x16x32_bf16 v[122:125], v[156:159], v[180:183], v[122:125]
	v_mfma_f32_16x16x32_bf16 v[110:113], v[140:143], v[188:191], v[110:113]
	s_barrier
	s_setprio 1
	s_waitcnt lgkmcnt(0)
	v_mfma_f32_16x16x32_bf16 v[106:109], v[156:159], v[188:191], v[106:109]
	v_mfma_f32_16x16x32_bf16 v[94:97], v[140:143], v[196:199], v[94:97]
	v_mfma_f32_16x16x32_bf16 v[90:93], v[156:159], v[196:199], v[90:93]
	v_mfma_f32_16x16x32_bf16 v[78:81], v[140:143], v[204:207], v[78:81]
	v_mfma_f32_16x16x32_bf16 v[74:77], v[156:159], v[204:207], v[74:77]
	v_mfma_f32_16x16x32_bf16 v[126:129], v[152:155], v[184:187], v[126:129]
	v_mfma_f32_16x16x32_bf16 v[122:125], v[160:163], v[184:187], v[122:125]
	v_mfma_f32_16x16x32_bf16 v[110:113], v[152:155], v[192:195], v[110:113]
	v_mfma_f32_16x16x32_bf16 v[106:109], v[160:163], v[192:195], v[106:109]
	v_mfma_f32_16x16x32_bf16 v[94:97], v[152:155], v[200:203], v[94:97]
	v_mfma_f32_16x16x32_bf16 v[90:93], v[160:163], v[200:203], v[90:93]
	v_mfma_f32_16x16x32_bf16 v[78:81], v[152:155], v[208:211], v[78:81]
	v_mfma_f32_16x16x32_bf16 v[74:77], v[160:163], v[208:211], v[74:77]
	s_setprio 0
	s_setprio 1
	v_mfma_f32_16x16x32_bf16 v[118:121], v[164:167], v[180:183], v[118:121]
	v_mfma_f32_16x16x32_bf16 v[114:117], v[172:175], v[180:183], v[114:117]
	v_mfma_f32_16x16x32_bf16 v[102:105], v[164:167], v[188:191], v[102:105]
	v_mfma_f32_16x16x32_bf16 v[98:101], v[172:175], v[188:191], v[98:101]
	v_mfma_f32_16x16x32_bf16 v[86:89], v[164:167], v[196:199], v[86:89]
	v_mfma_f32_16x16x32_bf16 v[82:85], v[172:175], v[196:199], v[82:85]
	v_mfma_f32_16x16x32_bf16 v[70:73], v[164:167], v[204:207], v[70:73]
	v_mfma_f32_16x16x32_bf16 v[66:69], v[172:175], v[204:207], v[66:69]
	v_mfma_f32_16x16x32_bf16 v[118:121], v[168:171], v[184:187], v[118:121]
	v_mfma_f32_16x16x32_bf16 v[114:117], v[176:179], v[184:187], v[114:117]
	v_mfma_f32_16x16x32_bf16 v[102:105], v[168:171], v[192:195], v[102:105]
	v_mfma_f32_16x16x32_bf16 v[98:101], v[176:179], v[192:195], v[98:101]
	v_mfma_f32_16x16x32_bf16 v[86:89], v[168:171], v[200:203], v[86:89]
	v_mfma_f32_16x16x32_bf16 v[82:85], v[176:179], v[200:203], v[82:85]
	v_mfma_f32_16x16x32_bf16 v[70:73], v[168:171], v[208:211], v[70:73]
	v_mfma_f32_16x16x32_bf16 v[66:69], v[176:179], v[208:211], v[66:69]
	s_setprio 0
	s_barrier
	s_add_i32 s52, s52, s28
	v_lshl_add_u64 v[144:145], s[20:21], 0, v[0:1]
	s_mov_b32 m0, s52
	ds_read_b128 v[180:183], v151 offset:16384
	ds_read_b128 v[184:187], v151 offset:17408
	ds_read_b128 v[188:191], v151 offset:18432
	ds_read_b128 v[192:195], v151 offset:19456
	ds_read_b128 v[196:199], v151 offset:20480
	ds_read_b128 v[200:203], v151 offset:21504
	ds_read_b128 v[204:207], v151 offset:22528
	ds_read_b128 v[208:211], v151 offset:23552
	global_load_lds_dwordx4 v[144:145], off
	s_add_i32 m0, s52, 0x2000
	s_add_u32 s52, s20, 0x40000
	v_lshl_add_u64 v[212:213], s[20:21], 0, v[130:131]
	s_addc_u32 s53, s21, 0
	s_add_i32 s54, s54, s28
	global_load_lds_dwordx4 v[212:213], off
	v_lshl_add_u64 v[214:215], s[52:53], 0, v[0:1]
	s_mov_b32 m0, s54
	v_lshl_add_u64 v[216:217], s[22:23], 0, v[132:133]
	global_load_lds_dwordx4 v[214:215], off
	v_lshl_add_u64 v[214:215], s[52:53], 0, v[130:131]
	s_add_i32 m0, s54, 0x2000
	s_nop 0
	global_load_lds_dwordx4 v[214:215], off
	v_lshl_add_u64 v[214:215], s[22:23], 0, v[134:135]
	s_mov_b32 m0, s29
	s_nop 0
	global_load_lds_dwordx4 v[214:215], off
	s_mov_b32 m0, s30
	s_nop 0
	global_load_lds_dwordx4 v[216:217], off
	s_waitcnt vmcnt(8)
	s_waitcnt lgkmcnt(0)
	v_mfma_f32_16x16x32_bf16 v[62:65], v[140:143], v[180:183], v[62:65]
	v_mfma_f32_16x16x32_bf16 v[58:61], v[156:159], v[180:183], v[58:61]
	v_mfma_f32_16x16x32_bf16 v[46:49], v[140:143], v[188:191], v[46:49]
	s_barrier
; #define PG8_STAGE(bufoff, gbase, voff) do { _Pragma("unroll") for (int _i = 0; _i < 2; ++_i) \
;         __builtin_amdgcn_global_load_lds((const unsigned*)((const char*)(gbase) + (voff)[_i]), (PG8_LAS unsigned*)(lds + (bufoff) + ldsw + _i * 8192), 16, 0, 0); } while (0)
; #define PG8_LDA(dst, b, h) do { _Pragma("unroll") for (int m = 0; m < 4; ++m) _Pragma("unroll") for (int k = 0; k < 2; ++k) dst[m][k] = *(const PG8_LAS bf16x8*)(lds + PG8_SA(b, h) + aoff + m * 2048 + k * 1024); } while (0)
; #define PG8_LDB(dst, b, h) do { _Pragma("unroll") for (int n = 0; n < 2; ++n) _Pragma("unroll") for (int k = 0; k < 2; ++k) dst[n][k] = *(const PG8_LAS bf16x8*)(lds + PG8_SB(b, h) + boff + n * 2048 + k * 1024); } while (0)
; #define PG8_WAIT_V(n) asm volatile("s_waitcnt vmcnt(" #n ")" ::: "memory")
; #define PG8_WAIT_L(n) asm volatile("s_waitcnt lgkmcnt(" #n ")" ::: "memory")
; #define PG8_BAR __builtin_amdgcn_s_barrier()
; #define PG8_SCHED __builtin_amdgcn_sched_barrier(0)
; template <class Epi, class Sched, bool ALIGN_EPI = false, bool SP2 = false, bool GATHER = false>
; __device__ __forceinline__ void gemm_phase(PG8_LAS unsigned char* lds, const Gemm g, const Sched& S, const Epi& E, int tid_in, const int* rowsrc = nullptr, PG8_LAS int* idx_lds = nullptr) {
;     ...
;             PG8_LDB(B0, 0, 0); PG8_LDB(B1, 0, 1); PG8_SCHED; PG8_LDA(At, 0, 0); PG8_STAGE(PG8_SA(1, 1), a1 + hstepA, PG8_OA(1));
;             PG8_WAIT_V(8); PG8_WAIT_L(0); PG8_BAR; PG8_MMA(0, 0, At, B0); PG8_MMA(0, 1, At, B1); PG8_BAR; PG8_SCHED;
;             PG8_LDA(At, 0, 1); PG8_STAGE(PG8_SB(0, 0), b2, voffB); PG8_STAGE(PG8_SB(0, 1), b2 + hstep, voffB); PG8_STAGE(PG8_SA(0, 0), a2, PG8_OS(0));
;             PG8_WAIT_V(8); PG8_WAIT_L(0); PG8_BAR; PG8_MMA(1, 0, At, B0); PG8_MMA(1, 1, At, B1); PG8_BAR; PG8_SCHED;
;             PG8_LDB(B0, 1, 0); PG8_LDB(B1, 1, 1); PG8_SCHED; PG8_LDA(At, 1, 0); PG8_STAGE(PG8_SA(0, 1), a2 + hstepA, PG8_OS(1));
;             PG8_WAIT_V(8); PG8_WAIT_L(0); PG8_BAR; PG8_MMA(0, 0, At, B0); PG8_MMA(0, 1, At, B1); PG8_BAR; PG8_SCHED;
;             PG8_LDA(At, 1, 1); PG8_STAGE(PG8_SB(1, 0), b3, voffB); PG8_STAGE(PG8_SB(1, 1), b3 + hstep, voffB); PG8_STAGE(PG8_SA(1, 0), a3, PG8_OS(0));
;             PG8_WAIT_V(8); PG8_WAIT_L(0); PG8_BAR; PG8_MMA(1, 0, At, B0); PG8_MMA(1, 1, At, B1); PG8_BAR; PG8_SCHED;
	s_setprio 1
	s_waitcnt lgkmcnt(0)
	v_mfma_f32_16x16x32_bf16 v[42:45], v[156:159], v[188:191], v[42:45]
	v_mfma_f32_16x16x32_bf16 v[30:33], v[140:143], v[196:199], v[30:33]
	v_mfma_f32_16x16x32_bf16 v[26:29], v[156:159], v[196:199], v[26:29]
	v_mfma_f32_16x16x32_bf16 v[14:17], v[140:143], v[204:207], v[14:17]
	v_mfma_f32_16x16x32_bf16 v[10:13], v[156:159], v[204:207], v[10:13]
	v_mfma_f32_16x16x32_bf16 v[62:65], v[152:155], v[184:187], v[62:65]
	v_mfma_f32_16x16x32_bf16 v[58:61], v[160:163], v[184:187], v[58:61]
	v_mfma_f32_16x16x32_bf16 v[46:49], v[152:155], v[192:195], v[46:49]
	v_mfma_f32_16x16x32_bf16 v[42:45], v[160:163], v[192:195], v[42:45]
	v_mfma_f32_16x16x32_bf16 v[30:33], v[152:155], v[200:203], v[30:33]
	v_mfma_f32_16x16x32_bf16 v[26:29], v[160:163], v[200:203], v[26:29]
	v_mfma_f32_16x16x32_bf16 v[14:17], v[152:155], v[208:211], v[14:17]
	v_mfma_f32_16x16x32_bf16 v[10:13], v[160:163], v[208:211], v[10:13]
	s_setprio 0
	s_setprio 1
	v_mfma_f32_16x16x32_bf16 v[54:57], v[164:167], v[180:183], v[54:57]
	v_mfma_f32_16x16x32_bf16 v[50:53], v[172:175], v[180:183], v[50:53]
	v_mfma_f32_16x16x32_bf16 v[38:41], v[164:167], v[188:191], v[38:41]
	v_mfma_f32_16x16x32_bf16 v[34:37], v[172:175], v[188:191], v[34:37]
	v_mfma_f32_16x16x32_bf16 v[22:25], v[164:167], v[196:199], v[22:25]
	v_mfma_f32_16x16x32_bf16 v[18:21], v[172:175], v[196:199], v[18:21]
	v_mfma_f32_16x16x32_bf16 v[6:9], v[164:167], v[204:207], v[6:9]
	v_mfma_f32_16x16x32_bf16 v[2:5], v[172:175], v[204:207], v[2:5]
	v_mfma_f32_16x16x32_bf16 v[54:57], v[168:171], v[184:187], v[54:57]
	v_mfma_f32_16x16x32_bf16 v[50:53], v[176:179], v[184:187], v[50:53]
	v_mfma_f32_16x16x32_bf16 v[38:41], v[168:171], v[192:195], v[38:41]
	v_mfma_f32_16x16x32_bf16 v[34:37], v[176:179], v[192:195], v[34:37]
	v_mfma_f32_16x16x32_bf16 v[22:25], v[168:171], v[200:203], v[22:25]
	v_mfma_f32_16x16x32_bf16 v[18:21], v[176:179], v[200:203], v[18:21]
	v_mfma_f32_16x16x32_bf16 v[6:9], v[168:171], v[208:211], v[6:9]
	v_mfma_f32_16x16x32_bf16 v[2:5], v[176:179], v[208:211], v[2:5]
	s_setprio 0
	s_barrier
	s_add_i32 s52, 0, 0x18000
	s_add_i32 s53, 0, 0x1c000
	v_add_u32_e32 v160, s52, v149
	v_add_u32_e32 v176, s53, v149
	ds_read_b128 v[140:143], v160
	ds_read_b128 v[152:155], v160 offset:1024
	ds_read_b128 v[156:159], v160 offset:2048
	ds_read_b128 v[160:163], v160 offset:3072
	ds_read_b128 v[164:167], v176
	ds_read_b128 v[168:171], v176 offset:1024
	ds_read_b128 v[172:175], v176 offset:2048
	ds_read_b128 v[176:179], v176 offset:3072
	s_add_u32 s22, s22, 0x40000
	s_addc_u32 s23, s23, 0
	s_mov_b32 m0, s31
	v_lshl_add_u64 v[218:219], s[22:23], 0, v[134:135]
	ds_read_b128 v[180:183], v151 offset:32768
	ds_read_b128 v[184:187], v151 offset:33792
	ds_read_b128 v[188:191], v151 offset:34816
	ds_read_b128 v[192:195], v151 offset:35840
	ds_read_b128 v[196:199], v151 offset:36864
	ds_read_b128 v[200:203], v151 offset:37888
	ds_read_b128 v[204:207], v151 offset:38912
	ds_read_b128 v[208:211], v151 offset:39936
	global_load_lds_dwordx4 v[218:219], off
	v_lshl_add_u64 v[218:219], s[22:23], 0, v[132:133]
	s_mov_b32 m0, s36
	s_nop 0
	global_load_lds_dwordx4 v[218:219], off
	s_waitcnt vmcnt(8)
	s_waitcnt lgkmcnt(0)
	v_mfma_f32_16x16x32_bf16 v[126:129], v[140:143], v[180:183], v[126:129]
	v_mfma_f32_16x16x32_bf16 v[122:125], v[156:159], v[180:183], v[122:125]
	v_mfma_f32_16x16x32_bf16 v[110:113], v[140:143], v[188:191], v[110:113]
	s_barrier
	s_setprio 1
	s_waitcnt lgkmcnt(0)
	v_mfma_f32_16x16x32_bf16 v[106:109], v[156:159], v[188:191], v[106:109]
	v_mfma_f32_16x16x32_bf16 v[94:97], v[140:143], v[196:199], v[94:97]
	v_mfma_f32_16x16x32_bf16 v[90:93], v[156:159], v[196:199], v[90:93]
	v_mfma_f32_16x16x32_bf16 v[78:81], v[140:143], v[204:207], v[78:81]
	v_mfma_f32_16x16x32_bf16 v[74:77], v[156:159], v[204:207], v[74:77]
	v_mfma_f32_16x16x32_bf16 v[126:129], v[152:155], v[184:187], v[126:129]
	v_mfma_f32_16x16x32_bf16 v[122:125], v[160:163], v[184:187], v[122:125]
	v_mfma_f32_16x16x32_bf16 v[110:113], v[152:155], v[192:195], v[110:113]
	v_mfma_f32_16x16x32_bf16 v[106:109], v[160:163], v[192:195], v[106:109]
	v_mfma_f32_16x16x32_bf16 v[94:97], v[152:155], v[200:203], v[94:97]
	v_mfma_f32_16x16x32_bf16 v[90:93], v[160:163], v[200:203], v[90:93]
	v_mfma_f32_16x16x32_bf16 v[78:81], v[152:155], v[208:211], v[78:81]
	v_mfma_f32_16x16x32_bf16 v[74:77], v[160:163], v[208:211], v[74:77]
	s_setprio 0
	s_setprio 1
	v_mfma_f32_16x16x32_bf16 v[118:121], v[164:167], v[180:183], v[118:121]
	v_mfma_f32_16x16x32_bf16 v[114:117], v[172:175], v[180:183], v[114:117]
	v_mfma_f32_16x16x32_bf16 v[102:105], v[164:167], v[188:191], v[102:105]
	v_mfma_f32_16x16x32_bf16 v[98:101], v[172:175], v[188:191], v[98:101]
	v_mfma_f32_16x16x32_bf16 v[86:89], v[164:167], v[196:199], v[86:89]
	v_mfma_f32_16x16x32_bf16 v[82:85], v[172:175], v[196:199], v[82:85]
	v_mfma_f32_16x16x32_bf16 v[70:73], v[164:167], v[204:207], v[70:73]
	v_mfma_f32_16x16x32_bf16 v[66:69], v[172:175], v[204:207], v[66:69]
	v_mfma_f32_16x16x32_bf16 v[118:121], v[168:171], v[184:187], v[118:121]
	v_mfma_f32_16x16x32_bf16 v[114:117], v[176:179], v[184:187], v[114:117]
	v_mfma_f32_16x16x32_bf16 v[102:105], v[168:171], v[192:195], v[102:105]
	v_mfma_f32_16x16x32_bf16 v[98:101], v[176:179], v[192:195], v[98:101]
	v_mfma_f32_16x16x32_bf16 v[86:89], v[168:171], v[200:203], v[86:89]
	v_mfma_f32_16x16x32_bf16 v[82:85], v[176:179], v[200:203], v[82:85]
	v_mfma_f32_16x16x32_bf16 v[70:73], v[168:171], v[208:211], v[70:73]
	v_mfma_f32_16x16x32_bf16 v[66:69], v[176:179], v[208:211], v[66:69]
	s_setprio 0
	s_barrier
; #define PG8_STAGE(bufoff, gbase, voff) do { _Pragma("unroll") for (int _i = 0; _i < 2; ++_i) \
;         __builtin_amdgcn_global_load_lds((const unsigned*)((const char*)(gbase) + (voff)[_i]), (PG8_LAS unsigned*)(lds + (bufoff) + ldsw + _i * 8192), 16, 0, 0); } while (0)
; #define PG8_LDA(dst, b, h) do { _Pragma("unroll") for (int m = 0; m < 4; ++m) _Pragma("unroll") for (int k = 0; k < 2; ++k) dst[m][k] = *(const PG8_LAS bf16x8*)(lds + PG8_SA(b, h) + aoff + m * 2048 + k * 1024); } while (0)
; #define PG8_LDB(dst, b, h) do { _Pragma("unroll") for (int n = 0; n < 2; ++n) _Pragma("unroll") for (int k = 0; k < 2; ++k) dst[n][k] = *(const PG8_LAS bf16x8*)(lds + PG8_SB(b, h) + boff + n * 2048 + k * 1024); } while (0)
; #define PG8_WAIT_V(n) asm volatile("s_waitcnt vmcnt(" #n ")" ::: "memory")
; #define PG8_WAIT_L(n) asm volatile("s_waitcnt lgkmcnt(" #n ")" ::: "memory")
; #define PG8_BAR __builtin_amdgcn_s_barrier()
; #define PG8_SCHED __builtin_amdgcn_sched_barrier(0)
; template <class Epi, class Sched, bool ALIGN_EPI = false, bool SP2 = false, bool GATHER = false>
; __device__ __forceinline__ void gemm_phase(PG8_LAS unsigned char* lds, const Gemm g, const Sched& S, const Epi& E, int tid_in, const int* rowsrc = nullptr, PG8_LAS int* idx_lds = nullptr) {
;     ...
;             PG8_LDB(B0, 0, 0); PG8_LDB(B1, 0, 1); PG8_SCHED; PG8_LDA(At, 0, 0); PG8_STAGE(PG8_SA(1, 1), a1 + hstepA, PG8_OA(1));
;             PG8_WAIT_V(8); PG8_WAIT_L(0); PG8_BAR; PG8_MMA(0, 0, At, B0); PG8_MMA(0, 1, At, B1); PG8_BAR; PG8_SCHED;
;             PG8_LDA(At, 0, 1); PG8_STAGE(PG8_SB(0, 0), b2, voffB); PG8_STAGE(PG8_SB(0, 1), b2 + hstep, voffB); PG8_STAGE(PG8_SA(0, 0), a2, PG8_OS(0));
;             PG8_WAIT_V(8); PG8_WAIT_L(0); PG8_BAR; PG8_MMA(1, 0, At, B0); PG8_MMA(1, 1, At, B1); PG8_BAR; PG8_SCHED;
;             PG8_LDB(B0, 1, 0); PG8_LDB(B1, 1, 1); PG8_SCHED; PG8_LDA(At, 1, 0); PG8_STAGE(PG8_SA(0, 1), a2 + hstepA, PG8_OS(1));
;             PG8_WAIT_V(8); PG8_WAIT_L(0); PG8_BAR; PG8_MMA(0, 0, At, B0); PG8_MMA(0, 1, At, B1); PG8_BAR; PG8_SCHED;
;             PG8_LDA(At, 1, 1); PG8_STAGE(PG8_SB(1, 0), b3, voffB); PG8_STAGE(PG8_SB(1, 1), b3 + hstep, voffB); PG8_STAGE(PG8_SA(1, 0), a3, PG8_OS(0));
;             PG8_WAIT_V(8); PG8_WAIT_L(0); PG8_BAR; PG8_MMA(1, 0, At, B0); PG8_MMA(1, 1, At, B1); PG8_BAR; PG8_SCHED;
	s_add_i32 s22, s52, s28
	v_lshl_add_u64 v[144:145], v[144:145], 0, s[10:11]
	s_mov_b32 m0, s22
	ds_read_b128 v[180:183], v151 offset:49152
	ds_read_b128 v[184:187], v151 offset:50176
	ds_read_b128 v[188:191], v151 offset:51200
	ds_read_b128 v[192:195], v151 offset:52224
	ds_read_b128 v[196:199], v151 offset:53248
	ds_read_b128 v[200:203], v151 offset:54272
	ds_read_b128 v[204:207], v151 offset:55296
	ds_read_b128 v[208:211], v151 offset:56320
	global_load_lds_dwordx4 v[144:145], off
	s_add_i32 m0, s22, 0x2000
	s_add_u32 s20, s20, 0x40080
	v_lshl_add_u64 v[144:145], v[212:213], 0, s[10:11]
	s_addc_u32 s21, s21, 0
	s_add_i32 s22, s53, s28
	global_load_lds_dwordx4 v[144:145], off
	v_lshl_add_u64 v[144:145], s[20:21], 0, v[0:1]
	s_mov_b32 m0, s22
	s_nop 0
	global_load_lds_dwordx4 v[144:145], off
	v_lshl_add_u64 v[144:145], s[20:21], 0, v[130:131]
	s_add_i32 m0, s22, 0x2000
	s_nop 0
	global_load_lds_dwordx4 v[144:145], off
	v_lshl_add_u64 v[144:145], v[214:215], 0, s[10:11]
	s_mov_b32 m0, s38
	s_nop 0
	global_load_lds_dwordx4 v[144:145], off
	v_lshl_add_u64 v[144:145], v[216:217], 0, s[10:11]
	s_mov_b32 m0, s39
	s_nop 0
	global_load_lds_dwordx4 v[144:145], off
	s_waitcnt vmcnt(8)
	s_waitcnt lgkmcnt(0)
	v_mfma_f32_16x16x32_bf16 v[62:65], v[140:143], v[180:183], v[62:65]
	v_mfma_f32_16x16x32_bf16 v[58:61], v[156:159], v[180:183], v[58:61]
	v_mfma_f32_16x16x32_bf16 v[46:49], v[140:143], v[188:191], v[46:49]
	s_barrier
	s_setprio 1
	s_waitcnt lgkmcnt(0)
	v_mfma_f32_16x16x32_bf16 v[42:45], v[156:159], v[188:191], v[42:45]
	v_mfma_f32_16x16x32_bf16 v[30:33], v[140:143], v[196:199], v[30:33]
	v_mfma_f32_16x16x32_bf16 v[26:29], v[156:159], v[196:199], v[26:29]
	v_mfma_f32_16x16x32_bf16 v[14:17], v[140:143], v[204:207], v[14:17]
	v_mfma_f32_16x16x32_bf16 v[10:13], v[156:159], v[204:207], v[10:13]
	v_mfma_f32_16x16x32_bf16 v[62:65], v[152:155], v[184:187], v[62:65]
	v_mfma_f32_16x16x32_bf16 v[58:61], v[160:163], v[184:187], v[58:61]
	v_mfma_f32_16x16x32_bf16 v[46:49], v[152:155], v[192:195], v[46:49]
	v_mfma_f32_16x16x32_bf16 v[42:45], v[160:163], v[192:195], v[42:45]
	v_mfma_f32_16x16x32_bf16 v[30:33], v[152:155], v[200:203], v[30:33]
	v_mfma_f32_16x16x32_bf16 v[26:29], v[160:163], v[200:203], v[26:29]
	v_mfma_f32_16x16x32_bf16 v[14:17], v[152:155], v[208:211], v[14:17]
	v_mfma_f32_16x16x32_bf16 v[10:13], v[160:163], v[208:211], v[10:13]
	s_setprio 0
	s_setprio 1
	v_mfma_f32_16x16x32_bf16 v[54:57], v[164:167], v[180:183], v[54:57]
	v_mfma_f32_16x16x32_bf16 v[50:53], v[172:175], v[180:183], v[50:53]
	v_mfma_f32_16x16x32_bf16 v[38:41], v[164:167], v[188:191], v[38:41]
	v_mfma_f32_16x16x32_bf16 v[34:37], v[172:175], v[188:191], v[34:37]
	v_mfma_f32_16x16x32_bf16 v[22:25], v[164:167], v[196:199], v[22:25]
	v_mfma_f32_16x16x32_bf16 v[18:21], v[172:175], v[196:199], v[18:21]
	v_mfma_f32_16x16x32_bf16 v[6:9], v[164:167], v[204:207], v[6:9]
	v_mfma_f32_16x16x32_bf16 v[2:5], v[172:175], v[204:207], v[2:5]
	v_mfma_f32_16x16x32_bf16 v[54:57], v[168:171], v[184:187], v[54:57]
	v_mfma_f32_16x16x32_bf16 v[50:53], v[176:179], v[184:187], v[50:53]
	v_mfma_f32_16x16x32_bf16 v[38:41], v[168:171], v[192:195], v[38:41]
	v_mfma_f32_16x16x32_bf16 v[34:37], v[176:179], v[192:195], v[34:37]
	v_mfma_f32_16x16x32_bf16 v[22:25], v[168:171], v[200:203], v[22:25]
	v_mfma_f32_16x16x32_bf16 v[18:21], v[176:179], v[200:203], v[18:21]
	v_mfma_f32_16x16x32_bf16 v[6:9], v[168:171], v[208:211], v[6:9]
	v_mfma_f32_16x16x32_bf16 v[2:5], v[176:179], v[208:211], v[2:5]
	s_setprio 0
	s_barrier
	s_add_i32 s51, s51, 2
	s_add_u32 s18, s18, 0x100
	s_addc_u32 s19, s19, 0
	s_add_u32 s49, s49, 0x100
	s_addc_u32 s50, s50, 0
	s_cmp_gt_u32 s51, 13
	s_cbranch_scc0 .LBB0_390
	s_and_b64 vcc, exec, s[6:7]
	s_cbranch_vccz .LBB0_393
	s_barrier

; #define PG8_STAGE(bufoff, gbase, voff) do { _Pragma("unroll") for (int _i = 0; _i < 2; ++_i) \
;         __builtin_amdgcn_global_load_lds((const unsigned*)((const char*)(gbase) + (voff)[_i]), (PG8_LAS unsigned*)(lds + (bufoff) + ldsw + _i * 8192), 16, 0, 0); } while (0)
; #define PG8_LDA(dst, b, h) do { _Pragma("unroll") for (int m = 0; m < 4; ++m) _Pragma("unroll") for (int k = 0; k < 2; ++k) dst[m][k] = *(const PG8_LAS bf16x8*)(lds + PG8_SA(b, h) + aoff + m * 2048 + k * 1024); } while (0)
; #define PG8_LDB(dst, b, h) do { _Pragma("unroll") for (int n = 0; n < 2; ++n) _Pragma("unroll") for (int k = 0; k < 2; ++k) dst[n][k] = *(const PG8_LAS bf16x8*)(lds + PG8_SB(b, h) + boff + n * 2048 + k * 1024); } while (0)
; #define PG8_WAIT_V(n) asm volatile("s_waitcnt vmcnt(" #n ")" ::: "memory")
; #define PG8_WAIT_L(n) asm volatile("s_waitcnt lgkmcnt(" #n ")" ::: "memory")
; #define PG8_BAR __builtin_amdgcn_s_barrier()
; #define PG8_SCHED __builtin_amdgcn_sched_barrier(0)
; template <class Epi, class Sched, bool ALIGN_EPI = false, bool SP2 = false, bool GATHER = false>
; __device__ __forceinline__ void gemm_phase(PG8_LAS unsigned char* lds, const Gemm g, const Sched& S, const Epi& E, int tid_in, const int* rowsrc = nullptr, PG8_LAS int* idx_lds = nullptr) {
;     ...
;             PG8_LDB(B0, 0, 0); PG8_LDB(B1, 0, 1); PG8_SCHED; PG8_LDA(At, 0, 0); PG8_STAGE(PG8_SA(1, 1), a1 + hstepA, PG8_OA(1));
;             PG8_WAIT_V(8); PG8_WAIT_L(0); PG8_BAR; PG8_MMA(0, 0, At, B0); PG8_MMA(0, 1, At, B1); PG8_BAR; PG8_SCHED;
;             PG8_LDA(At, 0, 1); PG8_STAGE(PG8_SB(0, 0), b2, voffB); PG8_STAGE(PG8_SB(0, 1), b2 + hstep, voffB); PG8_STAGE(PG8_SA(0, 0), a2, PG8_OS(0));
;             PG8_WAIT_V(8); PG8_WAIT_L(0); PG8_BAR; PG8_MMA(1, 0, At, B0); PG8_MMA(1, 1, At, B1); PG8_BAR; PG8_SCHED;
;             PG8_LDB(B0, 1, 0); PG8_LDB(B1, 1, 1); PG8_SCHED; PG8_LDA(At, 1, 0); PG8_STAGE(PG8_SA(0, 1), a2 + hstepA, PG8_OS(1));
;             PG8_WAIT_V(8); PG8_WAIT_L(0); PG8_BAR; PG8_MMA(0, 0, At, B0); PG8_MMA(0, 1, At, B1); PG8_BAR; PG8_SCHED;
;             PG8_LDA(At, 1, 1); PG8_STAGE(PG8_SB(1, 0), b3, voffB); PG8_STAGE(PG8_SB(1, 1), b3 + hstep, voffB); PG8_STAGE(PG8_SA(1, 0), a3, PG8_OS(0));
;             PG8_WAIT_V(8); PG8_WAIT_L(0); PG8_BAR; PG8_MMA(1, 0, At, B0); PG8_MMA(1, 1, At, B1); PG8_BAR; PG8_SCHED;
.LBB0_615:
	s_add_u32 s22, s20, 0xfff80080
	s_addc_u32 s23, s21, -1
	s_add_i32 s58, 0, 0x10000
	s_cmp_eq_u32 s57, 28
	s_cselect_b32 s25, s9, s23
	s_cselect_b32 s24, s17, s22
	s_cselect_b32 s23, s7, s56
	s_cselect_b32 s22, s19, s55
	s_add_i32 s60, 0, 0x14000
	v_add_u32_e32 v142, s58, v184
	v_add_u32_e32 v182, s60, v184
	ds_read_b128 v[122:125], v142
	ds_read_b128 v[126:129], v142 offset:1024
	ds_read_b128 v[134:137], v142 offset:2048
	ds_read_b128 v[142:145], v142 offset:3072
	ds_read_b128 v[174:177], v182
	ds_read_b128 v[178:181], v182 offset:1024
	ds_read_b128 v[188:191], v182 offset:2048
	ds_read_b128 v[192:195], v182 offset:3072
	v_lshl_add_u64 v[182:183], s[20:21], 0, v[170:171]
	s_add_i32 m0, s39, 0xc000
	ds_read_b128 v[196:199], v186
	ds_read_b128 v[200:203], v186 offset:1024
	ds_read_b128 v[204:207], v186 offset:2048
	ds_read_b128 v[208:211], v186 offset:3072
	ds_read_b128 v[212:215], v186 offset:4096
	ds_read_b128 v[216:219], v186 offset:5120
	ds_read_b128 v[220:223], v186 offset:6144
	ds_read_b128 v[224:227], v186 offset:7168
	global_load_lds_dwordx4 v[182:183], off
	v_lshl_add_u64 v[182:183], s[20:21], 0, v[172:173]
	s_add_i32 m0, s39, 0xe000
	s_nop 0
	global_load_lds_dwordx4 v[182:183], off
	s_waitcnt vmcnt(8)
	s_waitcnt lgkmcnt(0)
	v_mfma_f32_16x16x32_bf16 v[138:141], v[122:125], v[196:199], v[138:141]
	v_mfma_f32_16x16x32_bf16 v[130:133], v[134:137], v[196:199], v[130:133]
	v_mfma_f32_16x16x32_bf16 v[118:121], v[122:125], v[204:207], v[118:121]
	s_barrier
	s_setprio 1
	s_waitcnt lgkmcnt(0)
	v_mfma_f32_16x16x32_bf16 v[106:109], v[134:137], v[204:207], v[106:109]
	v_mfma_f32_16x16x32_bf16 v[102:105], v[122:125], v[212:215], v[102:105]
	v_mfma_f32_16x16x32_bf16 v[90:93], v[134:137], v[212:215], v[90:93]
	v_mfma_f32_16x16x32_bf16 v[86:89], v[122:125], v[220:223], v[86:89]
	v_mfma_f32_16x16x32_bf16 v[74:77], v[134:137], v[220:223], v[74:77]
	v_mfma_f32_16x16x32_bf16 v[138:141], v[126:129], v[200:203], v[138:141]
	v_mfma_f32_16x16x32_bf16 v[130:133], v[142:145], v[200:203], v[130:133]
	v_mfma_f32_16x16x32_bf16 v[118:121], v[126:129], v[208:211], v[118:121]
	v_mfma_f32_16x16x32_bf16 v[106:109], v[142:145], v[208:211], v[106:109]
	v_mfma_f32_16x16x32_bf16 v[102:105], v[126:129], v[216:219], v[102:105]
	v_mfma_f32_16x16x32_bf16 v[90:93], v[142:145], v[216:219], v[90:93]
	v_mfma_f32_16x16x32_bf16 v[86:89], v[126:129], v[224:227], v[86:89]
	v_mfma_f32_16x16x32_bf16 v[74:77], v[142:145], v[224:227], v[74:77]
	s_setprio 0
	s_setprio 1
	v_mfma_f32_16x16x32_bf16 v[114:117], v[174:177], v[196:199], v[114:117]
	v_mfma_f32_16x16x32_bf16 v[110:113], v[188:191], v[196:199], v[110:113]
	v_mfma_f32_16x16x32_bf16 v[98:101], v[174:177], v[204:207], v[98:101]
	v_mfma_f32_16x16x32_bf16 v[94:97], v[188:191], v[204:207], v[94:97]
	v_mfma_f32_16x16x32_bf16 v[82:85], v[174:177], v[212:215], v[82:85]
	v_mfma_f32_16x16x32_bf16 v[78:81], v[188:191], v[212:215], v[78:81]
	v_mfma_f32_16x16x32_bf16 v[70:73], v[174:177], v[220:223], v[70:73]
	v_mfma_f32_16x16x32_bf16 v[66:69], v[188:191], v[220:223], v[66:69]
	v_mfma_f32_16x16x32_bf16 v[114:117], v[178:181], v[200:203], v[114:117]
	v_mfma_f32_16x16x32_bf16 v[110:113], v[192:195], v[200:203], v[110:113]
	v_mfma_f32_16x16x32_bf16 v[98:101], v[178:181], v[208:211], v[98:101]
	v_mfma_f32_16x16x32_bf16 v[94:97], v[192:195], v[208:211], v[94:97]
	v_mfma_f32_16x16x32_bf16 v[82:85], v[178:181], v[216:219], v[82:85]
	v_mfma_f32_16x16x32_bf16 v[78:81], v[192:195], v[216:219], v[78:81]
	v_mfma_f32_16x16x32_bf16 v[70:73], v[178:181], v[224:227], v[70:73]
	v_mfma_f32_16x16x32_bf16 v[66:69], v[192:195], v[224:227], v[66:69]
	s_setprio 0
	s_barrier
	s_add_i32 s58, s58, s38
	v_lshl_add_u64 v[182:183], s[22:23], 0, v[0:1]
	s_mov_b32 m0, s58
	ds_read_b128 v[196:199], v186 offset:16384
	ds_read_b128 v[200:203], v186 offset:17408
	ds_read_b128 v[204:207], v186 offset:18432
	ds_read_b128 v[208:211], v186 offset:19456
	ds_read_b128 v[212:215], v186 offset:20480
	ds_read_b128 v[216:219], v186 offset:21504
	ds_read_b128 v[220:223], v186 offset:22528
	ds_read_b128 v[224:227], v186 offset:23552
	global_load_lds_dwordx4 v[182:183], off
	s_add_i32 m0, s58, 0x2000
	s_add_u32 s58, s22, 0x80000
	v_lshl_add_u64 v[228:229], s[22:23], 0, v[148:149]
	s_addc_u32 s59, s23, 0
	s_add_i32 s60, s60, s38
	global_load_lds_dwordx4 v[228:229], off
	v_lshl_add_u64 v[230:231], s[58:59], 0, v[0:1]
	s_mov_b32 m0, s60
	v_lshl_add_u64 v[232:233], s[24:25], 0, v[150:151]
	global_load_lds_dwordx4 v[230:231], off
	v_lshl_add_u64 v[230:231], s[58:59], 0, v[148:149]
	s_add_i32 m0, s60, 0x2000
	s_nop 0
	global_load_lds_dwordx4 v[230:231], off
	v_lshl_add_u64 v[230:231], s[24:25], 0, v[152:153]
	s_mov_b32 m0, s39
	s_nop 0
	global_load_lds_dwordx4 v[230:231], off
	s_mov_b32 m0, s41
	s_nop 0
	global_load_lds_dwordx4 v[232:233], off
	s_waitcnt vmcnt(8)
	s_waitcnt lgkmcnt(0)
	v_mfma_f32_16x16x32_bf16 v[62:65], v[122:125], v[196:199], v[62:65]
	v_mfma_f32_16x16x32_bf16 v[58:61], v[134:137], v[196:199], v[58:61]
	v_mfma_f32_16x16x32_bf16 v[54:57], v[122:125], v[204:207], v[54:57]
	s_barrier
; #define PG8_STAGE(bufoff, gbase, voff) do { _Pragma("unroll") for (int _i = 0; _i < 2; ++_i) \
;         __builtin_amdgcn_global_load_lds((const unsigned*)((const char*)(gbase) + (voff)[_i]), (PG8_LAS unsigned*)(lds + (bufoff) + ldsw + _i * 8192), 16, 0, 0); } while (0)
; #define PG8_LDA(dst, b, h) do { _Pragma("unroll") for (int m = 0; m < 4; ++m) _Pragma("unroll") for (int k = 0; k < 2; ++k) dst[m][k] = *(const PG8_LAS bf16x8*)(lds + PG8_SA(b, h) + aoff + m * 2048 + k * 1024); } while (0)
; #define PG8_LDB(dst, b, h) do { _Pragma("unroll") for (int n = 0; n < 2; ++n) _Pragma("unroll") for (int k = 0; k < 2; ++k) dst[n][k] = *(const PG8_LAS bf16x8*)(lds + PG8_SB(b, h) + boff + n * 2048 + k * 1024); } while (0)
; #define PG8_WAIT_V(n) asm volatile("s_waitcnt vmcnt(" #n ")" ::: "memory")
; #define PG8_WAIT_L(n) asm volatile("s_waitcnt lgkmcnt(" #n ")" ::: "memory")
; #define PG8_BAR __builtin_amdgcn_s_barrier()
; #define PG8_SCHED __builtin_amdgcn_sched_barrier(0)
; template <class Epi, class Sched, bool ALIGN_EPI = false, bool SP2 = false, bool GATHER = false>
; __device__ __forceinline__ void gemm_phase(PG8_LAS unsigned char* lds, const Gemm g, const Sched& S, const Epi& E, int tid_in, const int* rowsrc = nullptr, PG8_LAS int* idx_lds = nullptr) {
;     ...
;             PG8_LDB(B0, 0, 0); PG8_LDB(B1, 0, 1); PG8_SCHED; PG8_LDA(At, 0, 0); PG8_STAGE(PG8_SA(1, 1), a1 + hstepA, PG8_OA(1));
;             PG8_WAIT_V(8); PG8_WAIT_L(0); PG8_BAR; PG8_MMA(0, 0, At, B0); PG8_MMA(0, 1, At, B1); PG8_BAR; PG8_SCHED;
;             PG8_LDA(At, 0, 1); PG8_STAGE(PG8_SB(0, 0), b2, voffB); PG8_STAGE(PG8_SB(0, 1), b2 + hstep, voffB); PG8_STAGE(PG8_SA(0, 0), a2, PG8_OS(0));
;             PG8_WAIT_V(8); PG8_WAIT_L(0); PG8_BAR; PG8_MMA(1, 0, At, B0); PG8_MMA(1, 1, At, B1); PG8_BAR; PG8_SCHED;
;             PG8_LDB(B0, 1, 0); PG8_LDB(B1, 1, 1); PG8_SCHED; PG8_LDA(At, 1, 0); PG8_STAGE(PG8_SA(0, 1), a2 + hstepA, PG8_OS(1));
;             PG8_WAIT_V(8); PG8_WAIT_L(0); PG8_BAR; PG8_MMA(0, 0, At, B0); PG8_MMA(0, 1, At, B1); PG8_BAR; PG8_SCHED;
;             PG8_LDA(At, 1, 1); PG8_STAGE(PG8_SB(1, 0), b3, voffB); PG8_STAGE(PG8_SB(1, 1), b3 + hstep, voffB); PG8_STAGE(PG8_SA(1, 0), a3, PG8_OS(0));
;             PG8_WAIT_V(8); PG8_WAIT_L(0); PG8_BAR; PG8_MMA(1, 0, At, B0); PG8_MMA(1, 1, At, B1); PG8_BAR; PG8_SCHED;
	s_setprio 1
	s_waitcnt lgkmcnt(0)
	v_mfma_f32_16x16x32_bf16 v[42:45], v[134:137], v[204:207], v[42:45]
	v_mfma_f32_16x16x32_bf16 v[38:41], v[122:125], v[212:215], v[38:41]
	v_mfma_f32_16x16x32_bf16 v[26:29], v[134:137], v[212:215], v[26:29]
	v_mfma_f32_16x16x32_bf16 v[22:25], v[122:125], v[220:223], v[22:25]
	v_mfma_f32_16x16x32_bf16 v[10:13], v[134:137], v[220:223], v[10:13]
	v_mfma_f32_16x16x32_bf16 v[62:65], v[126:129], v[200:203], v[62:65]
	v_mfma_f32_16x16x32_bf16 v[58:61], v[142:145], v[200:203], v[58:61]
	v_mfma_f32_16x16x32_bf16 v[54:57], v[126:129], v[208:211], v[54:57]
	v_mfma_f32_16x16x32_bf16 v[42:45], v[142:145], v[208:211], v[42:45]
	v_mfma_f32_16x16x32_bf16 v[38:41], v[126:129], v[216:219], v[38:41]
	v_mfma_f32_16x16x32_bf16 v[26:29], v[142:145], v[216:219], v[26:29]
	v_mfma_f32_16x16x32_bf16 v[22:25], v[126:129], v[224:227], v[22:25]
	v_mfma_f32_16x16x32_bf16 v[10:13], v[142:145], v[224:227], v[10:13]
	s_setprio 0
	s_setprio 1
	v_mfma_f32_16x16x32_bf16 v[50:53], v[174:177], v[196:199], v[50:53]
	v_mfma_f32_16x16x32_bf16 v[46:49], v[188:191], v[196:199], v[46:49]
	v_mfma_f32_16x16x32_bf16 v[34:37], v[174:177], v[204:207], v[34:37]
	v_mfma_f32_16x16x32_bf16 v[30:33], v[188:191], v[204:207], v[30:33]
	v_mfma_f32_16x16x32_bf16 v[18:21], v[174:177], v[212:215], v[18:21]
	v_mfma_f32_16x16x32_bf16 v[14:17], v[188:191], v[212:215], v[14:17]
	v_mfma_f32_16x16x32_bf16 v[6:9], v[174:177], v[220:223], v[6:9]
	v_mfma_f32_16x16x32_bf16 v[2:5], v[188:191], v[220:223], v[2:5]
	v_mfma_f32_16x16x32_bf16 v[50:53], v[178:181], v[200:203], v[50:53]
	v_mfma_f32_16x16x32_bf16 v[46:49], v[192:195], v[200:203], v[46:49]
	v_mfma_f32_16x16x32_bf16 v[34:37], v[178:181], v[208:211], v[34:37]
	v_mfma_f32_16x16x32_bf16 v[30:33], v[192:195], v[208:211], v[30:33]
	v_mfma_f32_16x16x32_bf16 v[18:21], v[178:181], v[216:219], v[18:21]
	v_mfma_f32_16x16x32_bf16 v[14:17], v[192:195], v[216:219], v[14:17]
	v_mfma_f32_16x16x32_bf16 v[6:9], v[178:181], v[224:227], v[6:9]
	v_mfma_f32_16x16x32_bf16 v[2:5], v[192:195], v[224:227], v[2:5]
	s_setprio 0
	s_barrier
	s_add_i32 s58, 0, 0x18000
	s_add_i32 s59, 0, 0x1c000
	v_add_u32_e32 v142, s58, v184
	v_add_u32_e32 v187, s59, v184
	ds_read_b128 v[122:125], v142
	ds_read_b128 v[126:129], v142 offset:1024
	ds_read_b128 v[134:137], v142 offset:2048
	ds_read_b128 v[142:145], v142 offset:3072
	ds_read_b128 v[174:177], v187
	ds_read_b128 v[178:181], v187 offset:1024
	ds_read_b128 v[188:191], v187 offset:2048
	ds_read_b128 v[192:195], v187 offset:3072
	s_add_u32 s24, s24, 0x80000
	s_addc_u32 s25, s25, 0
	s_mov_b32 m0, s43
	v_lshl_add_u64 v[234:235], s[24:25], 0, v[152:153]
	ds_read_b128 v[196:199], v186 offset:32768
	ds_read_b128 v[200:203], v186 offset:33792
	ds_read_b128 v[204:207], v186 offset:34816
	ds_read_b128 v[208:211], v186 offset:35840
	ds_read_b128 v[212:215], v186 offset:36864
	ds_read_b128 v[216:219], v186 offset:37888
	ds_read_b128 v[220:223], v186 offset:38912
	ds_read_b128 v[224:227], v186 offset:39936
	global_load_lds_dwordx4 v[234:235], off
	v_lshl_add_u64 v[234:235], s[24:25], 0, v[150:151]
	s_mov_b32 m0, s45
	s_nop 0
	global_load_lds_dwordx4 v[234:235], off
	s_waitcnt vmcnt(8)
	s_waitcnt lgkmcnt(0)
	v_mfma_f32_16x16x32_bf16 v[138:141], v[122:125], v[196:199], v[138:141]
	v_mfma_f32_16x16x32_bf16 v[130:133], v[134:137], v[196:199], v[130:133]
	v_mfma_f32_16x16x32_bf16 v[118:121], v[122:125], v[204:207], v[118:121]
	s_barrier
	s_setprio 1
	s_waitcnt lgkmcnt(0)
	v_mfma_f32_16x16x32_bf16 v[106:109], v[134:137], v[204:207], v[106:109]
	v_mfma_f32_16x16x32_bf16 v[102:105], v[122:125], v[212:215], v[102:105]
	v_mfma_f32_16x16x32_bf16 v[90:93], v[134:137], v[212:215], v[90:93]
	v_mfma_f32_16x16x32_bf16 v[86:89], v[122:125], v[220:223], v[86:89]
	v_mfma_f32_16x16x32_bf16 v[74:77], v[134:137], v[220:223], v[74:77]
	v_mfma_f32_16x16x32_bf16 v[138:141], v[126:129], v[200:203], v[138:141]
	v_mfma_f32_16x16x32_bf16 v[130:133], v[142:145], v[200:203], v[130:133]
	v_mfma_f32_16x16x32_bf16 v[118:121], v[126:129], v[208:211], v[118:121]
	v_mfma_f32_16x16x32_bf16 v[106:109], v[142:145], v[208:211], v[106:109]
	v_mfma_f32_16x16x32_bf16 v[102:105], v[126:129], v[216:219], v[102:105]
	v_mfma_f32_16x16x32_bf16 v[90:93], v[142:145], v[216:219], v[90:93]
	v_mfma_f32_16x16x32_bf16 v[86:89], v[126:129], v[224:227], v[86:89]
	v_mfma_f32_16x16x32_bf16 v[74:77], v[142:145], v[224:227], v[74:77]
	s_setprio 0
	s_setprio 1
	v_mfma_f32_16x16x32_bf16 v[114:117], v[174:177], v[196:199], v[114:117]
	v_mfma_f32_16x16x32_bf16 v[110:113], v[188:191], v[196:199], v[110:113]
	v_mfma_f32_16x16x32_bf16 v[98:101], v[174:177], v[204:207], v[98:101]
	v_mfma_f32_16x16x32_bf16 v[94:97], v[188:191], v[204:207], v[94:97]
	v_mfma_f32_16x16x32_bf16 v[82:85], v[174:177], v[212:215], v[82:85]
	v_mfma_f32_16x16x32_bf16 v[78:81], v[188:191], v[212:215], v[78:81]
	v_mfma_f32_16x16x32_bf16 v[70:73], v[174:177], v[220:223], v[70:73]
	v_mfma_f32_16x16x32_bf16 v[66:69], v[188:191], v[220:223], v[66:69]
	v_mfma_f32_16x16x32_bf16 v[114:117], v[178:181], v[200:203], v[114:117]
	v_mfma_f32_16x16x32_bf16 v[110:113], v[192:195], v[200:203], v[110:113]
	v_mfma_f32_16x16x32_bf16 v[98:101], v[178:181], v[208:211], v[98:101]
	v_mfma_f32_16x16x32_bf16 v[94:97], v[192:195], v[208:211], v[94:97]
	v_mfma_f32_16x16x32_bf16 v[82:85], v[178:181], v[216:219], v[82:85]
	v_mfma_f32_16x16x32_bf16 v[78:81], v[192:195], v[216:219], v[78:81]
	v_mfma_f32_16x16x32_bf16 v[70:73], v[178:181], v[224:227], v[70:73]
	v_mfma_f32_16x16x32_bf16 v[66:69], v[192:195], v[224:227], v[66:69]
	s_setprio 0
	s_barrier
; #define PG8_STAGE(bufoff, gbase, voff) do { _Pragma("unroll") for (int _i = 0; _i < 2; ++_i) \
;         __builtin_amdgcn_global_load_lds((const unsigned*)((const char*)(gbase) + (voff)[_i]), (PG8_LAS unsigned*)(lds + (bufoff) + ldsw + _i * 8192), 16, 0, 0); } while (0)
; #define PG8_LDA(dst, b, h) do { _Pragma("unroll") for (int m = 0; m < 4; ++m) _Pragma("unroll") for (int k = 0; k < 2; ++k) dst[m][k] = *(const PG8_LAS bf16x8*)(lds + PG8_SA(b, h) + aoff + m * 2048 + k * 1024); } while (0)
; #define PG8_LDB(dst, b, h) do { _Pragma("unroll") for (int n = 0; n < 2; ++n) _Pragma("unroll") for (int k = 0; k < 2; ++k) dst[n][k] = *(const PG8_LAS bf16x8*)(lds + PG8_SB(b, h) + boff + n * 2048 + k * 1024); } while (0)
; #define PG8_WAIT_V(n) asm volatile("s_waitcnt vmcnt(" #n ")" ::: "memory")
; #define PG8_WAIT_L(n) asm volatile("s_waitcnt lgkmcnt(" #n ")" ::: "memory")
; #define PG8_BAR __builtin_amdgcn_s_barrier()
; #define PG8_SCHED __builtin_amdgcn_sched_barrier(0)
; template <class Epi, class Sched, bool ALIGN_EPI = false, bool SP2 = false, bool GATHER = false>
; __device__ __forceinline__ void gemm_phase(PG8_LAS unsigned char* lds, const Gemm g, const Sched& S, const Epi& E, int tid_in, const int* rowsrc = nullptr, PG8_LAS int* idx_lds = nullptr) {
;     ...
;             PG8_LDB(B0, 0, 0); PG8_LDB(B1, 0, 1); PG8_SCHED; PG8_LDA(At, 0, 0); PG8_STAGE(PG8_SA(1, 1), a1 + hstepA, PG8_OA(1));
;             PG8_WAIT_V(8); PG8_WAIT_L(0); PG8_BAR; PG8_MMA(0, 0, At, B0); PG8_MMA(0, 1, At, B1); PG8_BAR; PG8_SCHED;
;             PG8_LDA(At, 0, 1); PG8_STAGE(PG8_SB(0, 0), b2, voffB); PG8_STAGE(PG8_SB(0, 1), b2 + hstep, voffB); PG8_STAGE(PG8_SA(0, 0), a2, PG8_OS(0));
;             PG8_WAIT_V(8); PG8_WAIT_L(0); PG8_BAR; PG8_MMA(1, 0, At, B0); PG8_MMA(1, 1, At, B1); PG8_BAR; PG8_SCHED;
;             PG8_LDB(B0, 1, 0); PG8_LDB(B1, 1, 1); PG8_SCHED; PG8_LDA(At, 1, 0); PG8_STAGE(PG8_SA(0, 1), a2 + hstepA, PG8_OS(1));
;             PG8_WAIT_V(8); PG8_WAIT_L(0); PG8_BAR; PG8_MMA(0, 0, At, B0); PG8_MMA(0, 1, At, B1); PG8_BAR; PG8_SCHED;
;             PG8_LDA(At, 1, 1); PG8_STAGE(PG8_SB(1, 0), b3, voffB); PG8_STAGE(PG8_SB(1, 1), b3 + hstep, voffB); PG8_STAGE(PG8_SA(1, 0), a3, PG8_OS(0));
;             PG8_WAIT_V(8); PG8_WAIT_L(0); PG8_BAR; PG8_MMA(1, 0, At, B0); PG8_MMA(1, 1, At, B1); PG8_BAR; PG8_SCHED;
	s_add_i32 s24, s58, s38
	v_lshl_add_u64 v[182:183], v[182:183], 0, s[10:11]
	s_mov_b32 m0, s24
	ds_read_b128 v[196:199], v186 offset:49152
	ds_read_b128 v[200:203], v186 offset:50176
	ds_read_b128 v[204:207], v186 offset:51200
	ds_read_b128 v[208:211], v186 offset:52224
	ds_read_b128 v[212:215], v186 offset:53248
	ds_read_b128 v[216:219], v186 offset:54272
	ds_read_b128 v[220:223], v186 offset:55296
	ds_read_b128 v[224:227], v186 offset:56320
	global_load_lds_dwordx4 v[182:183], off
	s_add_i32 m0, s24, 0x2000
	s_add_u32 s22, s22, 0x80080
	v_lshl_add_u64 v[182:183], v[228:229], 0, s[10:11]
	s_addc_u32 s23, s23, 0
	s_add_i32 s24, s59, s38
	global_load_lds_dwordx4 v[182:183], off
	v_lshl_add_u64 v[182:183], s[22:23], 0, v[0:1]
	s_mov_b32 m0, s24
	s_nop 0
	global_load_lds_dwordx4 v[182:183], off
	v_lshl_add_u64 v[182:183], s[22:23], 0, v[148:149]
	s_add_i32 m0, s24, 0x2000
	s_nop 0
	global_load_lds_dwordx4 v[182:183], off
	v_lshl_add_u64 v[182:183], v[230:231], 0, s[10:11]
	s_mov_b32 m0, s52
	s_nop 0
	global_load_lds_dwordx4 v[182:183], off
	v_lshl_add_u64 v[182:183], v[232:233], 0, s[10:11]
	s_mov_b32 m0, s53
	s_nop 0
	global_load_lds_dwordx4 v[182:183], off
	s_waitcnt vmcnt(8)
	s_waitcnt lgkmcnt(0)
	v_mfma_f32_16x16x32_bf16 v[62:65], v[122:125], v[196:199], v[62:65]
	v_mfma_f32_16x16x32_bf16 v[58:61], v[134:137], v[196:199], v[58:61]
	v_mfma_f32_16x16x32_bf16 v[54:57], v[122:125], v[204:207], v[54:57]
	s_barrier
	s_setprio 1
	s_waitcnt lgkmcnt(0)
	v_mfma_f32_16x16x32_bf16 v[42:45], v[134:137], v[204:207], v[42:45]
	v_mfma_f32_16x16x32_bf16 v[38:41], v[122:125], v[212:215], v[38:41]
	v_mfma_f32_16x16x32_bf16 v[26:29], v[134:137], v[212:215], v[26:29]
	v_mfma_f32_16x16x32_bf16 v[22:25], v[122:125], v[220:223], v[22:25]
	v_mfma_f32_16x16x32_bf16 v[10:13], v[134:137], v[220:223], v[10:13]
	v_mfma_f32_16x16x32_bf16 v[62:65], v[126:129], v[200:203], v[62:65]
	v_mfma_f32_16x16x32_bf16 v[58:61], v[142:145], v[200:203], v[58:61]
	v_mfma_f32_16x16x32_bf16 v[54:57], v[126:129], v[208:211], v[54:57]
	v_mfma_f32_16x16x32_bf16 v[42:45], v[142:145], v[208:211], v[42:45]
	v_mfma_f32_16x16x32_bf16 v[38:41], v[126:129], v[216:219], v[38:41]
	v_mfma_f32_16x16x32_bf16 v[26:29], v[142:145], v[216:219], v[26:29]
	v_mfma_f32_16x16x32_bf16 v[22:25], v[126:129], v[224:227], v[22:25]
	v_mfma_f32_16x16x32_bf16 v[10:13], v[142:145], v[224:227], v[10:13]
	s_setprio 0
	s_setprio 1
	v_mfma_f32_16x16x32_bf16 v[50:53], v[174:177], v[196:199], v[50:53]
	v_mfma_f32_16x16x32_bf16 v[46:49], v[188:191], v[196:199], v[46:49]
	v_mfma_f32_16x16x32_bf16 v[34:37], v[174:177], v[204:207], v[34:37]
	v_mfma_f32_16x16x32_bf16 v[30:33], v[188:191], v[204:207], v[30:33]
	v_mfma_f32_16x16x32_bf16 v[18:21], v[174:177], v[212:215], v[18:21]
	v_mfma_f32_16x16x32_bf16 v[14:17], v[188:191], v[212:215], v[14:17]
	v_mfma_f32_16x16x32_bf16 v[6:9], v[174:177], v[220:223], v[6:9]
	v_mfma_f32_16x16x32_bf16 v[2:5], v[188:191], v[220:223], v[2:5]
	v_mfma_f32_16x16x32_bf16 v[50:53], v[178:181], v[200:203], v[50:53]
	v_mfma_f32_16x16x32_bf16 v[46:49], v[192:195], v[200:203], v[46:49]
	v_mfma_f32_16x16x32_bf16 v[34:37], v[178:181], v[208:211], v[34:37]
	v_mfma_f32_16x16x32_bf16 v[30:33], v[192:195], v[208:211], v[30:33]
	v_mfma_f32_16x16x32_bf16 v[18:21], v[178:181], v[216:219], v[18:21]
	v_mfma_f32_16x16x32_bf16 v[14:17], v[192:195], v[216:219], v[14:17]
	v_mfma_f32_16x16x32_bf16 v[6:9], v[178:181], v[224:227], v[6:9]
	v_mfma_f32_16x16x32_bf16 v[2:5], v[192:195], v[224:227], v[2:5]
	s_setprio 0
	s_barrier
	s_add_i32 s57, s57, 2
	s_add_u32 s20, s20, 0x100
	s_addc_u32 s21, s21, 0
	s_add_u32 s55, s55, 0x100
	s_addc_u32 s56, s56, 0
	s_cmp_gt_u32 s57, 29
	s_cbranch_scc0 .LBB0_615
	s_and_b64 vcc, exec, s[4:5]
	s_cbranch_vccz .LBB0_618
	s_barrier

; #define PG8_STAGE(bufoff, gbase, voff) do { _Pragma("unroll") for (int _i = 0; _i < 2; ++_i) \
;         __builtin_amdgcn_global_load_lds((const unsigned*)((const char*)(gbase) + (voff)[_i]), (PG8_LAS unsigned*)(lds + (bufoff) + ldsw + _i * 8192), 16, 0, 0); } while (0)
; #define PG8_LDA(dst, b, h) do { _Pragma("unroll") for (int m = 0; m < 4; ++m) _Pragma("unroll") for (int k = 0; k < 2; ++k) dst[m][k] = *(const PG8_LAS bf16x8*)(lds + PG8_SA(b, h) + aoff + m * 2048 + k * 1024); } while (0)
; #define PG8_LDB(dst, b, h) do { _Pragma("unroll") for (int n = 0; n < 2; ++n) _Pragma("unroll") for (int k = 0; k < 2; ++k) dst[n][k] = *(const PG8_LAS bf16x8*)(lds + PG8_SB(b, h) + boff + n * 2048 + k * 1024); } while (0)
; #define PG8_WAIT_V(n) asm volatile("s_waitcnt vmcnt(" #n ")" ::: "memory")
; #define PG8_WAIT_L(n) asm volatile("s_waitcnt lgkmcnt(" #n ")" ::: "memory")
; #define PG8_BAR __builtin_amdgcn_s_barrier()
; #define PG8_SCHED __builtin_amdgcn_sched_barrier(0)
; template <class Epi, class Sched, bool ALIGN_EPI = false, bool SP2 = false, bool GATHER = false>
; __device__ __forceinline__ void gemm_phase(PG8_LAS unsigned char* lds, const Gemm g, const Sched& S, const Epi& E, int tid_in, const int* rowsrc = nullptr, PG8_LAS int* idx_lds = nullptr) {
;     ...
;             PG8_LDB(B0, 0, 0); PG8_LDB(B1, 0, 1); PG8_SCHED; PG8_LDA(At, 0, 0); PG8_STAGE(PG8_SA(1, 1), a1 + hstepA, PG8_OA(1));
;             PG8_WAIT_V(8); PG8_WAIT_L(0); PG8_BAR; PG8_MMA(0, 0, At, B0); PG8_MMA(0, 1, At, B1); PG8_BAR; PG8_SCHED;
;             PG8_LDA(At, 0, 1); PG8_STAGE(PG8_SB(0, 0), b2, voffB); PG8_STAGE(PG8_SB(0, 1), b2 + hstep, voffB); PG8_STAGE(PG8_SA(0, 0), a2, PG8_OS(0));
;             PG8_WAIT_V(8); PG8_WAIT_L(0); PG8_BAR; PG8_MMA(1, 0, At, B0); PG8_MMA(1, 1, At, B1); PG8_BAR; PG8_SCHED;
;             PG8_LDB(B0, 1, 0); PG8_LDB(B1, 1, 1); PG8_SCHED; PG8_LDA(At, 1, 0); PG8_STAGE(PG8_SA(0, 1), a2 + hstepA, PG8_OS(1));
;             PG8_WAIT_V(8); PG8_WAIT_L(0); PG8_BAR; PG8_MMA(0, 0, At, B0); PG8_MMA(0, 1, At, B1); PG8_BAR; PG8_SCHED;
;             PG8_LDA(At, 1, 1); PG8_STAGE(PG8_SB(1, 0), b3, voffB); PG8_STAGE(PG8_SB(1, 1), b3 + hstep, voffB); PG8_STAGE(PG8_SA(1, 0), a3, PG8_OS(0));
;             PG8_WAIT_V(8); PG8_WAIT_L(0); PG8_BAR; PG8_MMA(1, 0, At, B0); PG8_MMA(1, 1, At, B1); PG8_BAR; PG8_SCHED;
.LBB0_692:
	s_add_u32 s22, s20, 0xfffc0080
	s_addc_u32 s23, s21, -1
	s_add_i32 s52, 0, 0x10000
	s_cmp_eq_u32 s51, 12
	s_cselect_b32 s25, s15, s23
	s_cselect_b32 s24, s47, s22
	s_cselect_b32 s23, s13, s50
	s_cselect_b32 s22, s48, s49
	s_add_i32 s54, 0, 0x14000
	v_add_u32_e32 v158, s52, v145
	v_add_u32_e32 v174, s54, v145
	ds_read_b128 v[140:143], v158
	ds_read_b128 v[150:153], v158 offset:1024
	ds_read_b128 v[154:157], v158 offset:2048
	ds_read_b128 v[158:161], v158 offset:3072
	ds_read_b128 v[162:165], v174
	ds_read_b128 v[166:169], v174 offset:1024
	ds_read_b128 v[170:173], v174 offset:2048
	ds_read_b128 v[174:177], v174 offset:3072
	v_lshl_add_u64 v[178:179], s[20:21], 0, v[136:137]
	s_add_i32 m0, s31, 0xc000
	ds_read_b128 v[184:187], v149
	ds_read_b128 v[188:191], v149 offset:1024
	ds_read_b128 v[192:195], v149 offset:2048
	ds_read_b128 v[196:199], v149 offset:3072
	ds_read_b128 v[200:203], v149 offset:4096
	ds_read_b128 v[204:207], v149 offset:5120
	ds_read_b128 v[208:211], v149 offset:6144
	ds_read_b128 v[212:215], v149 offset:7168
	global_load_lds_dwordx4 v[178:179], off
	v_lshl_add_u64 v[178:179], s[20:21], 0, v[138:139]
	s_add_i32 m0, s31, 0xe000
	s_nop 0
	global_load_lds_dwordx4 v[178:179], off
	s_waitcnt vmcnt(8)
	s_waitcnt lgkmcnt(0)
	v_mfma_f32_16x16x32_bf16 v[126:129], v[140:143], v[184:187], v[126:129]
	v_mfma_f32_16x16x32_bf16 v[122:125], v[154:157], v[184:187], v[122:125]
	v_mfma_f32_16x16x32_bf16 v[118:121], v[140:143], v[192:195], v[118:121]
	s_barrier
	s_setprio 1
	s_waitcnt lgkmcnt(0)
	v_mfma_f32_16x16x32_bf16 v[110:113], v[154:157], v[192:195], v[110:113]
	v_mfma_f32_16x16x32_bf16 v[102:105], v[140:143], v[200:203], v[102:105]
	v_mfma_f32_16x16x32_bf16 v[94:97], v[154:157], v[200:203], v[94:97]
	v_mfma_f32_16x16x32_bf16 v[86:89], v[140:143], v[208:211], v[86:89]
	v_mfma_f32_16x16x32_bf16 v[78:81], v[154:157], v[208:211], v[78:81]
	v_mfma_f32_16x16x32_bf16 v[126:129], v[150:153], v[188:191], v[126:129]
	v_mfma_f32_16x16x32_bf16 v[122:125], v[158:161], v[188:191], v[122:125]
	v_mfma_f32_16x16x32_bf16 v[118:121], v[150:153], v[196:199], v[118:121]
	v_mfma_f32_16x16x32_bf16 v[110:113], v[158:161], v[196:199], v[110:113]
	v_mfma_f32_16x16x32_bf16 v[102:105], v[150:153], v[204:207], v[102:105]
	v_mfma_f32_16x16x32_bf16 v[94:97], v[158:161], v[204:207], v[94:97]
	v_mfma_f32_16x16x32_bf16 v[86:89], v[150:153], v[212:215], v[86:89]
	v_mfma_f32_16x16x32_bf16 v[78:81], v[158:161], v[212:215], v[78:81]
	s_setprio 0
	s_setprio 1
	v_mfma_f32_16x16x32_bf16 v[114:117], v[162:165], v[184:187], v[114:117]
	v_mfma_f32_16x16x32_bf16 v[106:109], v[170:173], v[184:187], v[106:109]
	v_mfma_f32_16x16x32_bf16 v[98:101], v[162:165], v[192:195], v[98:101]
	v_mfma_f32_16x16x32_bf16 v[90:93], v[170:173], v[192:195], v[90:93]
	v_mfma_f32_16x16x32_bf16 v[82:85], v[162:165], v[200:203], v[82:85]
	v_mfma_f32_16x16x32_bf16 v[74:77], v[170:173], v[200:203], v[74:77]
	v_mfma_f32_16x16x32_bf16 v[70:73], v[162:165], v[208:211], v[70:73]
	v_mfma_f32_16x16x32_bf16 v[66:69], v[170:173], v[208:211], v[66:69]
	v_mfma_f32_16x16x32_bf16 v[114:117], v[166:169], v[188:191], v[114:117]
	v_mfma_f32_16x16x32_bf16 v[106:109], v[174:177], v[188:191], v[106:109]
	v_mfma_f32_16x16x32_bf16 v[98:101], v[166:169], v[196:199], v[98:101]
	v_mfma_f32_16x16x32_bf16 v[90:93], v[174:177], v[196:199], v[90:93]
	v_mfma_f32_16x16x32_bf16 v[82:85], v[166:169], v[204:207], v[82:85]
	v_mfma_f32_16x16x32_bf16 v[74:77], v[174:177], v[204:207], v[74:77]
	v_mfma_f32_16x16x32_bf16 v[70:73], v[166:169], v[212:215], v[70:73]
	v_mfma_f32_16x16x32_bf16 v[66:69], v[174:177], v[212:215], v[66:69]
	s_setprio 0
	s_barrier
	s_add_i32 s52, s52, s30
	v_lshl_add_u64 v[178:179], s[22:23], 0, v[0:1]
	s_mov_b32 m0, s52
	ds_read_b128 v[184:187], v149 offset:16384
	ds_read_b128 v[188:191], v149 offset:17408
	ds_read_b128 v[192:195], v149 offset:18432
	ds_read_b128 v[196:199], v149 offset:19456
	ds_read_b128 v[200:203], v149 offset:20480
	ds_read_b128 v[204:207], v149 offset:21504
	ds_read_b128 v[208:211], v149 offset:22528
	ds_read_b128 v[212:215], v149 offset:23552
	global_load_lds_dwordx4 v[178:179], off
	s_add_i32 m0, s52, 0x2000
	s_add_u32 s52, s22, 0x40000
	v_lshl_add_u64 v[180:181], s[22:23], 0, v[130:131]
	s_addc_u32 s53, s23, 0
	s_add_i32 s54, s54, s30
	global_load_lds_dwordx4 v[180:181], off
	v_lshl_add_u64 v[182:183], s[52:53], 0, v[0:1]
	s_mov_b32 m0, s54
	v_lshl_add_u64 v[216:217], s[24:25], 0, v[132:133]
	global_load_lds_dwordx4 v[182:183], off
	v_lshl_add_u64 v[182:183], s[52:53], 0, v[130:131]
	s_add_i32 m0, s54, 0x2000
	s_nop 0
	global_load_lds_dwordx4 v[182:183], off
	v_lshl_add_u64 v[182:183], s[24:25], 0, v[134:135]
	s_mov_b32 m0, s31
	s_nop 0
	global_load_lds_dwordx4 v[182:183], off
	s_mov_b32 m0, s34
	s_nop 0
	global_load_lds_dwordx4 v[216:217], off
	s_waitcnt vmcnt(8)
	s_waitcnt lgkmcnt(0)
	v_mfma_f32_16x16x32_bf16 v[62:65], v[140:143], v[184:187], v[62:65]
	v_mfma_f32_16x16x32_bf16 v[58:61], v[154:157], v[184:187], v[58:61]
	v_mfma_f32_16x16x32_bf16 v[54:57], v[140:143], v[192:195], v[54:57]
	s_barrier
; #define PG8_STAGE(bufoff, gbase, voff) do { _Pragma("unroll") for (int _i = 0; _i < 2; ++_i) \
;         __builtin_amdgcn_global_load_lds((const unsigned*)((const char*)(gbase) + (voff)[_i]), (PG8_LAS unsigned*)(lds + (bufoff) + ldsw + _i * 8192), 16, 0, 0); } while (0)
; #define PG8_LDA(dst, b, h) do { _Pragma("unroll") for (int m = 0; m < 4; ++m) _Pragma("unroll") for (int k = 0; k < 2; ++k) dst[m][k] = *(const PG8_LAS bf16x8*)(lds + PG8_SA(b, h) + aoff + m * 2048 + k * 1024); } while (0)
; #define PG8_LDB(dst, b, h) do { _Pragma("unroll") for (int n = 0; n < 2; ++n) _Pragma("unroll") for (int k = 0; k < 2; ++k) dst[n][k] = *(const PG8_LAS bf16x8*)(lds + PG8_SB(b, h) + boff + n * 2048 + k * 1024); } while (0)
; #define PG8_WAIT_V(n) asm volatile("s_waitcnt vmcnt(" #n ")" ::: "memory")
; #define PG8_WAIT_L(n) asm volatile("s_waitcnt lgkmcnt(" #n ")" ::: "memory")
; #define PG8_BAR __builtin_amdgcn_s_barrier()
; #define PG8_SCHED __builtin_amdgcn_sched_barrier(0)
; template <class Epi, class Sched, bool ALIGN_EPI = false, bool SP2 = false, bool GATHER = false>
; __device__ __forceinline__ void gemm_phase(PG8_LAS unsigned char* lds, const Gemm g, const Sched& S, const Epi& E, int tid_in, const int* rowsrc = nullptr, PG8_LAS int* idx_lds = nullptr) {
;     ...
;             PG8_LDB(B0, 0, 0); PG8_LDB(B1, 0, 1); PG8_SCHED; PG8_LDA(At, 0, 0); PG8_STAGE(PG8_SA(1, 1), a1 + hstepA, PG8_OA(1));
;             PG8_WAIT_V(8); PG8_WAIT_L(0); PG8_BAR; PG8_MMA(0, 0, At, B0); PG8_MMA(0, 1, At, B1); PG8_BAR; PG8_SCHED;
;             PG8_LDA(At, 0, 1); PG8_STAGE(PG8_SB(0, 0), b2, voffB); PG8_STAGE(PG8_SB(0, 1), b2 + hstep, voffB); PG8_STAGE(PG8_SA(0, 0), a2, PG8_OS(0));
;             PG8_WAIT_V(8); PG8_WAIT_L(0); PG8_BAR; PG8_MMA(1, 0, At, B0); PG8_MMA(1, 1, At, B1); PG8_BAR; PG8_SCHED;
;             PG8_LDB(B0, 1, 0); PG8_LDB(B1, 1, 1); PG8_SCHED; PG8_LDA(At, 1, 0); PG8_STAGE(PG8_SA(0, 1), a2 + hstepA, PG8_OS(1));
;             PG8_WAIT_V(8); PG8_WAIT_L(0); PG8_BAR; PG8_MMA(0, 0, At, B0); PG8_MMA(0, 1, At, B1); PG8_BAR; PG8_SCHED;
;             PG8_LDA(At, 1, 1); PG8_STAGE(PG8_SB(1, 0), b3, voffB); PG8_STAGE(PG8_SB(1, 1), b3 + hstep, voffB); PG8_STAGE(PG8_SA(1, 0), a3, PG8_OS(0));
;             PG8_WAIT_V(8); PG8_WAIT_L(0); PG8_BAR; PG8_MMA(1, 0, At, B0); PG8_MMA(1, 1, At, B1); PG8_BAR; PG8_SCHED;
	s_setprio 1
	s_waitcnt lgkmcnt(0)
	v_mfma_f32_16x16x32_bf16 v[46:49], v[154:157], v[192:195], v[46:49]
	v_mfma_f32_16x16x32_bf16 v[38:41], v[140:143], v[200:203], v[38:41]
	v_mfma_f32_16x16x32_bf16 v[30:33], v[154:157], v[200:203], v[30:33]
	v_mfma_f32_16x16x32_bf16 v[22:25], v[140:143], v[208:211], v[22:25]
	v_mfma_f32_16x16x32_bf16 v[14:17], v[154:157], v[208:211], v[14:17]
	v_mfma_f32_16x16x32_bf16 v[62:65], v[150:153], v[188:191], v[62:65]
	v_mfma_f32_16x16x32_bf16 v[58:61], v[158:161], v[188:191], v[58:61]
	v_mfma_f32_16x16x32_bf16 v[54:57], v[150:153], v[196:199], v[54:57]
	v_mfma_f32_16x16x32_bf16 v[46:49], v[158:161], v[196:199], v[46:49]
	v_mfma_f32_16x16x32_bf16 v[38:41], v[150:153], v[204:207], v[38:41]
	v_mfma_f32_16x16x32_bf16 v[30:33], v[158:161], v[204:207], v[30:33]
	v_mfma_f32_16x16x32_bf16 v[22:25], v[150:153], v[212:215], v[22:25]
	v_mfma_f32_16x16x32_bf16 v[14:17], v[158:161], v[212:215], v[14:17]
	s_setprio 0
	s_setprio 1
	v_mfma_f32_16x16x32_bf16 v[50:53], v[162:165], v[184:187], v[50:53]
	v_mfma_f32_16x16x32_bf16 v[42:45], v[170:173], v[184:187], v[42:45]
	v_mfma_f32_16x16x32_bf16 v[34:37], v[162:165], v[192:195], v[34:37]
	v_mfma_f32_16x16x32_bf16 v[26:29], v[170:173], v[192:195], v[26:29]
	v_mfma_f32_16x16x32_bf16 v[18:21], v[162:165], v[200:203], v[18:21]
	v_mfma_f32_16x16x32_bf16 v[10:13], v[170:173], v[200:203], v[10:13]
	v_mfma_f32_16x16x32_bf16 v[6:9], v[162:165], v[208:211], v[6:9]
	v_mfma_f32_16x16x32_bf16 v[2:5], v[170:173], v[208:211], v[2:5]
	v_mfma_f32_16x16x32_bf16 v[50:53], v[166:169], v[188:191], v[50:53]
	v_mfma_f32_16x16x32_bf16 v[42:45], v[174:177], v[188:191], v[42:45]
	v_mfma_f32_16x16x32_bf16 v[34:37], v[166:169], v[196:199], v[34:37]
	v_mfma_f32_16x16x32_bf16 v[26:29], v[174:177], v[196:199], v[26:29]
	v_mfma_f32_16x16x32_bf16 v[18:21], v[166:169], v[204:207], v[18:21]
	v_mfma_f32_16x16x32_bf16 v[10:13], v[174:177], v[204:207], v[10:13]
	v_mfma_f32_16x16x32_bf16 v[6:9], v[166:169], v[212:215], v[6:9]
	v_mfma_f32_16x16x32_bf16 v[2:5], v[174:177], v[212:215], v[2:5]
	s_setprio 0
	s_barrier
	s_add_i32 s52, 0, 0x18000
	s_add_i32 s53, 0, 0x1c000
	v_add_u32_e32 v158, s52, v145
	v_add_u32_e32 v174, s53, v145
	ds_read_b128 v[140:143], v158
	ds_read_b128 v[150:153], v158 offset:1024
	ds_read_b128 v[154:157], v158 offset:2048
	ds_read_b128 v[158:161], v158 offset:3072
	ds_read_b128 v[162:165], v174
	ds_read_b128 v[166:169], v174 offset:1024
	ds_read_b128 v[170:173], v174 offset:2048
	ds_read_b128 v[174:177], v174 offset:3072
	s_add_u32 s24, s24, 0x40000
	s_addc_u32 s25, s25, 0
	s_mov_b32 m0, s35
	v_lshl_add_u64 v[218:219], s[24:25], 0, v[134:135]
	ds_read_b128 v[184:187], v149 offset:32768
	ds_read_b128 v[188:191], v149 offset:33792
	ds_read_b128 v[192:195], v149 offset:34816
	ds_read_b128 v[196:199], v149 offset:35840
	ds_read_b128 v[200:203], v149 offset:36864
	ds_read_b128 v[204:207], v149 offset:37888
	ds_read_b128 v[208:211], v149 offset:38912
	ds_read_b128 v[212:215], v149 offset:39936
	global_load_lds_dwordx4 v[218:219], off
	v_lshl_add_u64 v[218:219], s[24:25], 0, v[132:133]
	s_mov_b32 m0, s36
	s_nop 0
	global_load_lds_dwordx4 v[218:219], off
	s_waitcnt vmcnt(8)
	s_waitcnt lgkmcnt(0)
	v_mfma_f32_16x16x32_bf16 v[126:129], v[140:143], v[184:187], v[126:129]
	v_mfma_f32_16x16x32_bf16 v[122:125], v[154:157], v[184:187], v[122:125]
	v_mfma_f32_16x16x32_bf16 v[118:121], v[140:143], v[192:195], v[118:121]
	s_barrier
	s_setprio 1
	s_waitcnt lgkmcnt(0)
	v_mfma_f32_16x16x32_bf16 v[110:113], v[154:157], v[192:195], v[110:113]
	v_mfma_f32_16x16x32_bf16 v[102:105], v[140:143], v[200:203], v[102:105]
	v_mfma_f32_16x16x32_bf16 v[94:97], v[154:157], v[200:203], v[94:97]
	v_mfma_f32_16x16x32_bf16 v[86:89], v[140:143], v[208:211], v[86:89]
	v_mfma_f32_16x16x32_bf16 v[78:81], v[154:157], v[208:211], v[78:81]
	v_mfma_f32_16x16x32_bf16 v[126:129], v[150:153], v[188:191], v[126:129]
	v_mfma_f32_16x16x32_bf16 v[122:125], v[158:161], v[188:191], v[122:125]
	v_mfma_f32_16x16x32_bf16 v[118:121], v[150:153], v[196:199], v[118:121]
	v_mfma_f32_16x16x32_bf16 v[110:113], v[158:161], v[196:199], v[110:113]
	v_mfma_f32_16x16x32_bf16 v[102:105], v[150:153], v[204:207], v[102:105]
	v_mfma_f32_16x16x32_bf16 v[94:97], v[158:161], v[204:207], v[94:97]
	v_mfma_f32_16x16x32_bf16 v[86:89], v[150:153], v[212:215], v[86:89]
	v_mfma_f32_16x16x32_bf16 v[78:81], v[158:161], v[212:215], v[78:81]
	s_setprio 0
	s_setprio 1
	v_mfma_f32_16x16x32_bf16 v[114:117], v[162:165], v[184:187], v[114:117]
	v_mfma_f32_16x16x32_bf16 v[106:109], v[170:173], v[184:187], v[106:109]
	v_mfma_f32_16x16x32_bf16 v[98:101], v[162:165], v[192:195], v[98:101]
	v_mfma_f32_16x16x32_bf16 v[90:93], v[170:173], v[192:195], v[90:93]
	v_mfma_f32_16x16x32_bf16 v[82:85], v[162:165], v[200:203], v[82:85]
	v_mfma_f32_16x16x32_bf16 v[74:77], v[170:173], v[200:203], v[74:77]
	v_mfma_f32_16x16x32_bf16 v[70:73], v[162:165], v[208:211], v[70:73]
	v_mfma_f32_16x16x32_bf16 v[66:69], v[170:173], v[208:211], v[66:69]
	v_mfma_f32_16x16x32_bf16 v[114:117], v[166:169], v[188:191], v[114:117]
	v_mfma_f32_16x16x32_bf16 v[106:109], v[174:177], v[188:191], v[106:109]
	v_mfma_f32_16x16x32_bf16 v[98:101], v[166:169], v[196:199], v[98:101]
	v_mfma_f32_16x16x32_bf16 v[90:93], v[174:177], v[196:199], v[90:93]
	v_mfma_f32_16x16x32_bf16 v[82:85], v[166:169], v[204:207], v[82:85]
	v_mfma_f32_16x16x32_bf16 v[74:77], v[174:177], v[204:207], v[74:77]
	v_mfma_f32_16x16x32_bf16 v[70:73], v[166:169], v[212:215], v[70:73]
	v_mfma_f32_16x16x32_bf16 v[66:69], v[174:177], v[212:215], v[66:69]
	s_setprio 0
	s_barrier
; #define PG8_STAGE(bufoff, gbase, voff) do { _Pragma("unroll") for (int _i = 0; _i < 2; ++_i) \
;         __builtin_amdgcn_global_load_lds((const unsigned*)((const char*)(gbase) + (voff)[_i]), (PG8_LAS unsigned*)(lds + (bufoff) + ldsw + _i * 8192), 16, 0, 0); } while (0)
; #define PG8_LDA(dst, b, h) do { _Pragma("unroll") for (int m = 0; m < 4; ++m) _Pragma("unroll") for (int k = 0; k < 2; ++k) dst[m][k] = *(const PG8_LAS bf16x8*)(lds + PG8_SA(b, h) + aoff + m * 2048 + k * 1024); } while (0)
; #define PG8_LDB(dst, b, h) do { _Pragma("unroll") for (int n = 0; n < 2; ++n) _Pragma("unroll") for (int k = 0; k < 2; ++k) dst[n][k] = *(const PG8_LAS bf16x8*)(lds + PG8_SB(b, h) + boff + n * 2048 + k * 1024); } while (0)
; #define PG8_WAIT_V(n) asm volatile("s_waitcnt vmcnt(" #n ")" ::: "memory")
; #define PG8_WAIT_L(n) asm volatile("s_waitcnt lgkmcnt(" #n ")" ::: "memory")
; #define PG8_BAR __builtin_amdgcn_s_barrier()
; #define PG8_SCHED __builtin_amdgcn_sched_barrier(0)
; template <class Epi, class Sched, bool ALIGN_EPI = false, bool SP2 = false, bool GATHER = false>
; __device__ __forceinline__ void gemm_phase(PG8_LAS unsigned char* lds, const Gemm g, const Sched& S, const Epi& E, int tid_in, const int* rowsrc = nullptr, PG8_LAS int* idx_lds = nullptr) {
;     ...
;             PG8_LDB(B0, 0, 0); PG8_LDB(B1, 0, 1); PG8_SCHED; PG8_LDA(At, 0, 0); PG8_STAGE(PG8_SA(1, 1), a1 + hstepA, PG8_OA(1));
;             PG8_WAIT_V(8); PG8_WAIT_L(0); PG8_BAR; PG8_MMA(0, 0, At, B0); PG8_MMA(0, 1, At, B1); PG8_BAR; PG8_SCHED;
;             PG8_LDA(At, 0, 1); PG8_STAGE(PG8_SB(0, 0), b2, voffB); PG8_STAGE(PG8_SB(0, 1), b2 + hstep, voffB); PG8_STAGE(PG8_SA(0, 0), a2, PG8_OS(0));
;             PG8_WAIT_V(8); PG8_WAIT_L(0); PG8_BAR; PG8_MMA(1, 0, At, B0); PG8_MMA(1, 1, At, B1); PG8_BAR; PG8_SCHED;
;             PG8_LDB(B0, 1, 0); PG8_LDB(B1, 1, 1); PG8_SCHED; PG8_LDA(At, 1, 0); PG8_STAGE(PG8_SA(0, 1), a2 + hstepA, PG8_OS(1));
;             PG8_WAIT_V(8); PG8_WAIT_L(0); PG8_BAR; PG8_MMA(0, 0, At, B0); PG8_MMA(0, 1, At, B1); PG8_BAR; PG8_SCHED;
;             PG8_LDA(At, 1, 1); PG8_STAGE(PG8_SB(1, 0), b3, voffB); PG8_STAGE(PG8_SB(1, 1), b3 + hstep, voffB); PG8_STAGE(PG8_SA(1, 0), a3, PG8_OS(0));
;             PG8_WAIT_V(8); PG8_WAIT_L(0); PG8_BAR; PG8_MMA(1, 0, At, B0); PG8_MMA(1, 1, At, B1); PG8_BAR; PG8_SCHED;
	s_add_i32 s24, s52, s30
	v_lshl_add_u64 v[178:179], v[178:179], 0, s[10:11]
	s_mov_b32 m0, s24
	ds_read_b128 v[184:187], v149 offset:49152
	ds_read_b128 v[188:191], v149 offset:50176
	ds_read_b128 v[192:195], v149 offset:51200
	ds_read_b128 v[196:199], v149 offset:52224
	ds_read_b128 v[200:203], v149 offset:53248
	ds_read_b128 v[204:207], v149 offset:54272
	ds_read_b128 v[208:211], v149 offset:55296
	ds_read_b128 v[212:215], v149 offset:56320
	global_load_lds_dwordx4 v[178:179], off
	s_add_i32 m0, s24, 0x2000
	s_add_u32 s22, s22, 0x40080
	v_lshl_add_u64 v[178:179], v[180:181], 0, s[10:11]
	s_addc_u32 s23, s23, 0
	s_add_i32 s24, s53, s30
	global_load_lds_dwordx4 v[178:179], off
	v_lshl_add_u64 v[178:179], s[22:23], 0, v[0:1]
	s_mov_b32 m0, s24
	s_nop 0
	global_load_lds_dwordx4 v[178:179], off
	v_lshl_add_u64 v[178:179], s[22:23], 0, v[130:131]
	s_add_i32 m0, s24, 0x2000
	s_nop 0
	global_load_lds_dwordx4 v[178:179], off
	v_lshl_add_u64 v[178:179], v[182:183], 0, s[10:11]
	s_mov_b32 m0, s38
	s_nop 0
	global_load_lds_dwordx4 v[178:179], off
	v_lshl_add_u64 v[178:179], v[216:217], 0, s[10:11]
	s_mov_b32 m0, s39
	s_nop 0
	global_load_lds_dwordx4 v[178:179], off
	s_waitcnt vmcnt(8)
	s_waitcnt lgkmcnt(0)
	v_mfma_f32_16x16x32_bf16 v[62:65], v[140:143], v[184:187], v[62:65]
	v_mfma_f32_16x16x32_bf16 v[58:61], v[154:157], v[184:187], v[58:61]
	v_mfma_f32_16x16x32_bf16 v[54:57], v[140:143], v[192:195], v[54:57]
	s_barrier
	s_setprio 1
	s_waitcnt lgkmcnt(0)
	v_mfma_f32_16x16x32_bf16 v[46:49], v[154:157], v[192:195], v[46:49]
	v_mfma_f32_16x16x32_bf16 v[38:41], v[140:143], v[200:203], v[38:41]
	v_mfma_f32_16x16x32_bf16 v[30:33], v[154:157], v[200:203], v[30:33]
	v_mfma_f32_16x16x32_bf16 v[22:25], v[140:143], v[208:211], v[22:25]
	v_mfma_f32_16x16x32_bf16 v[14:17], v[154:157], v[208:211], v[14:17]
	v_mfma_f32_16x16x32_bf16 v[62:65], v[150:153], v[188:191], v[62:65]
	v_mfma_f32_16x16x32_bf16 v[58:61], v[158:161], v[188:191], v[58:61]
	v_mfma_f32_16x16x32_bf16 v[54:57], v[150:153], v[196:199], v[54:57]
	v_mfma_f32_16x16x32_bf16 v[46:49], v[158:161], v[196:199], v[46:49]
	v_mfma_f32_16x16x32_bf16 v[38:41], v[150:153], v[204:207], v[38:41]
	v_mfma_f32_16x16x32_bf16 v[30:33], v[158:161], v[204:207], v[30:33]
	v_mfma_f32_16x16x32_bf16 v[22:25], v[150:153], v[212:215], v[22:25]
	v_mfma_f32_16x16x32_bf16 v[14:17], v[158:161], v[212:215], v[14:17]
	s_setprio 0
	s_setprio 1
	v_mfma_f32_16x16x32_bf16 v[50:53], v[162:165], v[184:187], v[50:53]
	v_mfma_f32_16x16x32_bf16 v[42:45], v[170:173], v[184:187], v[42:45]
	v_mfma_f32_16x16x32_bf16 v[34:37], v[162:165], v[192:195], v[34:37]
	v_mfma_f32_16x16x32_bf16 v[26:29], v[170:173], v[192:195], v[26:29]
	v_mfma_f32_16x16x32_bf16 v[18:21], v[162:165], v[200:203], v[18:21]
	v_mfma_f32_16x16x32_bf16 v[10:13], v[170:173], v[200:203], v[10:13]
	v_mfma_f32_16x16x32_bf16 v[6:9], v[162:165], v[208:211], v[6:9]
	v_mfma_f32_16x16x32_bf16 v[2:5], v[170:173], v[208:211], v[2:5]
	v_mfma_f32_16x16x32_bf16 v[50:53], v[166:169], v[188:191], v[50:53]
	v_mfma_f32_16x16x32_bf16 v[42:45], v[174:177], v[188:191], v[42:45]
	v_mfma_f32_16x16x32_bf16 v[34:37], v[166:169], v[196:199], v[34:37]
	v_mfma_f32_16x16x32_bf16 v[26:29], v[174:177], v[196:199], v[26:29]
	v_mfma_f32_16x16x32_bf16 v[18:21], v[166:169], v[204:207], v[18:21]
	v_mfma_f32_16x16x32_bf16 v[10:13], v[174:177], v[204:207], v[10:13]
	v_mfma_f32_16x16x32_bf16 v[6:9], v[166:169], v[212:215], v[6:9]
	v_mfma_f32_16x16x32_bf16 v[2:5], v[174:177], v[212:215], v[2:5]
	s_setprio 0
	s_barrier
	s_add_i32 s51, s51, 2
	s_add_u32 s20, s20, 0x100
	s_addc_u32 s21, s21, 0
	s_add_u32 s49, s49, 0x100
	s_addc_u32 s50, s50, 0
	s_cmp_gt_u32 s51, 13
	s_cbranch_scc0 .LBB0_692
	s_and_b64 vcc, exec, s[8:9]
	s_cbranch_vccz .LBB0_695
	s_barrier

; #define LAS __attribute__((address_space(3)))
; __device__ __forceinline__ int v_rd_base(int lane) { return ((lane & 3) << 3) | (((lane >> 2) & 3) << 6) | (((lane >> 4) & 1) << 5) | (((lane >> 5) & 1) << 8); }
; #define DMA_WAIT(last) do { if (last) asm volatile("s_waitcnt vmcnt(0)" ::: "memory"); else asm volatile("s_waitcnt vmcnt(%0)" :: "n"(NPW) : "memory"); } while (0)
;   template <int NQ> __device__ __forceinline__ void load(bf16x8 (&qr)[NQ], int r, int hi) const {
;     const bf16* src = q + (long)r * ldq + hi * 8;
; #pragma unroll
;     for (int d0 = 0; d0 < NQ; ++d0) qr[d0] = *reinterpret_cast<const bf16x8*>(src + d0 * 16);
; template <int DK, int DV, bool OFF, class QLoader> ...
;     ...
;   QL.load(qr, wid * QBLK + r32, hi);
;   asm volatile("s_waitcnt vmcnt(0)" ::: "memory");
;   unsigned koff[KPW], voff[VPW];
; #pragma unroll
;   for (int i = 0; i < (DK == 64 ? 1 : KPW); ++i) { const int row = (wid * KPW + i) * 4 + (lane >> 4); int c = (lane & 15) ^ (row & 7); c = (c < DK / 8) ? c : (c & 7); koff[i] = (unsigned)((row * ldk) * 2 + c * 16); }
; #pragma unroll
;   for (int i = 0; i < 1; ++i) { const int sidx = (wid * VPW + i) * 2 + (lane >> 5), kg = sidx / ND, st = sidx % ND, kk = kg * 8 + ((lane & 31) >> 2);
;     const int k = (kk & ~0xC) | ((kk & 4) << 1) | ((kk & 8) >> 1), c = st * 32 + (lane & 3) * 8; voff[i] = (unsigned)((k * ldv + c) * 2); }
;   const int vb0 = (int)(uintptr_t)V_lds + v_rd_base(lane);
;   LAS unsigned* const ldsK = (LAS unsigned*)(LAS char*)K_lds + (wid * KPW) * 256; LAS unsigned* const ldsV = (LAS unsigned*)(LAS char*)V_lds + (wid * VPW) * 256;
;     ...
;   f32x16 pA0, pA1, pB0, pB1; bf16x8 pa0, pa1, pa2, pa3; const int NT = nkeys / KVBLK;
;   DMA_TILE(0, 0); DMA_TILE(1, 1); DMA_WAIT(false); __syncthreads(); if (2 < NT) DMA_TILE(2, 2);
.LBB0_838:
	s_and_b64 s[16:17], s[14:15], exec
	s_cselect_b32 s76, s12, s2
	s_ashr_i32 s2, s76, 4
	s_and_b32 s22, s76, 15
	s_mul_i32 s78, s76, 0x88000
	s_mul_hi_i32 s77, s76, 0x88000
	s_add_u32 s16, s65, s78
	s_addc_u32 s17, s66, s77
	s_lshl_b32 s4, s2, 8
	s_add_i32 s23, s4, 0x8000
	s_mul_i32 s80, s23, 0x1800
	s_mul_hi_i32 s79, s23, 0x1800
	s_add_u32 s4, s67, s80
	s_addc_u32 s12, s68, s79
	s_lshl_b32 s13, s76, 7
	s_and_b32 s13, s13, 0x700
	s_add_u32 s4, s4, s13
	s_addc_u32 s12, s12, 0
	s_add_u32 s18, s4, 0x1000
	s_addc_u32 s19, s12, 0
	s_lshl_b32 s12, s2, 12
	s_mul_i32 s2, s2, 0x1800000
	s_mul_hi_i32 s4, s12, 0x1800
	s_add_u32 s24, s67, s2
	s_addc_u32 s25, s68, s4
	s_add_u32 s13, s24, s13
	s_addc_u32 s24, s25, 0
	s_add_u32 s74, s13, 0x1000
	s_addc_u32 s75, s24, 0
	s_lshl_b32 s5, s5, 8
	s_or_b32 s5, s12, s5
	s_and_b64 s[12:13], s[14:15], exec
	s_cselect_b32 s12, s5, s23
	s_ashr_i32 s13, s12, 31
	s_lshl_b64 s[12:13], s[12:13], 12
	s_add_u32 s5, s69, s12
	s_addc_u32 s13, s70, s13
	s_lshl_b32 s12, s22, 8
	s_add_u32 s12, s5, s12
	s_addc_u32 s13, s13, 0
	s_andn2_b64 vcc, exec, s[34:35]
	s_mov_b64 s[22:23], -1
	s_cbranch_vccnz .LBB0_882
	v_mov_b32_e32 v25, v159
	v_mov_b32_e32 v33, v1
	v_readfirstlane_b32 s23, v25
	s_ashr_i32 s26, s23, 6
	v_and_b32_e32 v10, 31, v25
	s_lshl_b32 s22, s26, 5
	v_or_b32_e32 v2, s22, v10
	v_ashrrev_i32_e32 v3, 31, v2
	v_bfe_u32 v4, v25, 5, 1
	v_lshlrev_b64 v[2:3], 7, v[2:3]
	v_lshl_add_u64 v[2:3], s[20:21], 0, v[2:3]
	v_lshlrev_b32_e32 v32, 4, v4
	v_lshl_add_u64 v[2:3], v[2:3], 0, v[32:33]
	global_load_dwordx4 v[114:117], v[2:3], off
	global_load_dwordx4 v[118:121], v[2:3], off offset:32
	global_load_dwordx4 v[122:125], v[2:3], off offset:64
	global_load_dwordx4 v[126:129], v[2:3], off offset:96
	v_bfe_u32 v0, v25, 4, 2
	s_bfe_i32 s24, s26, 0x1001d
	v_and_b32_e32 v2, 15, v25
	v_bitop3_b32 v3, v0, v25, 15 bitop3:0x78
	v_lshl_or_b32 v20, s26, 2, v4
	s_lshr_b32 s24, s24, 30
	v_lshlrev_b32_e32 v3, 4, v3
	v_cmp_gt_u32_e32 vcc, 8, v2
	v_add_u32_e32 v2, s24, v20
	v_and_b32_e32 v5, 0x70, v3
	v_ashrrev_i32_e32 v21, 2, v2
	v_cndmask_b32_e32 v19, v5, v3, vcc
	v_lshlrev_b32_e32 v4, 3, v21
	v_bfe_u32 v5, v25, 2, 3
	v_bitop3_b32 v22, v4, -13, v5 bitop3:0xc8
	v_lshrrev_b32_e32 v4, 1, v25
	s_lshl_b32 s5, s26, 10
	v_lshlrev_b32_e32 v18, 7, v0
	v_and_b32_e32 v23, 8, v4
	v_and_b32_e32 v26, 4, v2
	v_or_b32_e32 v0, s5, v18
	v_and_b32_e32 v3, 0x3fffffc, v2
	v_or3_b32 v2, v23, v22, v26
	s_movk_i32 s24, 0xc00
	v_add_u32_e32 v0, v0, v19
	v_lshlrev_b32_e32 v4, 3, v25
	v_mul_lo_u32 v2, v2, s24
	s_add_i32 s27, 0, 0x10000
	s_lshl_b32 s24, s26, 11
	v_sub_u32_e32 v3, v20, v3
	v_and_b32_e32 v24, 24, v4
	s_add_i32 s81, s27, s24
	v_xor_b32_e32 v150, 64, v0
	v_mov_b32_e32 v151, v1
	v_lshl_or_b32 v3, v3, 5, v24
	s_add_i32 s82, s24, 0
	s_mov_b32 m0, s81
	v_lshl_add_u64 v[4:5], s[16:17], 0, v[150:151]
	s_mov_b64 s[24:25], 0x200
	s_add_i32 s83, s81, 0x400
	v_add_lshl_u32 v148, v3, v2, 1
	global_load_lds_dwordx4 v0, s[16:17]
	v_lshl_add_u64 v[6:7], v[4:5], 0, s[24:25]
	s_mov_b32 m0, s83
	v_mov_b32_e32 v149, v1
	global_load_lds_dwordx4 v[6:7], off
	v_lshl_add_u64 v[6:7], s[18:19], 0, v[148:149]
	s_mov_b32 m0, s82
	s_add_i32 s84, s82, 0x400
	v_lshl_add_u64 v[2:3], s[16:17], 0, v[0:1]
	global_load_lds_dwordx4 v148, s[18:19]
	v_lshl_add_u64 v[8:9], v[6:7], 0, s[10:11]
	s_mov_b32 m0, s84
	s_mov_b64 s[24:25], 0x2000
	s_add_i32 s85, s81, 0x4000
	global_load_lds_dwordx4 v[8:9], off
	v_lshl_add_u64 v[8:9], v[2:3], 0, s[24:25]
	s_mov_b32 m0, s85
	s_mov_b64 s[24:25], 0x2200
	s_add_i32 s86, s81, 0x4400
	global_load_lds_dwordx4 v[8:9], off
	v_lshl_add_u64 v[8:9], v[4:5], 0, s[24:25]
	s_mov_b32 m0, s86
	s_mov_b64 s[24:25], 0x60000
	s_add_i32 s87, s82, 0x4000
	global_load_lds_dwordx4 v[8:9], off
	v_lshl_add_u64 v[8:9], v[6:7], 0, s[24:25]
	s_mov_b32 m0, s87
	s_mov_b64 s[24:25], 0x60080
	s_add_i32 s88, s82, 0x4400
	global_load_lds_dwordx4 v[8:9], off
	v_lshl_add_u64 v[8:9], v[6:7], 0, s[24:25]
	s_mov_b32 m0, s88
	s_mov_b64 s[24:25], 0x4000
	s_add_i32 s89, s81, 0x8000
	global_load_lds_dwordx4 v[8:9], off
	v_lshl_add_u64 v[2:3], v[2:3], 0, s[24:25]
	s_mov_b32 m0, s89
	s_mov_b64 s[24:25], 0x4200
	s_add_i32 s90, s81, 0x8400
	s_waitcnt vmcnt(4)
	s_waitcnt vmcnt(0) lgkmcnt(0)
	s_barrier
	global_load_lds_dwordx4 v[2:3], off
	v_lshl_add_u64 v[2:3], v[4:5], 0, s[24:25]
	s_mov_b32 m0, s90
	s_mov_b64 s[24:25], 0xc0000
	s_add_i32 s91, s82, 0x8000
	global_load_lds_dwordx4 v[2:3], off
	v_lshl_add_u64 v[2:3], v[6:7], 0, s[24:25]
	s_mov_b32 m0, s91
	s_mov_b64 s[24:25], 0xc0080
	s_add_i32 s92, s82, 0x8400
	global_load_lds_dwordx4 v[2:3], off
	v_lshl_add_u64 v[2:3], v[6:7], 0, s[24:25]
	s_mov_b32 m0, s92
	v_lshlrev_b32_e32 v27, 8, v10
	global_load_lds_dwordx4 v[2:3], off
	v_lshlrev_b32_e32 v2, 4, v25
	v_and_b32_e32 v33, 0x70, v2
	v_bitop3_b32 v161, v32, v27, v33 bitop3:0xde
	v_add_u32_e32 v162, s27, v161
	ds_read_b128 v[2:5], v162
	ds_read_b128 v[28:31], v162 offset:8192
	s_waitcnt lgkmcnt(0)
	v_mfma_f32_32x32x16_bf16 v[66:81], v[28:31], v[114:117], 0
	v_or_b32_e32 v28, 32, v32
	v_bitop3_b32 v163, v28, v27, v33 bitop3:0xde
	v_add_u32_e32 v164, s27, v163
	ds_read_b128 v[28:31], v164
	s_cmp_lt_i32 s26, 4
	v_mfma_f32_32x32x16_bf16 v[2:17], v[2:5], v[114:117], 0
	s_waitcnt lgkmcnt(0)
	v_mfma_f32_32x32x16_bf16 v[2:17], v[28:31], v[118:121], v[2:17]
	ds_read_b128 v[28:31], v164 offset:8192
	s_waitcnt lgkmcnt(0)
	v_mfma_f32_32x32x16_bf16 v[66:81], v[28:31], v[118:121], v[66:81]
	v_or_b32_e32 v28, 64, v32
	v_bitop3_b32 v165, v28, v27, v33 bitop3:0xde
	v_add_u32_e32 v166, s27, v165
	ds_read_b128 v[28:31], v166
	s_waitcnt lgkmcnt(0)
	v_mfma_f32_32x32x16_bf16 v[2:17], v[28:31], v[122:125], v[2:17]
	ds_read_b128 v[28:31], v166 offset:8192
	s_waitcnt lgkmcnt(0)
	v_mfma_f32_32x32x16_bf16 v[66:81], v[28:31], v[122:125], v[66:81]
	v_or_b32_e32 v28, 0x60, v32
	v_bitop3_b32 v167, v28, v27, v33 bitop3:0xde
	v_add_u32_e32 v168, s27, v167
	ds_read_b128 v[28:31], v168
	s_waitcnt lgkmcnt(0)
	v_mfma_f32_32x32x16_bf16 v[2:17], v[28:31], v[126:129], v[2:17]
	ds_read_b128 v[28:31], v168 offset:8192
	s_waitcnt lgkmcnt(0)
	v_mfma_f32_32x32x16_bf16 v[66:81], v[28:31], v[126:129], v[66:81]
	s_cbranch_scc1 .LBB0_841
	s_setprio 1

; #define PG8_STAGE(bufoff, gbase, voff) do { _Pragma("unroll") for (int _i = 0; _i < 2; ++_i) \
;         __builtin_amdgcn_global_load_lds((const unsigned*)((const char*)(gbase) + (voff)[_i]), (PG8_LAS unsigned*)(lds + (bufoff) + ldsw + _i * 8192), 16, 0, 0); } while (0)
; #define PG8_LDA(dst, b, h) do { _Pragma("unroll") for (int m = 0; m < 4; ++m) _Pragma("unroll") for (int k = 0; k < 2; ++k) dst[m][k] = *(const PG8_LAS bf16x8*)(lds + PG8_SA(b, h) + aoff + m * 2048 + k * 1024); } while (0)
; #define PG8_LDB(dst, b, h) do { _Pragma("unroll") for (int n = 0; n < 2; ++n) _Pragma("unroll") for (int k = 0; k < 2; ++k) dst[n][k] = *(const PG8_LAS bf16x8*)(lds + PG8_SB(b, h) + boff + n * 2048 + k * 1024); } while (0)
; #define PG8_WAIT_V(n) asm volatile("s_waitcnt vmcnt(" #n ")" ::: "memory")
; #define PG8_WAIT_L(n) asm volatile("s_waitcnt lgkmcnt(" #n ")" ::: "memory")
; #define PG8_BAR __builtin_amdgcn_s_barrier()
; #define PG8_SCHED __builtin_amdgcn_sched_barrier(0)
; template <class Epi, class Sched, bool ALIGN_EPI = false, bool SP2 = false, bool GATHER = false>
; __device__ __forceinline__ void gemm_phase(PG8_LAS unsigned char* lds, const Gemm g, const Sched& S, const Epi& E, int tid_in, const int* rowsrc = nullptr, PG8_LAS int* idx_lds = nullptr) {
;     ...
;             PG8_LDB(B0, 0, 0); PG8_LDB(B1, 0, 1); PG8_SCHED; PG8_LDA(At, 0, 0); PG8_STAGE(PG8_SA(1, 1), a1 + hstepA, PG8_OA(1));
;             PG8_WAIT_V(8); PG8_WAIT_L(0); PG8_BAR; PG8_MMA(0, 0, At, B0); PG8_MMA(0, 1, At, B1); PG8_BAR; PG8_SCHED;
;             PG8_LDA(At, 0, 1); PG8_STAGE(PG8_SB(0, 0), b2, voffB); PG8_STAGE(PG8_SB(0, 1), b2 + hstep, voffB); PG8_STAGE(PG8_SA(0, 0), a2, PG8_OS(0));
;             PG8_WAIT_V(8); PG8_WAIT_L(0); PG8_BAR; PG8_MMA(1, 0, At, B0); PG8_MMA(1, 1, At, B1); PG8_BAR; PG8_SCHED;
;             PG8_LDB(B0, 1, 0); PG8_LDB(B1, 1, 1); PG8_SCHED; PG8_LDA(At, 1, 0); PG8_STAGE(PG8_SA(0, 1), a2 + hstepA, PG8_OS(1));
;             PG8_WAIT_V(8); PG8_WAIT_L(0); PG8_BAR; PG8_MMA(0, 0, At, B0); PG8_MMA(0, 1, At, B1); PG8_BAR; PG8_SCHED;
;             PG8_LDA(At, 1, 1); PG8_STAGE(PG8_SB(1, 0), b3, voffB); PG8_STAGE(PG8_SB(1, 1), b3 + hstep, voffB); PG8_STAGE(PG8_SA(1, 0), a3, PG8_OS(0));
;             PG8_WAIT_V(8); PG8_WAIT_L(0); PG8_BAR; PG8_MMA(1, 0, At, B0); PG8_MMA(1, 1, At, B1); PG8_BAR; PG8_SCHED;
.LBB0_1101:
	s_add_u32 s22, s20, 0xfffc0080
	s_addc_u32 s23, s21, -1
	s_add_i32 s58, 0, 0x10000
	s_cmp_eq_u32 s57, 12
	s_cselect_b32 s25, s9, s23
	s_cselect_b32 s24, s17, s22
	s_cselect_b32 s23, s7, s56
	s_cselect_b32 s22, s19, s55
	s_add_i32 s60, 0, 0x14000
	v_add_u32_e32 v142, s58, v184
	v_add_u32_e32 v182, s60, v184
	ds_read_b128 v[122:125], v142
	ds_read_b128 v[126:129], v142 offset:1024
	ds_read_b128 v[134:137], v142 offset:2048
	ds_read_b128 v[142:145], v142 offset:3072
	ds_read_b128 v[174:177], v182
	ds_read_b128 v[178:181], v182 offset:1024
	ds_read_b128 v[188:191], v182 offset:2048
	ds_read_b128 v[192:195], v182 offset:3072
	v_lshl_add_u64 v[182:183], s[20:21], 0, v[170:171]
	s_add_i32 m0, s39, 0xc000
	ds_read_b128 v[196:199], v186
	ds_read_b128 v[200:203], v186 offset:1024
	ds_read_b128 v[204:207], v186 offset:2048
	ds_read_b128 v[208:211], v186 offset:3072
	ds_read_b128 v[212:215], v186 offset:4096
	ds_read_b128 v[216:219], v186 offset:5120
	ds_read_b128 v[220:223], v186 offset:6144
	ds_read_b128 v[224:227], v186 offset:7168
	global_load_lds_dwordx4 v[182:183], off
	v_lshl_add_u64 v[182:183], s[20:21], 0, v[172:173]
	s_add_i32 m0, s39, 0xe000
	s_nop 0
	global_load_lds_dwordx4 v[182:183], off
	s_waitcnt vmcnt(8)
	s_waitcnt lgkmcnt(0)
	v_mfma_f32_16x16x32_bf16 v[138:141], v[122:125], v[196:199], v[138:141]
	v_mfma_f32_16x16x32_bf16 v[130:133], v[134:137], v[196:199], v[130:133]
	v_mfma_f32_16x16x32_bf16 v[118:121], v[122:125], v[204:207], v[118:121]
	s_barrier
	s_setprio 1
	s_waitcnt lgkmcnt(0)
	v_mfma_f32_16x16x32_bf16 v[106:109], v[134:137], v[204:207], v[106:109]
	v_mfma_f32_16x16x32_bf16 v[102:105], v[122:125], v[212:215], v[102:105]
	v_mfma_f32_16x16x32_bf16 v[90:93], v[134:137], v[212:215], v[90:93]
	v_mfma_f32_16x16x32_bf16 v[86:89], v[122:125], v[220:223], v[86:89]
	v_mfma_f32_16x16x32_bf16 v[74:77], v[134:137], v[220:223], v[74:77]
	v_mfma_f32_16x16x32_bf16 v[138:141], v[126:129], v[200:203], v[138:141]
	v_mfma_f32_16x16x32_bf16 v[130:133], v[142:145], v[200:203], v[130:133]
	v_mfma_f32_16x16x32_bf16 v[118:121], v[126:129], v[208:211], v[118:121]
	v_mfma_f32_16x16x32_bf16 v[106:109], v[142:145], v[208:211], v[106:109]
	v_mfma_f32_16x16x32_bf16 v[102:105], v[126:129], v[216:219], v[102:105]
	v_mfma_f32_16x16x32_bf16 v[90:93], v[142:145], v[216:219], v[90:93]
	v_mfma_f32_16x16x32_bf16 v[86:89], v[126:129], v[224:227], v[86:89]
	v_mfma_f32_16x16x32_bf16 v[74:77], v[142:145], v[224:227], v[74:77]
	s_setprio 0
	s_setprio 1
	v_mfma_f32_16x16x32_bf16 v[114:117], v[174:177], v[196:199], v[114:117]
	v_mfma_f32_16x16x32_bf16 v[110:113], v[188:191], v[196:199], v[110:113]
	v_mfma_f32_16x16x32_bf16 v[98:101], v[174:177], v[204:207], v[98:101]
	v_mfma_f32_16x16x32_bf16 v[94:97], v[188:191], v[204:207], v[94:97]
	v_mfma_f32_16x16x32_bf16 v[82:85], v[174:177], v[212:215], v[82:85]
	v_mfma_f32_16x16x32_bf16 v[78:81], v[188:191], v[212:215], v[78:81]
	v_mfma_f32_16x16x32_bf16 v[70:73], v[174:177], v[220:223], v[70:73]
	v_mfma_f32_16x16x32_bf16 v[66:69], v[188:191], v[220:223], v[66:69]
	v_mfma_f32_16x16x32_bf16 v[114:117], v[178:181], v[200:203], v[114:117]
	v_mfma_f32_16x16x32_bf16 v[110:113], v[192:195], v[200:203], v[110:113]
	v_mfma_f32_16x16x32_bf16 v[98:101], v[178:181], v[208:211], v[98:101]
	v_mfma_f32_16x16x32_bf16 v[94:97], v[192:195], v[208:211], v[94:97]
	v_mfma_f32_16x16x32_bf16 v[82:85], v[178:181], v[216:219], v[82:85]
	v_mfma_f32_16x16x32_bf16 v[78:81], v[192:195], v[216:219], v[78:81]
	v_mfma_f32_16x16x32_bf16 v[70:73], v[178:181], v[224:227], v[70:73]
	v_mfma_f32_16x16x32_bf16 v[66:69], v[192:195], v[224:227], v[66:69]
	s_setprio 0
	s_barrier
	s_add_i32 s58, s58, s38
	v_lshl_add_u64 v[182:183], s[22:23], 0, v[0:1]
	s_mov_b32 m0, s58
	ds_read_b128 v[196:199], v186 offset:16384
	ds_read_b128 v[200:203], v186 offset:17408
	ds_read_b128 v[204:207], v186 offset:18432
	ds_read_b128 v[208:211], v186 offset:19456
	ds_read_b128 v[212:215], v186 offset:20480
	ds_read_b128 v[216:219], v186 offset:21504
	ds_read_b128 v[220:223], v186 offset:22528
	ds_read_b128 v[224:227], v186 offset:23552
	global_load_lds_dwordx4 v[182:183], off
	s_add_i32 m0, s58, 0x2000
	s_add_u32 s58, s22, 0x40000
	v_lshl_add_u64 v[228:229], s[22:23], 0, v[148:149]
	s_addc_u32 s59, s23, 0
	s_add_i32 s60, s60, s38
	global_load_lds_dwordx4 v[228:229], off
	v_lshl_add_u64 v[230:231], s[58:59], 0, v[0:1]
	s_mov_b32 m0, s60
	v_lshl_add_u64 v[232:233], s[24:25], 0, v[150:151]
	global_load_lds_dwordx4 v[230:231], off
	v_lshl_add_u64 v[230:231], s[58:59], 0, v[148:149]
	s_add_i32 m0, s60, 0x2000
	s_nop 0
	global_load_lds_dwordx4 v[230:231], off
	v_lshl_add_u64 v[230:231], s[24:25], 0, v[152:153]
	s_mov_b32 m0, s39
	s_nop 0
	global_load_lds_dwordx4 v[230:231], off
	s_mov_b32 m0, s41
	s_nop 0
	global_load_lds_dwordx4 v[232:233], off
	s_waitcnt vmcnt(8)
	s_waitcnt lgkmcnt(0)
	v_mfma_f32_16x16x32_bf16 v[62:65], v[122:125], v[196:199], v[62:65]
	v_mfma_f32_16x16x32_bf16 v[58:61], v[134:137], v[196:199], v[58:61]
	v_mfma_f32_16x16x32_bf16 v[54:57], v[122:125], v[204:207], v[54:57]
	s_barrier
; #define PG8_STAGE(bufoff, gbase, voff) do { _Pragma("unroll") for (int _i = 0; _i < 2; ++_i) \
;         __builtin_amdgcn_global_load_lds((const unsigned*)((const char*)(gbase) + (voff)[_i]), (PG8_LAS unsigned*)(lds + (bufoff) + ldsw + _i * 8192), 16, 0, 0); } while (0)
; #define PG8_LDA(dst, b, h) do { _Pragma("unroll") for (int m = 0; m < 4; ++m) _Pragma("unroll") for (int k = 0; k < 2; ++k) dst[m][k] = *(const PG8_LAS bf16x8*)(lds + PG8_SA(b, h) + aoff + m * 2048 + k * 1024); } while (0)
; #define PG8_LDB(dst, b, h) do { _Pragma("unroll") for (int n = 0; n < 2; ++n) _Pragma("unroll") for (int k = 0; k < 2; ++k) dst[n][k] = *(const PG8_LAS bf16x8*)(lds + PG8_SB(b, h) + boff + n * 2048 + k * 1024); } while (0)
; #define PG8_WAIT_V(n) asm volatile("s_waitcnt vmcnt(" #n ")" ::: "memory")
; #define PG8_WAIT_L(n) asm volatile("s_waitcnt lgkmcnt(" #n ")" ::: "memory")
; #define PG8_BAR __builtin_amdgcn_s_barrier()
; #define PG8_SCHED __builtin_amdgcn_sched_barrier(0)
; template <class Epi, class Sched, bool ALIGN_EPI = false, bool SP2 = false, bool GATHER = false>
; __device__ __forceinline__ void gemm_phase(PG8_LAS unsigned char* lds, const Gemm g, const Sched& S, const Epi& E, int tid_in, const int* rowsrc = nullptr, PG8_LAS int* idx_lds = nullptr) {
;     ...
;             PG8_LDB(B0, 0, 0); PG8_LDB(B1, 0, 1); PG8_SCHED; PG8_LDA(At, 0, 0); PG8_STAGE(PG8_SA(1, 1), a1 + hstepA, PG8_OA(1));
;             PG8_WAIT_V(8); PG8_WAIT_L(0); PG8_BAR; PG8_MMA(0, 0, At, B0); PG8_MMA(0, 1, At, B1); PG8_BAR; PG8_SCHED;
;             PG8_LDA(At, 0, 1); PG8_STAGE(PG8_SB(0, 0), b2, voffB); PG8_STAGE(PG8_SB(0, 1), b2 + hstep, voffB); PG8_STAGE(PG8_SA(0, 0), a2, PG8_OS(0));
;             PG8_WAIT_V(8); PG8_WAIT_L(0); PG8_BAR; PG8_MMA(1, 0, At, B0); PG8_MMA(1, 1, At, B1); PG8_BAR; PG8_SCHED;
;             PG8_LDB(B0, 1, 0); PG8_LDB(B1, 1, 1); PG8_SCHED; PG8_LDA(At, 1, 0); PG8_STAGE(PG8_SA(0, 1), a2 + hstepA, PG8_OS(1));
;             PG8_WAIT_V(8); PG8_WAIT_L(0); PG8_BAR; PG8_MMA(0, 0, At, B0); PG8_MMA(0, 1, At, B1); PG8_BAR; PG8_SCHED;
;             PG8_LDA(At, 1, 1); PG8_STAGE(PG8_SB(1, 0), b3, voffB); PG8_STAGE(PG8_SB(1, 1), b3 + hstep, voffB); PG8_STAGE(PG8_SA(1, 0), a3, PG8_OS(0));
;             PG8_WAIT_V(8); PG8_WAIT_L(0); PG8_BAR; PG8_MMA(1, 0, At, B0); PG8_MMA(1, 1, At, B1); PG8_BAR; PG8_SCHED;
	s_setprio 1
	s_waitcnt lgkmcnt(0)
	v_mfma_f32_16x16x32_bf16 v[42:45], v[134:137], v[204:207], v[42:45]
	v_mfma_f32_16x16x32_bf16 v[38:41], v[122:125], v[212:215], v[38:41]
	v_mfma_f32_16x16x32_bf16 v[26:29], v[134:137], v[212:215], v[26:29]
	v_mfma_f32_16x16x32_bf16 v[22:25], v[122:125], v[220:223], v[22:25]
	v_mfma_f32_16x16x32_bf16 v[10:13], v[134:137], v[220:223], v[10:13]
	v_mfma_f32_16x16x32_bf16 v[62:65], v[126:129], v[200:203], v[62:65]
	v_mfma_f32_16x16x32_bf16 v[58:61], v[142:145], v[200:203], v[58:61]
	v_mfma_f32_16x16x32_bf16 v[54:57], v[126:129], v[208:211], v[54:57]
	v_mfma_f32_16x16x32_bf16 v[42:45], v[142:145], v[208:211], v[42:45]
	v_mfma_f32_16x16x32_bf16 v[38:41], v[126:129], v[216:219], v[38:41]
	v_mfma_f32_16x16x32_bf16 v[26:29], v[142:145], v[216:219], v[26:29]
	v_mfma_f32_16x16x32_bf16 v[22:25], v[126:129], v[224:227], v[22:25]
	v_mfma_f32_16x16x32_bf16 v[10:13], v[142:145], v[224:227], v[10:13]
	s_setprio 0
	s_setprio 1
	v_mfma_f32_16x16x32_bf16 v[50:53], v[174:177], v[196:199], v[50:53]
	v_mfma_f32_16x16x32_bf16 v[46:49], v[188:191], v[196:199], v[46:49]
	v_mfma_f32_16x16x32_bf16 v[34:37], v[174:177], v[204:207], v[34:37]
	v_mfma_f32_16x16x32_bf16 v[30:33], v[188:191], v[204:207], v[30:33]
	v_mfma_f32_16x16x32_bf16 v[18:21], v[174:177], v[212:215], v[18:21]
	v_mfma_f32_16x16x32_bf16 v[14:17], v[188:191], v[212:215], v[14:17]
	v_mfma_f32_16x16x32_bf16 v[6:9], v[174:177], v[220:223], v[6:9]
	v_mfma_f32_16x16x32_bf16 v[2:5], v[188:191], v[220:223], v[2:5]
	v_mfma_f32_16x16x32_bf16 v[50:53], v[178:181], v[200:203], v[50:53]
	v_mfma_f32_16x16x32_bf16 v[46:49], v[192:195], v[200:203], v[46:49]
	v_mfma_f32_16x16x32_bf16 v[34:37], v[178:181], v[208:211], v[34:37]
	v_mfma_f32_16x16x32_bf16 v[30:33], v[192:195], v[208:211], v[30:33]
	v_mfma_f32_16x16x32_bf16 v[18:21], v[178:181], v[216:219], v[18:21]
	v_mfma_f32_16x16x32_bf16 v[14:17], v[192:195], v[216:219], v[14:17]
	v_mfma_f32_16x16x32_bf16 v[6:9], v[178:181], v[224:227], v[6:9]
	v_mfma_f32_16x16x32_bf16 v[2:5], v[192:195], v[224:227], v[2:5]
	s_setprio 0
	s_barrier
	s_add_i32 s58, 0, 0x18000
	s_add_i32 s59, 0, 0x1c000
	v_add_u32_e32 v142, s58, v184
	v_add_u32_e32 v187, s59, v184
	ds_read_b128 v[122:125], v142
	ds_read_b128 v[126:129], v142 offset:1024
	ds_read_b128 v[134:137], v142 offset:2048
	ds_read_b128 v[142:145], v142 offset:3072
	ds_read_b128 v[174:177], v187
	ds_read_b128 v[178:181], v187 offset:1024
	ds_read_b128 v[188:191], v187 offset:2048
	ds_read_b128 v[192:195], v187 offset:3072
	s_add_u32 s24, s24, 0x40000
	s_addc_u32 s25, s25, 0
	s_mov_b32 m0, s43
	v_lshl_add_u64 v[234:235], s[24:25], 0, v[152:153]
	ds_read_b128 v[196:199], v186 offset:32768
	ds_read_b128 v[200:203], v186 offset:33792
	ds_read_b128 v[204:207], v186 offset:34816
	ds_read_b128 v[208:211], v186 offset:35840
	ds_read_b128 v[212:215], v186 offset:36864
	ds_read_b128 v[216:219], v186 offset:37888
	ds_read_b128 v[220:223], v186 offset:38912
	ds_read_b128 v[224:227], v186 offset:39936
	global_load_lds_dwordx4 v[234:235], off
	v_lshl_add_u64 v[234:235], s[24:25], 0, v[150:151]
	s_mov_b32 m0, s45
	s_nop 0
	global_load_lds_dwordx4 v[234:235], off
	s_waitcnt vmcnt(8)
	s_waitcnt lgkmcnt(0)
	v_mfma_f32_16x16x32_bf16 v[138:141], v[122:125], v[196:199], v[138:141]
	v_mfma_f32_16x16x32_bf16 v[130:133], v[134:137], v[196:199], v[130:133]
	v_mfma_f32_16x16x32_bf16 v[118:121], v[122:125], v[204:207], v[118:121]
	s_barrier
	s_setprio 1
	s_waitcnt lgkmcnt(0)
	v_mfma_f32_16x16x32_bf16 v[106:109], v[134:137], v[204:207], v[106:109]
	v_mfma_f32_16x16x32_bf16 v[102:105], v[122:125], v[212:215], v[102:105]
	v_mfma_f32_16x16x32_bf16 v[90:93], v[134:137], v[212:215], v[90:93]
	v_mfma_f32_16x16x32_bf16 v[86:89], v[122:125], v[220:223], v[86:89]
	v_mfma_f32_16x16x32_bf16 v[74:77], v[134:137], v[220:223], v[74:77]
	v_mfma_f32_16x16x32_bf16 v[138:141], v[126:129], v[200:203], v[138:141]
	v_mfma_f32_16x16x32_bf16 v[130:133], v[142:145], v[200:203], v[130:133]
	v_mfma_f32_16x16x32_bf16 v[118:121], v[126:129], v[208:211], v[118:121]
	v_mfma_f32_16x16x32_bf16 v[106:109], v[142:145], v[208:211], v[106:109]
	v_mfma_f32_16x16x32_bf16 v[102:105], v[126:129], v[216:219], v[102:105]
	v_mfma_f32_16x16x32_bf16 v[90:93], v[142:145], v[216:219], v[90:93]
	v_mfma_f32_16x16x32_bf16 v[86:89], v[126:129], v[224:227], v[86:89]
	v_mfma_f32_16x16x32_bf16 v[74:77], v[142:145], v[224:227], v[74:77]
	s_setprio 0
	s_setprio 1
	v_mfma_f32_16x16x32_bf16 v[114:117], v[174:177], v[196:199], v[114:117]
	v_mfma_f32_16x16x32_bf16 v[110:113], v[188:191], v[196:199], v[110:113]
	v_mfma_f32_16x16x32_bf16 v[98:101], v[174:177], v[204:207], v[98:101]
	v_mfma_f32_16x16x32_bf16 v[94:97], v[188:191], v[204:207], v[94:97]
	v_mfma_f32_16x16x32_bf16 v[82:85], v[174:177], v[212:215], v[82:85]
	v_mfma_f32_16x16x32_bf16 v[78:81], v[188:191], v[212:215], v[78:81]
	v_mfma_f32_16x16x32_bf16 v[70:73], v[174:177], v[220:223], v[70:73]
	v_mfma_f32_16x16x32_bf16 v[66:69], v[188:191], v[220:223], v[66:69]
	v_mfma_f32_16x16x32_bf16 v[114:117], v[178:181], v[200:203], v[114:117]
	v_mfma_f32_16x16x32_bf16 v[110:113], v[192:195], v[200:203], v[110:113]
	v_mfma_f32_16x16x32_bf16 v[98:101], v[178:181], v[208:211], v[98:101]
	v_mfma_f32_16x16x32_bf16 v[94:97], v[192:195], v[208:211], v[94:97]
	v_mfma_f32_16x16x32_bf16 v[82:85], v[178:181], v[216:219], v[82:85]
	v_mfma_f32_16x16x32_bf16 v[78:81], v[192:195], v[216:219], v[78:81]
	v_mfma_f32_16x16x32_bf16 v[70:73], v[178:181], v[224:227], v[70:73]
	v_mfma_f32_16x16x32_bf16 v[66:69], v[192:195], v[224:227], v[66:69]
	s_setprio 0
	s_barrier
; #define PG8_STAGE(bufoff, gbase, voff) do { _Pragma("unroll") for (int _i = 0; _i < 2; ++_i) \
;         __builtin_amdgcn_global_load_lds((const unsigned*)((const char*)(gbase) + (voff)[_i]), (PG8_LAS unsigned*)(lds + (bufoff) + ldsw + _i * 8192), 16, 0, 0); } while (0)
; #define PG8_LDA(dst, b, h) do { _Pragma("unroll") for (int m = 0; m < 4; ++m) _Pragma("unroll") for (int k = 0; k < 2; ++k) dst[m][k] = *(const PG8_LAS bf16x8*)(lds + PG8_SA(b, h) + aoff + m * 2048 + k * 1024); } while (0)
; #define PG8_LDB(dst, b, h) do { _Pragma("unroll") for (int n = 0; n < 2; ++n) _Pragma("unroll") for (int k = 0; k < 2; ++k) dst[n][k] = *(const PG8_LAS bf16x8*)(lds + PG8_SB(b, h) + boff + n * 2048 + k * 1024); } while (0)
; #define PG8_WAIT_V(n) asm volatile("s_waitcnt vmcnt(" #n ")" ::: "memory")
; #define PG8_WAIT_L(n) asm volatile("s_waitcnt lgkmcnt(" #n ")" ::: "memory")
; #define PG8_BAR __builtin_amdgcn_s_barrier()
; #define PG8_SCHED __builtin_amdgcn_sched_barrier(0)
; template <class Epi, class Sched, bool ALIGN_EPI = false, bool SP2 = false, bool GATHER = false>
; __device__ __forceinline__ void gemm_phase(PG8_LAS unsigned char* lds, const Gemm g, const Sched& S, const Epi& E, int tid_in, const int* rowsrc = nullptr, PG8_LAS int* idx_lds = nullptr) {
;     ...
;             PG8_LDB(B0, 0, 0); PG8_LDB(B1, 0, 1); PG8_SCHED; PG8_LDA(At, 0, 0); PG8_STAGE(PG8_SA(1, 1), a1 + hstepA, PG8_OA(1));
;             PG8_WAIT_V(8); PG8_WAIT_L(0); PG8_BAR; PG8_MMA(0, 0, At, B0); PG8_MMA(0, 1, At, B1); PG8_BAR; PG8_SCHED;
;             PG8_LDA(At, 0, 1); PG8_STAGE(PG8_SB(0, 0), b2, voffB); PG8_STAGE(PG8_SB(0, 1), b2 + hstep, voffB); PG8_STAGE(PG8_SA(0, 0), a2, PG8_OS(0));
;             PG8_WAIT_V(8); PG8_WAIT_L(0); PG8_BAR; PG8_MMA(1, 0, At, B0); PG8_MMA(1, 1, At, B1); PG8_BAR; PG8_SCHED;
;             PG8_LDB(B0, 1, 0); PG8_LDB(B1, 1, 1); PG8_SCHED; PG8_LDA(At, 1, 0); PG8_STAGE(PG8_SA(0, 1), a2 + hstepA, PG8_OS(1));
;             PG8_WAIT_V(8); PG8_WAIT_L(0); PG8_BAR; PG8_MMA(0, 0, At, B0); PG8_MMA(0, 1, At, B1); PG8_BAR; PG8_SCHED;
;             PG8_LDA(At, 1, 1); PG8_STAGE(PG8_SB(1, 0), b3, voffB); PG8_STAGE(PG8_SB(1, 1), b3 + hstep, voffB); PG8_STAGE(PG8_SA(1, 0), a3, PG8_OS(0));
;             PG8_WAIT_V(8); PG8_WAIT_L(0); PG8_BAR; PG8_MMA(1, 0, At, B0); PG8_MMA(1, 1, At, B1); PG8_BAR; PG8_SCHED;
	s_add_i32 s24, s58, s38
	v_lshl_add_u64 v[182:183], v[182:183], 0, s[10:11]
	s_mov_b32 m0, s24
	ds_read_b128 v[196:199], v186 offset:49152
	ds_read_b128 v[200:203], v186 offset:50176
	ds_read_b128 v[204:207], v186 offset:51200
	ds_read_b128 v[208:211], v186 offset:52224
	ds_read_b128 v[212:215], v186 offset:53248
	ds_read_b128 v[216:219], v186 offset:54272
	ds_read_b128 v[220:223], v186 offset:55296
	ds_read_b128 v[224:227], v186 offset:56320
	global_load_lds_dwordx4 v[182:183], off
	s_add_i32 m0, s24, 0x2000
	s_add_u32 s22, s22, 0x40080
	v_lshl_add_u64 v[182:183], v[228:229], 0, s[10:11]
	s_addc_u32 s23, s23, 0
	s_add_i32 s24, s59, s38
	global_load_lds_dwordx4 v[182:183], off
	v_lshl_add_u64 v[182:183], s[22:23], 0, v[0:1]
	s_mov_b32 m0, s24
	s_nop 0
	global_load_lds_dwordx4 v[182:183], off
	v_lshl_add_u64 v[182:183], s[22:23], 0, v[148:149]
	s_add_i32 m0, s24, 0x2000
	s_nop 0
	global_load_lds_dwordx4 v[182:183], off
	v_lshl_add_u64 v[182:183], v[230:231], 0, s[10:11]
	s_mov_b32 m0, s52
	s_nop 0
	global_load_lds_dwordx4 v[182:183], off
	v_lshl_add_u64 v[182:183], v[232:233], 0, s[10:11]
	s_mov_b32 m0, s53
	s_nop 0
	global_load_lds_dwordx4 v[182:183], off
	s_waitcnt vmcnt(8)
	s_waitcnt lgkmcnt(0)
	v_mfma_f32_16x16x32_bf16 v[62:65], v[122:125], v[196:199], v[62:65]
	v_mfma_f32_16x16x32_bf16 v[58:61], v[134:137], v[196:199], v[58:61]
	v_mfma_f32_16x16x32_bf16 v[54:57], v[122:125], v[204:207], v[54:57]
	s_barrier
	s_setprio 1
	s_waitcnt lgkmcnt(0)
	v_mfma_f32_16x16x32_bf16 v[42:45], v[134:137], v[204:207], v[42:45]
	v_mfma_f32_16x16x32_bf16 v[38:41], v[122:125], v[212:215], v[38:41]
	v_mfma_f32_16x16x32_bf16 v[26:29], v[134:137], v[212:215], v[26:29]
	v_mfma_f32_16x16x32_bf16 v[22:25], v[122:125], v[220:223], v[22:25]
	v_mfma_f32_16x16x32_bf16 v[10:13], v[134:137], v[220:223], v[10:13]
	v_mfma_f32_16x16x32_bf16 v[62:65], v[126:129], v[200:203], v[62:65]
	v_mfma_f32_16x16x32_bf16 v[58:61], v[142:145], v[200:203], v[58:61]
	v_mfma_f32_16x16x32_bf16 v[54:57], v[126:129], v[208:211], v[54:57]
	v_mfma_f32_16x16x32_bf16 v[42:45], v[142:145], v[208:211], v[42:45]
	v_mfma_f32_16x16x32_bf16 v[38:41], v[126:129], v[216:219], v[38:41]
	v_mfma_f32_16x16x32_bf16 v[26:29], v[142:145], v[216:219], v[26:29]
	v_mfma_f32_16x16x32_bf16 v[22:25], v[126:129], v[224:227], v[22:25]
	v_mfma_f32_16x16x32_bf16 v[10:13], v[142:145], v[224:227], v[10:13]
	s_setprio 0
	s_setprio 1
	v_mfma_f32_16x16x32_bf16 v[50:53], v[174:177], v[196:199], v[50:53]
	v_mfma_f32_16x16x32_bf16 v[46:49], v[188:191], v[196:199], v[46:49]
	v_mfma_f32_16x16x32_bf16 v[34:37], v[174:177], v[204:207], v[34:37]
	v_mfma_f32_16x16x32_bf16 v[30:33], v[188:191], v[204:207], v[30:33]
	v_mfma_f32_16x16x32_bf16 v[18:21], v[174:177], v[212:215], v[18:21]
	v_mfma_f32_16x16x32_bf16 v[14:17], v[188:191], v[212:215], v[14:17]
	v_mfma_f32_16x16x32_bf16 v[6:9], v[174:177], v[220:223], v[6:9]
	v_mfma_f32_16x16x32_bf16 v[2:5], v[188:191], v[220:223], v[2:5]
	v_mfma_f32_16x16x32_bf16 v[50:53], v[178:181], v[200:203], v[50:53]
	v_mfma_f32_16x16x32_bf16 v[46:49], v[192:195], v[200:203], v[46:49]
	v_mfma_f32_16x16x32_bf16 v[34:37], v[178:181], v[208:211], v[34:37]
	v_mfma_f32_16x16x32_bf16 v[30:33], v[192:195], v[208:211], v[30:33]
	v_mfma_f32_16x16x32_bf16 v[18:21], v[178:181], v[216:219], v[18:21]
	v_mfma_f32_16x16x32_bf16 v[14:17], v[192:195], v[216:219], v[14:17]
	v_mfma_f32_16x16x32_bf16 v[6:9], v[178:181], v[224:227], v[6:9]
	v_mfma_f32_16x16x32_bf16 v[2:5], v[192:195], v[224:227], v[2:5]
	s_setprio 0
	s_barrier
	s_add_i32 s57, s57, 2
	s_add_u32 s20, s20, 0x100
	s_addc_u32 s21, s21, 0
	s_add_u32 s55, s55, 0x100
	s_addc_u32 s56, s56, 0
	s_cmp_gt_u32 s57, 13
	s_cbranch_scc0 .LBB0_1101
	s_and_b64 vcc, exec, s[4:5]
	s_cbranch_vccz .LBB0_1104
	s_barrier

; #define PG8_STAGE(bufoff, gbase, voff) do { _Pragma("unroll") for (int _i = 0; _i < 2; ++_i) \
;         __builtin_amdgcn_global_load_lds((const unsigned*)((const char*)(gbase) + (voff)[_i]), (PG8_LAS unsigned*)(lds + (bufoff) + ldsw + _i * 8192), 16, 0, 0); } while (0)
; #define PG8_LDA(dst, b, h) do { _Pragma("unroll") for (int m = 0; m < 4; ++m) _Pragma("unroll") for (int k = 0; k < 2; ++k) dst[m][k] = *(const PG8_LAS bf16x8*)(lds + PG8_SA(b, h) + aoff + m * 2048 + k * 1024); } while (0)
; #define PG8_LDB(dst, b, h) do { _Pragma("unroll") for (int n = 0; n < 2; ++n) _Pragma("unroll") for (int k = 0; k < 2; ++k) dst[n][k] = *(const PG8_LAS bf16x8*)(lds + PG8_SB(b, h) + boff + n * 2048 + k * 1024); } while (0)
; #define PG8_WAIT_V(n) asm volatile("s_waitcnt vmcnt(" #n ")" ::: "memory")
; #define PG8_WAIT_L(n) asm volatile("s_waitcnt lgkmcnt(" #n ")" ::: "memory")
; #define PG8_BAR __builtin_amdgcn_s_barrier()
; #define PG8_SCHED __builtin_amdgcn_sched_barrier(0)
; template <class Epi, class Sched, bool ALIGN_EPI = false, bool SP2 = false, bool GATHER = false>
; __device__ __forceinline__ void gemm_phase(PG8_LAS unsigned char* lds, const Gemm g, const Sched& S, const Epi& E, int tid_in, const int* rowsrc = nullptr, PG8_LAS int* idx_lds = nullptr) {
;     ...
;             PG8_LDB(B0, 0, 0); PG8_LDB(B1, 0, 1); PG8_SCHED; PG8_LDA(At, 0, 0); PG8_STAGE(PG8_SA(1, 1), a1 + hstepA, PG8_OA(1));
;             PG8_WAIT_V(8); PG8_WAIT_L(0); PG8_BAR; PG8_MMA(0, 0, At, B0); PG8_MMA(0, 1, At, B1); PG8_BAR; PG8_SCHED;
;             PG8_LDA(At, 0, 1); PG8_STAGE(PG8_SB(0, 0), b2, voffB); PG8_STAGE(PG8_SB(0, 1), b2 + hstep, voffB); PG8_STAGE(PG8_SA(0, 0), a2, PG8_OS(0));
;             PG8_WAIT_V(8); PG8_WAIT_L(0); PG8_BAR; PG8_MMA(1, 0, At, B0); PG8_MMA(1, 1, At, B1); PG8_BAR; PG8_SCHED;
;             PG8_LDB(B0, 1, 0); PG8_LDB(B1, 1, 1); PG8_SCHED; PG8_LDA(At, 1, 0); PG8_STAGE(PG8_SA(0, 1), a2 + hstepA, PG8_OS(1));
;             PG8_WAIT_V(8); PG8_WAIT_L(0); PG8_BAR; PG8_MMA(0, 0, At, B0); PG8_MMA(0, 1, At, B1); PG8_BAR; PG8_SCHED;
;             PG8_LDA(At, 1, 1); PG8_STAGE(PG8_SB(1, 0), b3, voffB); PG8_STAGE(PG8_SB(1, 1), b3 + hstep, voffB); PG8_STAGE(PG8_SA(1, 0), a3, PG8_OS(0));
;             PG8_WAIT_V(8); PG8_WAIT_L(0); PG8_BAR; PG8_MMA(1, 0, At, B0); PG8_MMA(1, 1, At, B1); PG8_BAR; PG8_SCHED;
.LBB0_1127:
	s_add_u32 s22, s20, 0xfffc0080
	s_addc_u32 s23, s21, -1
	s_add_i32 s52, 0, 0x10000
	s_cmp_eq_u32 s51, 12
	s_cselect_b32 s25, s15, s23
	s_cselect_b32 s24, s45, s22
	v_add_u32_e32 v140, s52, v143
	s_cselect_b32 s23, s13, s50
	s_cselect_b32 s22, s48, s49
	s_add_i32 s54, 0, 0x14000
	ds_read_b128 v[148:151], v140
	ds_read_b128 v[152:155], v140 offset:1024
	ds_read_b128 v[156:159], v140 offset:2048
	ds_read_b128 v[160:163], v140 offset:3072
	v_add_u32_e32 v140, s54, v143
	ds_read_b128 v[164:167], v140
	ds_read_b128 v[168:171], v140 offset:1024
	ds_read_b128 v[172:175], v140 offset:2048
	ds_read_b128 v[184:187], v140 offset:3072
	v_lshl_add_u64 v[140:141], s[20:21], 0, v[136:137]
	s_add_i32 m0, s31, 0xc000
	ds_read_b128 v[188:191], v145
	ds_read_b128 v[192:195], v145 offset:1024
	ds_read_b128 v[196:199], v145 offset:2048
	ds_read_b128 v[200:203], v145 offset:3072
	ds_read_b128 v[204:207], v145 offset:4096
	ds_read_b128 v[208:211], v145 offset:5120
	ds_read_b128 v[212:215], v145 offset:6144
	ds_read_b128 v[216:219], v145 offset:7168
	global_load_lds_dwordx4 v[140:141], off
	v_lshl_add_u64 v[140:141], s[20:21], 0, v[138:139]
	s_add_i32 m0, s31, 0xe000
	s_nop 0
	global_load_lds_dwordx4 v[140:141], off
	s_waitcnt vmcnt(8)
	s_waitcnt lgkmcnt(0)
	v_mfma_f32_16x16x32_bf16 v[126:129], v[148:151], v[188:191], v[126:129]
	v_mfma_f32_16x16x32_bf16 v[122:125], v[156:159], v[188:191], v[122:125]
	v_mfma_f32_16x16x32_bf16 v[118:121], v[148:151], v[196:199], v[118:121]
	s_barrier
	s_setprio 1
	s_waitcnt lgkmcnt(0)
	v_mfma_f32_16x16x32_bf16 v[110:113], v[156:159], v[196:199], v[110:113]
	v_mfma_f32_16x16x32_bf16 v[102:105], v[148:151], v[204:207], v[102:105]
	v_mfma_f32_16x16x32_bf16 v[94:97], v[156:159], v[204:207], v[94:97]
	v_mfma_f32_16x16x32_bf16 v[86:89], v[148:151], v[212:215], v[86:89]
	v_mfma_f32_16x16x32_bf16 v[78:81], v[156:159], v[212:215], v[78:81]
	v_mfma_f32_16x16x32_bf16 v[126:129], v[152:155], v[192:195], v[126:129]
	v_mfma_f32_16x16x32_bf16 v[122:125], v[160:163], v[192:195], v[122:125]
	v_mfma_f32_16x16x32_bf16 v[118:121], v[152:155], v[200:203], v[118:121]
	v_mfma_f32_16x16x32_bf16 v[110:113], v[160:163], v[200:203], v[110:113]
	v_mfma_f32_16x16x32_bf16 v[102:105], v[152:155], v[208:211], v[102:105]
	v_mfma_f32_16x16x32_bf16 v[94:97], v[160:163], v[208:211], v[94:97]
	v_mfma_f32_16x16x32_bf16 v[86:89], v[152:155], v[216:219], v[86:89]
	v_mfma_f32_16x16x32_bf16 v[78:81], v[160:163], v[216:219], v[78:81]
	s_setprio 0
	s_setprio 1
	v_mfma_f32_16x16x32_bf16 v[114:117], v[164:167], v[188:191], v[114:117]
	v_mfma_f32_16x16x32_bf16 v[106:109], v[172:175], v[188:191], v[106:109]
	v_mfma_f32_16x16x32_bf16 v[98:101], v[164:167], v[196:199], v[98:101]
	v_mfma_f32_16x16x32_bf16 v[90:93], v[172:175], v[196:199], v[90:93]
	v_mfma_f32_16x16x32_bf16 v[82:85], v[164:167], v[204:207], v[82:85]
	v_mfma_f32_16x16x32_bf16 v[74:77], v[172:175], v[204:207], v[74:77]
	v_mfma_f32_16x16x32_bf16 v[70:73], v[164:167], v[212:215], v[70:73]
	v_mfma_f32_16x16x32_bf16 v[66:69], v[172:175], v[212:215], v[66:69]
	v_mfma_f32_16x16x32_bf16 v[114:117], v[168:171], v[192:195], v[114:117]
	v_mfma_f32_16x16x32_bf16 v[106:109], v[184:187], v[192:195], v[106:109]
	v_mfma_f32_16x16x32_bf16 v[98:101], v[168:171], v[200:203], v[98:101]
	v_mfma_f32_16x16x32_bf16 v[90:93], v[184:187], v[200:203], v[90:93]
	v_mfma_f32_16x16x32_bf16 v[82:85], v[168:171], v[208:211], v[82:85]
	v_mfma_f32_16x16x32_bf16 v[74:77], v[184:187], v[208:211], v[74:77]
	v_mfma_f32_16x16x32_bf16 v[70:73], v[168:171], v[216:219], v[70:73]
	v_mfma_f32_16x16x32_bf16 v[66:69], v[184:187], v[216:219], v[66:69]
	s_setprio 0
	s_barrier
	s_add_i32 s52, s52, s30
	v_lshl_add_u64 v[140:141], s[22:23], 0, v[0:1]
	s_mov_b32 m0, s52
	ds_read_b128 v[188:191], v145 offset:16384
	ds_read_b128 v[192:195], v145 offset:17408
	ds_read_b128 v[196:199], v145 offset:18432
	ds_read_b128 v[200:203], v145 offset:19456
	ds_read_b128 v[204:207], v145 offset:20480
	ds_read_b128 v[208:211], v145 offset:21504
	ds_read_b128 v[212:215], v145 offset:22528
	ds_read_b128 v[216:219], v145 offset:23552
	global_load_lds_dwordx4 v[140:141], off
	s_add_i32 m0, s52, 0x2000
	s_add_u32 s52, s22, 0x40000
	v_lshl_add_u64 v[176:177], s[22:23], 0, v[130:131]
	s_addc_u32 s53, s23, 0
	s_add_i32 s54, s54, s30
	global_load_lds_dwordx4 v[176:177], off
	v_lshl_add_u64 v[178:179], s[52:53], 0, v[0:1]
	s_mov_b32 m0, s54
	v_lshl_add_u64 v[180:181], s[24:25], 0, v[132:133]
	global_load_lds_dwordx4 v[178:179], off
	v_lshl_add_u64 v[178:179], s[52:53], 0, v[130:131]
	s_add_i32 m0, s54, 0x2000
	s_nop 0
	global_load_lds_dwordx4 v[178:179], off
	v_lshl_add_u64 v[178:179], s[24:25], 0, v[134:135]
	s_mov_b32 m0, s31
	s_nop 0
	global_load_lds_dwordx4 v[178:179], off
	s_mov_b32 m0, s34
	s_nop 0
	global_load_lds_dwordx4 v[180:181], off
	s_waitcnt vmcnt(8)
	s_waitcnt lgkmcnt(0)
	v_mfma_f32_16x16x32_bf16 v[62:65], v[148:151], v[188:191], v[62:65]
	v_mfma_f32_16x16x32_bf16 v[58:61], v[156:159], v[188:191], v[58:61]
	v_mfma_f32_16x16x32_bf16 v[54:57], v[148:151], v[196:199], v[54:57]
	s_barrier
; #define PG8_STAGE(bufoff, gbase, voff) do { _Pragma("unroll") for (int _i = 0; _i < 2; ++_i) \
;         __builtin_amdgcn_global_load_lds((const unsigned*)((const char*)(gbase) + (voff)[_i]), (PG8_LAS unsigned*)(lds + (bufoff) + ldsw + _i * 8192), 16, 0, 0); } while (0)
; #define PG8_LDA(dst, b, h) do { _Pragma("unroll") for (int m = 0; m < 4; ++m) _Pragma("unroll") for (int k = 0; k < 2; ++k) dst[m][k] = *(const PG8_LAS bf16x8*)(lds + PG8_SA(b, h) + aoff + m * 2048 + k * 1024); } while (0)
; #define PG8_LDB(dst, b, h) do { _Pragma("unroll") for (int n = 0; n < 2; ++n) _Pragma("unroll") for (int k = 0; k < 2; ++k) dst[n][k] = *(const PG8_LAS bf16x8*)(lds + PG8_SB(b, h) + boff + n * 2048 + k * 1024); } while (0)
; #define PG8_WAIT_V(n) asm volatile("s_waitcnt vmcnt(" #n ")" ::: "memory")
; #define PG8_WAIT_L(n) asm volatile("s_waitcnt lgkmcnt(" #n ")" ::: "memory")
; #define PG8_BAR __builtin_amdgcn_s_barrier()
; #define PG8_SCHED __builtin_amdgcn_sched_barrier(0)
; template <class Epi, class Sched, bool ALIGN_EPI = false, bool SP2 = false, bool GATHER = false>
; __device__ __forceinline__ void gemm_phase(PG8_LAS unsigned char* lds, const Gemm g, const Sched& S, const Epi& E, int tid_in, const int* rowsrc = nullptr, PG8_LAS int* idx_lds = nullptr) {
;     ...
;             PG8_LDB(B0, 0, 0); PG8_LDB(B1, 0, 1); PG8_SCHED; PG8_LDA(At, 0, 0); PG8_STAGE(PG8_SA(1, 1), a1 + hstepA, PG8_OA(1));
;             PG8_WAIT_V(8); PG8_WAIT_L(0); PG8_BAR; PG8_MMA(0, 0, At, B0); PG8_MMA(0, 1, At, B1); PG8_BAR; PG8_SCHED;
;             PG8_LDA(At, 0, 1); PG8_STAGE(PG8_SB(0, 0), b2, voffB); PG8_STAGE(PG8_SB(0, 1), b2 + hstep, voffB); PG8_STAGE(PG8_SA(0, 0), a2, PG8_OS(0));
;             PG8_WAIT_V(8); PG8_WAIT_L(0); PG8_BAR; PG8_MMA(1, 0, At, B0); PG8_MMA(1, 1, At, B1); PG8_BAR; PG8_SCHED;
;             PG8_LDB(B0, 1, 0); PG8_LDB(B1, 1, 1); PG8_SCHED; PG8_LDA(At, 1, 0); PG8_STAGE(PG8_SA(0, 1), a2 + hstepA, PG8_OS(1));
;             PG8_WAIT_V(8); PG8_WAIT_L(0); PG8_BAR; PG8_MMA(0, 0, At, B0); PG8_MMA(0, 1, At, B1); PG8_BAR; PG8_SCHED;
;             PG8_LDA(At, 1, 1); PG8_STAGE(PG8_SB(1, 0), b3, voffB); PG8_STAGE(PG8_SB(1, 1), b3 + hstep, voffB); PG8_STAGE(PG8_SA(1, 0), a3, PG8_OS(0));
;             PG8_WAIT_V(8); PG8_WAIT_L(0); PG8_BAR; PG8_MMA(1, 0, At, B0); PG8_MMA(1, 1, At, B1); PG8_BAR; PG8_SCHED;
	s_setprio 1
	s_waitcnt lgkmcnt(0)
	v_mfma_f32_16x16x32_bf16 v[46:49], v[156:159], v[196:199], v[46:49]
	v_mfma_f32_16x16x32_bf16 v[38:41], v[148:151], v[204:207], v[38:41]
	v_mfma_f32_16x16x32_bf16 v[30:33], v[156:159], v[204:207], v[30:33]
	v_mfma_f32_16x16x32_bf16 v[22:25], v[148:151], v[212:215], v[22:25]
	v_mfma_f32_16x16x32_bf16 v[14:17], v[156:159], v[212:215], v[14:17]
	v_mfma_f32_16x16x32_bf16 v[62:65], v[152:155], v[192:195], v[62:65]
	v_mfma_f32_16x16x32_bf16 v[58:61], v[160:163], v[192:195], v[58:61]
	v_mfma_f32_16x16x32_bf16 v[54:57], v[152:155], v[200:203], v[54:57]
	v_mfma_f32_16x16x32_bf16 v[46:49], v[160:163], v[200:203], v[46:49]
	v_mfma_f32_16x16x32_bf16 v[38:41], v[152:155], v[208:211], v[38:41]
	v_mfma_f32_16x16x32_bf16 v[30:33], v[160:163], v[208:211], v[30:33]
	v_mfma_f32_16x16x32_bf16 v[22:25], v[152:155], v[216:219], v[22:25]
	v_mfma_f32_16x16x32_bf16 v[14:17], v[160:163], v[216:219], v[14:17]
	s_setprio 0
	s_setprio 1
	v_mfma_f32_16x16x32_bf16 v[50:53], v[164:167], v[188:191], v[50:53]
	v_mfma_f32_16x16x32_bf16 v[42:45], v[172:175], v[188:191], v[42:45]
	v_mfma_f32_16x16x32_bf16 v[34:37], v[164:167], v[196:199], v[34:37]
	v_mfma_f32_16x16x32_bf16 v[26:29], v[172:175], v[196:199], v[26:29]
	v_mfma_f32_16x16x32_bf16 v[18:21], v[164:167], v[204:207], v[18:21]
	v_mfma_f32_16x16x32_bf16 v[10:13], v[172:175], v[204:207], v[10:13]
	v_mfma_f32_16x16x32_bf16 v[6:9], v[164:167], v[212:215], v[6:9]
	v_mfma_f32_16x16x32_bf16 v[2:5], v[172:175], v[212:215], v[2:5]
	v_mfma_f32_16x16x32_bf16 v[50:53], v[168:171], v[192:195], v[50:53]
	v_mfma_f32_16x16x32_bf16 v[42:45], v[184:187], v[192:195], v[42:45]
	v_mfma_f32_16x16x32_bf16 v[34:37], v[168:171], v[200:203], v[34:37]
	v_mfma_f32_16x16x32_bf16 v[26:29], v[184:187], v[200:203], v[26:29]
	v_mfma_f32_16x16x32_bf16 v[18:21], v[168:171], v[208:211], v[18:21]
	v_mfma_f32_16x16x32_bf16 v[10:13], v[184:187], v[208:211], v[10:13]
	v_mfma_f32_16x16x32_bf16 v[6:9], v[168:171], v[216:219], v[6:9]
	v_mfma_f32_16x16x32_bf16 v[2:5], v[184:187], v[216:219], v[2:5]
	s_setprio 0
	s_barrier
	s_add_i32 s52, 0, 0x18000
	s_add_i32 s53, 0, 0x1c000
	v_add_u32_e32 v160, s52, v143
	v_add_u32_e32 v182, s53, v143
	ds_read_b128 v[148:151], v160
	ds_read_b128 v[152:155], v160 offset:1024
	ds_read_b128 v[156:159], v160 offset:2048
	ds_read_b128 v[160:163], v160 offset:3072
	ds_read_b128 v[164:167], v182
	ds_read_b128 v[168:171], v182 offset:1024
	ds_read_b128 v[172:175], v182 offset:2048
	ds_read_b128 v[184:187], v182 offset:3072
	s_add_u32 s24, s24, 0x40000
	s_addc_u32 s25, s25, 0
	s_mov_b32 m0, s35
	v_lshl_add_u64 v[182:183], s[24:25], 0, v[134:135]
	ds_read_b128 v[188:191], v145 offset:32768
	ds_read_b128 v[192:195], v145 offset:33792
	ds_read_b128 v[196:199], v145 offset:34816
	ds_read_b128 v[200:203], v145 offset:35840
	ds_read_b128 v[204:207], v145 offset:36864
	ds_read_b128 v[208:211], v145 offset:37888
	ds_read_b128 v[212:215], v145 offset:38912
	ds_read_b128 v[216:219], v145 offset:39936
	global_load_lds_dwordx4 v[182:183], off
	v_lshl_add_u64 v[182:183], s[24:25], 0, v[132:133]
	s_mov_b32 m0, s36
	s_nop 0
	global_load_lds_dwordx4 v[182:183], off
	s_waitcnt vmcnt(8)
	s_waitcnt lgkmcnt(0)
	v_mfma_f32_16x16x32_bf16 v[126:129], v[148:151], v[188:191], v[126:129]
	v_mfma_f32_16x16x32_bf16 v[122:125], v[156:159], v[188:191], v[122:125]
	v_mfma_f32_16x16x32_bf16 v[118:121], v[148:151], v[196:199], v[118:121]
	s_barrier
	s_setprio 1
	s_waitcnt lgkmcnt(0)
	v_mfma_f32_16x16x32_bf16 v[110:113], v[156:159], v[196:199], v[110:113]
	v_mfma_f32_16x16x32_bf16 v[102:105], v[148:151], v[204:207], v[102:105]
	v_mfma_f32_16x16x32_bf16 v[94:97], v[156:159], v[204:207], v[94:97]
	v_mfma_f32_16x16x32_bf16 v[86:89], v[148:151], v[212:215], v[86:89]
	v_mfma_f32_16x16x32_bf16 v[78:81], v[156:159], v[212:215], v[78:81]
	v_mfma_f32_16x16x32_bf16 v[126:129], v[152:155], v[192:195], v[126:129]
	v_mfma_f32_16x16x32_bf16 v[122:125], v[160:163], v[192:195], v[122:125]
	v_mfma_f32_16x16x32_bf16 v[118:121], v[152:155], v[200:203], v[118:121]
	v_mfma_f32_16x16x32_bf16 v[110:113], v[160:163], v[200:203], v[110:113]
	v_mfma_f32_16x16x32_bf16 v[102:105], v[152:155], v[208:211], v[102:105]
	v_mfma_f32_16x16x32_bf16 v[94:97], v[160:163], v[208:211], v[94:97]
	v_mfma_f32_16x16x32_bf16 v[86:89], v[152:155], v[216:219], v[86:89]
	v_mfma_f32_16x16x32_bf16 v[78:81], v[160:163], v[216:219], v[78:81]
	s_setprio 0
	s_setprio 1
	v_mfma_f32_16x16x32_bf16 v[114:117], v[164:167], v[188:191], v[114:117]
	v_mfma_f32_16x16x32_bf16 v[106:109], v[172:175], v[188:191], v[106:109]
	v_mfma_f32_16x16x32_bf16 v[98:101], v[164:167], v[196:199], v[98:101]
	v_mfma_f32_16x16x32_bf16 v[90:93], v[172:175], v[196:199], v[90:93]
	v_mfma_f32_16x16x32_bf16 v[82:85], v[164:167], v[204:207], v[82:85]
	v_mfma_f32_16x16x32_bf16 v[74:77], v[172:175], v[204:207], v[74:77]
	v_mfma_f32_16x16x32_bf16 v[70:73], v[164:167], v[212:215], v[70:73]
	v_mfma_f32_16x16x32_bf16 v[66:69], v[172:175], v[212:215], v[66:69]
	v_mfma_f32_16x16x32_bf16 v[114:117], v[168:171], v[192:195], v[114:117]
	v_mfma_f32_16x16x32_bf16 v[106:109], v[184:187], v[192:195], v[106:109]
	v_mfma_f32_16x16x32_bf16 v[98:101], v[168:171], v[200:203], v[98:101]
	v_mfma_f32_16x16x32_bf16 v[90:93], v[184:187], v[200:203], v[90:93]
	v_mfma_f32_16x16x32_bf16 v[82:85], v[168:171], v[208:211], v[82:85]
	v_mfma_f32_16x16x32_bf16 v[74:77], v[184:187], v[208:211], v[74:77]
	v_mfma_f32_16x16x32_bf16 v[70:73], v[168:171], v[216:219], v[70:73]
	v_mfma_f32_16x16x32_bf16 v[66:69], v[184:187], v[216:219], v[66:69]
	s_setprio 0
	s_barrier
; #define PG8_STAGE(bufoff, gbase, voff) do { _Pragma("unroll") for (int _i = 0; _i < 2; ++_i) \
;         __builtin_amdgcn_global_load_lds((const unsigned*)((const char*)(gbase) + (voff)[_i]), (PG8_LAS unsigned*)(lds + (bufoff) + ldsw + _i * 8192), 16, 0, 0); } while (0)
; #define PG8_LDA(dst, b, h) do { _Pragma("unroll") for (int m = 0; m < 4; ++m) _Pragma("unroll") for (int k = 0; k < 2; ++k) dst[m][k] = *(const PG8_LAS bf16x8*)(lds + PG8_SA(b, h) + aoff + m * 2048 + k * 1024); } while (0)
; #define PG8_LDB(dst, b, h) do { _Pragma("unroll") for (int n = 0; n < 2; ++n) _Pragma("unroll") for (int k = 0; k < 2; ++k) dst[n][k] = *(const PG8_LAS bf16x8*)(lds + PG8_SB(b, h) + boff + n * 2048 + k * 1024); } while (0)
; #define PG8_WAIT_V(n) asm volatile("s_waitcnt vmcnt(" #n ")" ::: "memory")
; #define PG8_WAIT_L(n) asm volatile("s_waitcnt lgkmcnt(" #n ")" ::: "memory")
; #define PG8_BAR __builtin_amdgcn_s_barrier()
; #define PG8_SCHED __builtin_amdgcn_sched_barrier(0)
; template <class Epi, class Sched, bool ALIGN_EPI = false, bool SP2 = false, bool GATHER = false>
; __device__ __forceinline__ void gemm_phase(PG8_LAS unsigned char* lds, const Gemm g, const Sched& S, const Epi& E, int tid_in, const int* rowsrc = nullptr, PG8_LAS int* idx_lds = nullptr) {
;     ...
;             PG8_LDB(B0, 0, 0); PG8_LDB(B1, 0, 1); PG8_SCHED; PG8_LDA(At, 0, 0); PG8_STAGE(PG8_SA(1, 1), a1 + hstepA, PG8_OA(1));
;             PG8_WAIT_V(8); PG8_WAIT_L(0); PG8_BAR; PG8_MMA(0, 0, At, B0); PG8_MMA(0, 1, At, B1); PG8_BAR; PG8_SCHED;
;             PG8_LDA(At, 0, 1); PG8_STAGE(PG8_SB(0, 0), b2, voffB); PG8_STAGE(PG8_SB(0, 1), b2 + hstep, voffB); PG8_STAGE(PG8_SA(0, 0), a2, PG8_OS(0));
;             PG8_WAIT_V(8); PG8_WAIT_L(0); PG8_BAR; PG8_MMA(1, 0, At, B0); PG8_MMA(1, 1, At, B1); PG8_BAR; PG8_SCHED;
;             PG8_LDB(B0, 1, 0); PG8_LDB(B1, 1, 1); PG8_SCHED; PG8_LDA(At, 1, 0); PG8_STAGE(PG8_SA(0, 1), a2 + hstepA, PG8_OS(1));
;             PG8_WAIT_V(8); PG8_WAIT_L(0); PG8_BAR; PG8_MMA(0, 0, At, B0); PG8_MMA(0, 1, At, B1); PG8_BAR; PG8_SCHED;
;             PG8_LDA(At, 1, 1); PG8_STAGE(PG8_SB(1, 0), b3, voffB); PG8_STAGE(PG8_SB(1, 1), b3 + hstep, voffB); PG8_STAGE(PG8_SA(1, 0), a3, PG8_OS(0));
;             PG8_WAIT_V(8); PG8_WAIT_L(0); PG8_BAR; PG8_MMA(1, 0, At, B0); PG8_MMA(1, 1, At, B1); PG8_BAR; PG8_SCHED;
	s_add_i32 s24, s52, s30
	v_lshl_add_u64 v[140:141], v[140:141], 0, s[10:11]
	s_mov_b32 m0, s24
	ds_read_b128 v[188:191], v145 offset:49152
	ds_read_b128 v[192:195], v145 offset:50176
	ds_read_b128 v[196:199], v145 offset:51200
	ds_read_b128 v[200:203], v145 offset:52224
	ds_read_b128 v[204:207], v145 offset:53248
	ds_read_b128 v[208:211], v145 offset:54272
	ds_read_b128 v[212:215], v145 offset:55296
	ds_read_b128 v[216:219], v145 offset:56320
	global_load_lds_dwordx4 v[140:141], off
	s_add_i32 m0, s24, 0x2000
	s_add_u32 s22, s22, 0x40080
	v_lshl_add_u64 v[140:141], v[176:177], 0, s[10:11]
	s_addc_u32 s23, s23, 0
	s_add_i32 s24, s53, s30
	global_load_lds_dwordx4 v[140:141], off
	v_lshl_add_u64 v[140:141], s[22:23], 0, v[0:1]
	s_mov_b32 m0, s24
	s_nop 0
	global_load_lds_dwordx4 v[140:141], off
	v_lshl_add_u64 v[140:141], s[22:23], 0, v[130:131]
	s_add_i32 m0, s24, 0x2000
	s_nop 0
	global_load_lds_dwordx4 v[140:141], off
	v_lshl_add_u64 v[140:141], v[178:179], 0, s[10:11]
	s_mov_b32 m0, s38
	s_nop 0
	global_load_lds_dwordx4 v[140:141], off
	v_lshl_add_u64 v[140:141], v[180:181], 0, s[10:11]
	s_mov_b32 m0, s39
	s_nop 0
	global_load_lds_dwordx4 v[140:141], off
	s_waitcnt vmcnt(8)
	s_waitcnt lgkmcnt(0)
	v_mfma_f32_16x16x32_bf16 v[62:65], v[148:151], v[188:191], v[62:65]
	v_mfma_f32_16x16x32_bf16 v[58:61], v[156:159], v[188:191], v[58:61]
	v_mfma_f32_16x16x32_bf16 v[54:57], v[148:151], v[196:199], v[54:57]
	s_barrier
	s_setprio 1
	s_waitcnt lgkmcnt(0)
	v_mfma_f32_16x16x32_bf16 v[46:49], v[156:159], v[196:199], v[46:49]
	v_mfma_f32_16x16x32_bf16 v[38:41], v[148:151], v[204:207], v[38:41]
	v_mfma_f32_16x16x32_bf16 v[30:33], v[156:159], v[204:207], v[30:33]
	v_mfma_f32_16x16x32_bf16 v[22:25], v[148:151], v[212:215], v[22:25]
	v_mfma_f32_16x16x32_bf16 v[14:17], v[156:159], v[212:215], v[14:17]
	v_mfma_f32_16x16x32_bf16 v[62:65], v[152:155], v[192:195], v[62:65]
	v_mfma_f32_16x16x32_bf16 v[58:61], v[160:163], v[192:195], v[58:61]
	v_mfma_f32_16x16x32_bf16 v[54:57], v[152:155], v[200:203], v[54:57]
	v_mfma_f32_16x16x32_bf16 v[46:49], v[160:163], v[200:203], v[46:49]
	v_mfma_f32_16x16x32_bf16 v[38:41], v[152:155], v[208:211], v[38:41]
	v_mfma_f32_16x16x32_bf16 v[30:33], v[160:163], v[208:211], v[30:33]
	v_mfma_f32_16x16x32_bf16 v[22:25], v[152:155], v[216:219], v[22:25]
	v_mfma_f32_16x16x32_bf16 v[14:17], v[160:163], v[216:219], v[14:17]
	s_setprio 0
	s_setprio 1
	v_mfma_f32_16x16x32_bf16 v[50:53], v[164:167], v[188:191], v[50:53]
	v_mfma_f32_16x16x32_bf16 v[42:45], v[172:175], v[188:191], v[42:45]
	v_mfma_f32_16x16x32_bf16 v[34:37], v[164:167], v[196:199], v[34:37]
	v_mfma_f32_16x16x32_bf16 v[26:29], v[172:175], v[196:199], v[26:29]
	v_mfma_f32_16x16x32_bf16 v[18:21], v[164:167], v[204:207], v[18:21]
	v_mfma_f32_16x16x32_bf16 v[10:13], v[172:175], v[204:207], v[10:13]
	v_mfma_f32_16x16x32_bf16 v[6:9], v[164:167], v[212:215], v[6:9]
	v_mfma_f32_16x16x32_bf16 v[2:5], v[172:175], v[212:215], v[2:5]
	v_mfma_f32_16x16x32_bf16 v[50:53], v[168:171], v[192:195], v[50:53]
	v_mfma_f32_16x16x32_bf16 v[42:45], v[184:187], v[192:195], v[42:45]
	v_mfma_f32_16x16x32_bf16 v[34:37], v[168:171], v[200:203], v[34:37]
	v_mfma_f32_16x16x32_bf16 v[26:29], v[184:187], v[200:203], v[26:29]
	v_mfma_f32_16x16x32_bf16 v[18:21], v[168:171], v[208:211], v[18:21]
	v_mfma_f32_16x16x32_bf16 v[10:13], v[184:187], v[208:211], v[10:13]
	v_mfma_f32_16x16x32_bf16 v[6:9], v[168:171], v[216:219], v[6:9]
	v_mfma_f32_16x16x32_bf16 v[2:5], v[184:187], v[216:219], v[2:5]
	s_setprio 0
	s_barrier
	s_add_i32 s51, s51, 2
	s_add_u32 s20, s20, 0x100
	s_addc_u32 s21, s21, 0
	s_add_u32 s49, s49, 0x100
	s_addc_u32 s50, s50, 0
	s_cmp_gt_u32 s51, 13
	s_cbranch_scc0 .LBB0_1127
	s_and_b64 vcc, exec, s[8:9]
	s_cbranch_vccz .LBB0_1130
	s_barrier

; #define PG8_STAGE(bufoff, gbase, voff) do { _Pragma("unroll") for (int _i = 0; _i < 2; ++_i) \
;         __builtin_amdgcn_global_load_lds((const unsigned*)((const char*)(gbase) + (voff)[_i]), (PG8_LAS unsigned*)(lds + (bufoff) + ldsw + _i * 8192), 16, 0, 0); } while (0)
; #define PG8_LDA(dst, b, h) do { _Pragma("unroll") for (int m = 0; m < 4; ++m) _Pragma("unroll") for (int k = 0; k < 2; ++k) dst[m][k] = *(const PG8_LAS bf16x8*)(lds + PG8_SA(b, h) + aoff + m * 2048 + k * 1024); } while (0)
; #define PG8_LDB(dst, b, h) do { _Pragma("unroll") for (int n = 0; n < 2; ++n) _Pragma("unroll") for (int k = 0; k < 2; ++k) dst[n][k] = *(const PG8_LAS bf16x8*)(lds + PG8_SB(b, h) + boff + n * 2048 + k * 1024); } while (0)
; #define PG8_WAIT_V(n) asm volatile("s_waitcnt vmcnt(" #n ")" ::: "memory")
; #define PG8_WAIT_L(n) asm volatile("s_waitcnt lgkmcnt(" #n ")" ::: "memory")
; #define PG8_BAR __builtin_amdgcn_s_barrier()
; #define PG8_SCHED __builtin_amdgcn_sched_barrier(0)
; template <class Epi, class Sched, bool ALIGN_EPI = false, bool SP2 = false, bool GATHER = false>
; __device__ __forceinline__ void gemm_phase(PG8_LAS unsigned char* lds, const Gemm g, const Sched& S, const Epi& E, int tid_in, const int* rowsrc = nullptr, PG8_LAS int* idx_lds = nullptr) {
;     ...
;             PG8_LDB(B0, 0, 0); PG8_LDB(B1, 0, 1); PG8_SCHED; PG8_LDA(At, 0, 0); PG8_STAGE(PG8_SA(1, 1), a1 + hstepA, PG8_OA(1));
;             PG8_WAIT_V(8); PG8_WAIT_L(0); PG8_BAR; PG8_MMA(0, 0, At, B0); PG8_MMA(0, 1, At, B1); PG8_BAR; PG8_SCHED;
;             PG8_LDA(At, 0, 1); PG8_STAGE(PG8_SB(0, 0), b2, voffB); PG8_STAGE(PG8_SB(0, 1), b2 + hstep, voffB); PG8_STAGE(PG8_SA(0, 0), a2, PG8_OS(0));
;             PG8_WAIT_V(8); PG8_WAIT_L(0); PG8_BAR; PG8_MMA(1, 0, At, B0); PG8_MMA(1, 1, At, B1); PG8_BAR; PG8_SCHED;
;             PG8_LDB(B0, 1, 0); PG8_LDB(B1, 1, 1); PG8_SCHED; PG8_LDA(At, 1, 0); PG8_STAGE(PG8_SA(0, 1), a2 + hstepA, PG8_OS(1));
;             PG8_WAIT_V(8); PG8_WAIT_L(0); PG8_BAR; PG8_MMA(0, 0, At, B0); PG8_MMA(0, 1, At, B1); PG8_BAR; PG8_SCHED;
;             PG8_LDA(At, 1, 1); PG8_STAGE(PG8_SB(1, 0), b3, voffB); PG8_STAGE(PG8_SB(1, 1), b3 + hstep, voffB); PG8_STAGE(PG8_SA(1, 0), a3, PG8_OS(0));
;             PG8_WAIT_V(8); PG8_WAIT_L(0); PG8_BAR; PG8_MMA(1, 0, At, B0); PG8_MMA(1, 1, At, B1); PG8_BAR; PG8_SCHED;
.LBB0_1227:
	s_add_u32 s26, s24, 0xfffc0080
	s_addc_u32 s27, s25, -1
	s_add_i32 s60, 0, 0x10000
	s_cmp_eq_u32 s59, 4
	s_cselect_b32 s29, s15, s27
	s_cselect_b32 s28, s55, s26
	v_add_u32_e32 v151, s60, v148
	s_cselect_b32 s27, s13, s58
	s_cselect_b32 s26, s56, s57
	s_add_i32 s62, 0, 0x14000
	ds_read_b128 v[140:143], v151
	ds_read_b128 v[152:155], v151 offset:1024
	ds_read_b128 v[156:159], v151 offset:2048
	ds_read_b128 v[160:163], v151 offset:3072
	v_add_u32_e32 v151, s62, v148
	ds_read_b128 v[164:167], v151
	ds_read_b128 v[168:171], v151 offset:1024
	ds_read_b128 v[172:175], v151 offset:2048
	ds_read_b128 v[184:187], v151 offset:3072
	v_lshl_add_u64 v[176:177], s[24:25], 0, v[136:137]
	s_add_i32 m0, s17, 0xc000
	ds_read_b128 v[188:191], v150
	ds_read_b128 v[192:195], v150 offset:1024
	ds_read_b128 v[196:199], v150 offset:2048
	ds_read_b128 v[200:203], v150 offset:3072
	ds_read_b128 v[204:207], v150 offset:4096
	ds_read_b128 v[208:211], v150 offset:5120
	ds_read_b128 v[212:215], v150 offset:6144
	ds_read_b128 v[216:219], v150 offset:7168
	global_load_lds_dwordx4 v[176:177], off
	v_lshl_add_u64 v[176:177], s[24:25], 0, v[138:139]
	s_add_i32 m0, s17, 0xe000
	s_nop 0
	global_load_lds_dwordx4 v[176:177], off
	s_waitcnt vmcnt(8)
	s_waitcnt lgkmcnt(0)
	v_mfma_f32_16x16x32_bf16 v[126:129], v[140:143], v[188:191], v[126:129]
	v_mfma_f32_16x16x32_bf16 v[122:125], v[156:159], v[188:191], v[122:125]
	v_mfma_f32_16x16x32_bf16 v[118:121], v[140:143], v[196:199], v[118:121]
	s_barrier
	s_setprio 1
	s_waitcnt lgkmcnt(0)
	v_mfma_f32_16x16x32_bf16 v[110:113], v[156:159], v[196:199], v[110:113]
	v_mfma_f32_16x16x32_bf16 v[102:105], v[140:143], v[204:207], v[102:105]
	v_mfma_f32_16x16x32_bf16 v[94:97], v[156:159], v[204:207], v[94:97]
	v_mfma_f32_16x16x32_bf16 v[86:89], v[140:143], v[212:215], v[86:89]
	v_mfma_f32_16x16x32_bf16 v[78:81], v[156:159], v[212:215], v[78:81]
	v_mfma_f32_16x16x32_bf16 v[126:129], v[152:155], v[192:195], v[126:129]
	v_mfma_f32_16x16x32_bf16 v[122:125], v[160:163], v[192:195], v[122:125]
	v_mfma_f32_16x16x32_bf16 v[118:121], v[152:155], v[200:203], v[118:121]
	v_mfma_f32_16x16x32_bf16 v[110:113], v[160:163], v[200:203], v[110:113]
	v_mfma_f32_16x16x32_bf16 v[102:105], v[152:155], v[208:211], v[102:105]
	v_mfma_f32_16x16x32_bf16 v[94:97], v[160:163], v[208:211], v[94:97]
	v_mfma_f32_16x16x32_bf16 v[86:89], v[152:155], v[216:219], v[86:89]
	v_mfma_f32_16x16x32_bf16 v[78:81], v[160:163], v[216:219], v[78:81]
	s_setprio 0
	s_setprio 1
	v_mfma_f32_16x16x32_bf16 v[114:117], v[164:167], v[188:191], v[114:117]
	v_mfma_f32_16x16x32_bf16 v[106:109], v[172:175], v[188:191], v[106:109]
	v_mfma_f32_16x16x32_bf16 v[98:101], v[164:167], v[196:199], v[98:101]
	v_mfma_f32_16x16x32_bf16 v[90:93], v[172:175], v[196:199], v[90:93]
	v_mfma_f32_16x16x32_bf16 v[82:85], v[164:167], v[204:207], v[82:85]
	v_mfma_f32_16x16x32_bf16 v[74:77], v[172:175], v[204:207], v[74:77]
	v_mfma_f32_16x16x32_bf16 v[70:73], v[164:167], v[212:215], v[70:73]
	v_mfma_f32_16x16x32_bf16 v[66:69], v[172:175], v[212:215], v[66:69]
	v_mfma_f32_16x16x32_bf16 v[114:117], v[168:171], v[192:195], v[114:117]
	v_mfma_f32_16x16x32_bf16 v[106:109], v[184:187], v[192:195], v[106:109]
	v_mfma_f32_16x16x32_bf16 v[98:101], v[168:171], v[200:203], v[98:101]
	v_mfma_f32_16x16x32_bf16 v[90:93], v[184:187], v[200:203], v[90:93]
	v_mfma_f32_16x16x32_bf16 v[82:85], v[168:171], v[208:211], v[82:85]
	v_mfma_f32_16x16x32_bf16 v[74:77], v[184:187], v[208:211], v[74:77]
	v_mfma_f32_16x16x32_bf16 v[70:73], v[168:171], v[216:219], v[70:73]
	v_mfma_f32_16x16x32_bf16 v[66:69], v[184:187], v[216:219], v[66:69]
	s_setprio 0
	s_barrier
	s_add_i32 s60, s60, s49
	v_lshl_add_u64 v[176:177], s[26:27], 0, v[0:1]
	s_mov_b32 m0, s60
	ds_read_b128 v[188:191], v150 offset:16384
	ds_read_b128 v[192:195], v150 offset:17408
	ds_read_b128 v[196:199], v150 offset:18432
	ds_read_b128 v[200:203], v150 offset:19456
	ds_read_b128 v[204:207], v150 offset:20480
	ds_read_b128 v[208:211], v150 offset:21504
	ds_read_b128 v[212:215], v150 offset:22528
	ds_read_b128 v[216:219], v150 offset:23552
	global_load_lds_dwordx4 v[176:177], off
	s_add_i32 m0, s60, 0x2000
	s_add_u32 s60, s26, 0x20000
	v_lshl_add_u64 v[178:179], s[26:27], 0, v[130:131]
	s_addc_u32 s61, s27, 0
	s_add_i32 s62, s62, s49
	global_load_lds_dwordx4 v[178:179], off
	v_lshl_add_u64 v[180:181], s[60:61], 0, v[0:1]
	s_mov_b32 m0, s62
	v_lshl_add_u64 v[182:183], s[28:29], 0, v[132:133]
	global_load_lds_dwordx4 v[180:181], off
	v_lshl_add_u64 v[180:181], s[60:61], 0, v[130:131]
	s_add_i32 m0, s62, 0x2000
	s_nop 0
	global_load_lds_dwordx4 v[180:181], off
	v_lshl_add_u64 v[180:181], s[28:29], 0, v[134:135]
	s_mov_b32 m0, s17
	s_nop 0
	global_load_lds_dwordx4 v[180:181], off
	s_mov_b32 m0, s19
	s_nop 0
	global_load_lds_dwordx4 v[182:183], off
	s_waitcnt vmcnt(8)
	s_waitcnt lgkmcnt(0)
	v_mfma_f32_16x16x32_bf16 v[62:65], v[140:143], v[188:191], v[62:65]
	v_mfma_f32_16x16x32_bf16 v[58:61], v[156:159], v[188:191], v[58:61]
	v_mfma_f32_16x16x32_bf16 v[54:57], v[140:143], v[196:199], v[54:57]
	s_barrier
; #define PG8_STAGE(bufoff, gbase, voff) do { _Pragma("unroll") for (int _i = 0; _i < 2; ++_i) \
;         __builtin_amdgcn_global_load_lds((const unsigned*)((const char*)(gbase) + (voff)[_i]), (PG8_LAS unsigned*)(lds + (bufoff) + ldsw + _i * 8192), 16, 0, 0); } while (0)
; #define PG8_LDA(dst, b, h) do { _Pragma("unroll") for (int m = 0; m < 4; ++m) _Pragma("unroll") for (int k = 0; k < 2; ++k) dst[m][k] = *(const PG8_LAS bf16x8*)(lds + PG8_SA(b, h) + aoff + m * 2048 + k * 1024); } while (0)
; #define PG8_LDB(dst, b, h) do { _Pragma("unroll") for (int n = 0; n < 2; ++n) _Pragma("unroll") for (int k = 0; k < 2; ++k) dst[n][k] = *(const PG8_LAS bf16x8*)(lds + PG8_SB(b, h) + boff + n * 2048 + k * 1024); } while (0)
; #define PG8_WAIT_V(n) asm volatile("s_waitcnt vmcnt(" #n ")" ::: "memory")
; #define PG8_WAIT_L(n) asm volatile("s_waitcnt lgkmcnt(" #n ")" ::: "memory")
; #define PG8_BAR __builtin_amdgcn_s_barrier()
; #define PG8_SCHED __builtin_amdgcn_sched_barrier(0)
; template <class Epi, class Sched, bool ALIGN_EPI = false, bool SP2 = false, bool GATHER = false>
; __device__ __forceinline__ void gemm_phase(PG8_LAS unsigned char* lds, const Gemm g, const Sched& S, const Epi& E, int tid_in, const int* rowsrc = nullptr, PG8_LAS int* idx_lds = nullptr) {
;     ...
;             PG8_LDB(B0, 0, 0); PG8_LDB(B1, 0, 1); PG8_SCHED; PG8_LDA(At, 0, 0); PG8_STAGE(PG8_SA(1, 1), a1 + hstepA, PG8_OA(1));
;             PG8_WAIT_V(8); PG8_WAIT_L(0); PG8_BAR; PG8_MMA(0, 0, At, B0); PG8_MMA(0, 1, At, B1); PG8_BAR; PG8_SCHED;
;             PG8_LDA(At, 0, 1); PG8_STAGE(PG8_SB(0, 0), b2, voffB); PG8_STAGE(PG8_SB(0, 1), b2 + hstep, voffB); PG8_STAGE(PG8_SA(0, 0), a2, PG8_OS(0));
;             PG8_WAIT_V(8); PG8_WAIT_L(0); PG8_BAR; PG8_MMA(1, 0, At, B0); PG8_MMA(1, 1, At, B1); PG8_BAR; PG8_SCHED;
;             PG8_LDB(B0, 1, 0); PG8_LDB(B1, 1, 1); PG8_SCHED; PG8_LDA(At, 1, 0); PG8_STAGE(PG8_SA(0, 1), a2 + hstepA, PG8_OS(1));
;             PG8_WAIT_V(8); PG8_WAIT_L(0); PG8_BAR; PG8_MMA(0, 0, At, B0); PG8_MMA(0, 1, At, B1); PG8_BAR; PG8_SCHED;
;             PG8_LDA(At, 1, 1); PG8_STAGE(PG8_SB(1, 0), b3, voffB); PG8_STAGE(PG8_SB(1, 1), b3 + hstep, voffB); PG8_STAGE(PG8_SA(1, 0), a3, PG8_OS(0));
;             PG8_WAIT_V(8); PG8_WAIT_L(0); PG8_BAR; PG8_MMA(1, 0, At, B0); PG8_MMA(1, 1, At, B1); PG8_BAR; PG8_SCHED;
	s_setprio 1
	s_waitcnt lgkmcnt(0)
	v_mfma_f32_16x16x32_bf16 v[46:49], v[156:159], v[196:199], v[46:49]
	v_mfma_f32_16x16x32_bf16 v[38:41], v[140:143], v[204:207], v[38:41]
	v_mfma_f32_16x16x32_bf16 v[30:33], v[156:159], v[204:207], v[30:33]
	v_mfma_f32_16x16x32_bf16 v[22:25], v[140:143], v[212:215], v[22:25]
	v_mfma_f32_16x16x32_bf16 v[14:17], v[156:159], v[212:215], v[14:17]
	v_mfma_f32_16x16x32_bf16 v[62:65], v[152:155], v[192:195], v[62:65]
	v_mfma_f32_16x16x32_bf16 v[58:61], v[160:163], v[192:195], v[58:61]
	v_mfma_f32_16x16x32_bf16 v[54:57], v[152:155], v[200:203], v[54:57]
	v_mfma_f32_16x16x32_bf16 v[46:49], v[160:163], v[200:203], v[46:49]
	v_mfma_f32_16x16x32_bf16 v[38:41], v[152:155], v[208:211], v[38:41]
	v_mfma_f32_16x16x32_bf16 v[30:33], v[160:163], v[208:211], v[30:33]
	v_mfma_f32_16x16x32_bf16 v[22:25], v[152:155], v[216:219], v[22:25]
	v_mfma_f32_16x16x32_bf16 v[14:17], v[160:163], v[216:219], v[14:17]
	s_setprio 0
	s_setprio 1
	v_mfma_f32_16x16x32_bf16 v[50:53], v[164:167], v[188:191], v[50:53]
	v_mfma_f32_16x16x32_bf16 v[42:45], v[172:175], v[188:191], v[42:45]
	v_mfma_f32_16x16x32_bf16 v[34:37], v[164:167], v[196:199], v[34:37]
	v_mfma_f32_16x16x32_bf16 v[26:29], v[172:175], v[196:199], v[26:29]
	v_mfma_f32_16x16x32_bf16 v[18:21], v[164:167], v[204:207], v[18:21]
	v_mfma_f32_16x16x32_bf16 v[10:13], v[172:175], v[204:207], v[10:13]
	v_mfma_f32_16x16x32_bf16 v[6:9], v[164:167], v[212:215], v[6:9]
	v_mfma_f32_16x16x32_bf16 v[2:5], v[172:175], v[212:215], v[2:5]
	v_mfma_f32_16x16x32_bf16 v[50:53], v[168:171], v[192:195], v[50:53]
	v_mfma_f32_16x16x32_bf16 v[42:45], v[184:187], v[192:195], v[42:45]
	v_mfma_f32_16x16x32_bf16 v[34:37], v[168:171], v[200:203], v[34:37]
	v_mfma_f32_16x16x32_bf16 v[26:29], v[184:187], v[200:203], v[26:29]
	v_mfma_f32_16x16x32_bf16 v[18:21], v[168:171], v[208:211], v[18:21]
	v_mfma_f32_16x16x32_bf16 v[10:13], v[184:187], v[208:211], v[10:13]
	v_mfma_f32_16x16x32_bf16 v[6:9], v[168:171], v[216:219], v[6:9]
	v_mfma_f32_16x16x32_bf16 v[2:5], v[184:187], v[216:219], v[2:5]
	s_setprio 0
	s_barrier
	s_add_i32 s60, 0, 0x18000
	v_add_u32_e32 v151, s60, v148
	s_add_i32 s61, 0, 0x1c000
	ds_read_b128 v[140:143], v151
	ds_read_b128 v[152:155], v151 offset:1024
	ds_read_b128 v[156:159], v151 offset:2048
	ds_read_b128 v[160:163], v151 offset:3072
	v_add_u32_e32 v151, s61, v148
	ds_read_b128 v[164:167], v151
	ds_read_b128 v[168:171], v151 offset:1024
	ds_read_b128 v[172:175], v151 offset:2048
	ds_read_b128 v[184:187], v151 offset:3072
	s_add_u32 s28, s28, 0x40000
	s_addc_u32 s29, s29, 0
	s_mov_b32 m0, s50
	v_lshl_add_u64 v[220:221], s[28:29], 0, v[134:135]
	ds_read_b128 v[188:191], v150 offset:32768
	ds_read_b128 v[192:195], v150 offset:33792
	ds_read_b128 v[196:199], v150 offset:34816
	ds_read_b128 v[200:203], v150 offset:35840
	ds_read_b128 v[204:207], v150 offset:36864
	ds_read_b128 v[208:211], v150 offset:37888
	ds_read_b128 v[212:215], v150 offset:38912
	ds_read_b128 v[216:219], v150 offset:39936
	global_load_lds_dwordx4 v[220:221], off
	v_lshl_add_u64 v[220:221], s[28:29], 0, v[132:133]
	s_mov_b32 m0, s51
	s_nop 0
	global_load_lds_dwordx4 v[220:221], off
	s_waitcnt vmcnt(8)
	s_waitcnt lgkmcnt(0)
	v_mfma_f32_16x16x32_bf16 v[126:129], v[140:143], v[188:191], v[126:129]
	v_mfma_f32_16x16x32_bf16 v[122:125], v[156:159], v[188:191], v[122:125]
	v_mfma_f32_16x16x32_bf16 v[118:121], v[140:143], v[196:199], v[118:121]
	s_barrier
	s_setprio 1
	s_waitcnt lgkmcnt(0)
	v_mfma_f32_16x16x32_bf16 v[110:113], v[156:159], v[196:199], v[110:113]
	v_mfma_f32_16x16x32_bf16 v[102:105], v[140:143], v[204:207], v[102:105]
	v_mfma_f32_16x16x32_bf16 v[94:97], v[156:159], v[204:207], v[94:97]
	v_mfma_f32_16x16x32_bf16 v[86:89], v[140:143], v[212:215], v[86:89]
	v_mfma_f32_16x16x32_bf16 v[78:81], v[156:159], v[212:215], v[78:81]
	v_mfma_f32_16x16x32_bf16 v[126:129], v[152:155], v[192:195], v[126:129]
	v_mfma_f32_16x16x32_bf16 v[122:125], v[160:163], v[192:195], v[122:125]
	v_mfma_f32_16x16x32_bf16 v[118:121], v[152:155], v[200:203], v[118:121]
	v_mfma_f32_16x16x32_bf16 v[110:113], v[160:163], v[200:203], v[110:113]
	v_mfma_f32_16x16x32_bf16 v[102:105], v[152:155], v[208:211], v[102:105]
	v_mfma_f32_16x16x32_bf16 v[94:97], v[160:163], v[208:211], v[94:97]
	v_mfma_f32_16x16x32_bf16 v[86:89], v[152:155], v[216:219], v[86:89]
	v_mfma_f32_16x16x32_bf16 v[78:81], v[160:163], v[216:219], v[78:81]
	s_setprio 0
	s_setprio 1
	v_mfma_f32_16x16x32_bf16 v[114:117], v[164:167], v[188:191], v[114:117]
	v_mfma_f32_16x16x32_bf16 v[106:109], v[172:175], v[188:191], v[106:109]
	v_mfma_f32_16x16x32_bf16 v[98:101], v[164:167], v[196:199], v[98:101]
	v_mfma_f32_16x16x32_bf16 v[90:93], v[172:175], v[196:199], v[90:93]
	v_mfma_f32_16x16x32_bf16 v[82:85], v[164:167], v[204:207], v[82:85]
	v_mfma_f32_16x16x32_bf16 v[74:77], v[172:175], v[204:207], v[74:77]
	v_mfma_f32_16x16x32_bf16 v[70:73], v[164:167], v[212:215], v[70:73]
	v_mfma_f32_16x16x32_bf16 v[66:69], v[172:175], v[212:215], v[66:69]
	v_mfma_f32_16x16x32_bf16 v[114:117], v[168:171], v[192:195], v[114:117]
	v_mfma_f32_16x16x32_bf16 v[106:109], v[184:187], v[192:195], v[106:109]
	v_mfma_f32_16x16x32_bf16 v[98:101], v[168:171], v[200:203], v[98:101]
	v_mfma_f32_16x16x32_bf16 v[90:93], v[184:187], v[200:203], v[90:93]
	v_mfma_f32_16x16x32_bf16 v[82:85], v[168:171], v[208:211], v[82:85]
	v_mfma_f32_16x16x32_bf16 v[74:77], v[184:187], v[208:211], v[74:77]
	v_mfma_f32_16x16x32_bf16 v[70:73], v[168:171], v[216:219], v[70:73]
	v_mfma_f32_16x16x32_bf16 v[66:69], v[184:187], v[216:219], v[66:69]
	s_setprio 0
	s_barrier
; #define PG8_STAGE(bufoff, gbase, voff) do { _Pragma("unroll") for (int _i = 0; _i < 2; ++_i) \
;         __builtin_amdgcn_global_load_lds((const unsigned*)((const char*)(gbase) + (voff)[_i]), (PG8_LAS unsigned*)(lds + (bufoff) + ldsw + _i * 8192), 16, 0, 0); } while (0)
; #define PG8_LDA(dst, b, h) do { _Pragma("unroll") for (int m = 0; m < 4; ++m) _Pragma("unroll") for (int k = 0; k < 2; ++k) dst[m][k] = *(const PG8_LAS bf16x8*)(lds + PG8_SA(b, h) + aoff + m * 2048 + k * 1024); } while (0)
; #define PG8_LDB(dst, b, h) do { _Pragma("unroll") for (int n = 0; n < 2; ++n) _Pragma("unroll") for (int k = 0; k < 2; ++k) dst[n][k] = *(const PG8_LAS bf16x8*)(lds + PG8_SB(b, h) + boff + n * 2048 + k * 1024); } while (0)
; #define PG8_WAIT_V(n) asm volatile("s_waitcnt vmcnt(" #n ")" ::: "memory")
; #define PG8_WAIT_L(n) asm volatile("s_waitcnt lgkmcnt(" #n ")" ::: "memory")
; #define PG8_BAR __builtin_amdgcn_s_barrier()
; #define PG8_SCHED __builtin_amdgcn_sched_barrier(0)
; template <class Epi, class Sched, bool ALIGN_EPI = false, bool SP2 = false, bool GATHER = false>
; __device__ __forceinline__ void gemm_phase(PG8_LAS unsigned char* lds, const Gemm g, const Sched& S, const Epi& E, int tid_in, const int* rowsrc = nullptr, PG8_LAS int* idx_lds = nullptr) {
;     ...
;             PG8_LDB(B0, 0, 0); PG8_LDB(B1, 0, 1); PG8_SCHED; PG8_LDA(At, 0, 0); PG8_STAGE(PG8_SA(1, 1), a1 + hstepA, PG8_OA(1));
;             PG8_WAIT_V(8); PG8_WAIT_L(0); PG8_BAR; PG8_MMA(0, 0, At, B0); PG8_MMA(0, 1, At, B1); PG8_BAR; PG8_SCHED;
;             PG8_LDA(At, 0, 1); PG8_STAGE(PG8_SB(0, 0), b2, voffB); PG8_STAGE(PG8_SB(0, 1), b2 + hstep, voffB); PG8_STAGE(PG8_SA(0, 0), a2, PG8_OS(0));
;             PG8_WAIT_V(8); PG8_WAIT_L(0); PG8_BAR; PG8_MMA(1, 0, At, B0); PG8_MMA(1, 1, At, B1); PG8_BAR; PG8_SCHED;
;             PG8_LDB(B0, 1, 0); PG8_LDB(B1, 1, 1); PG8_SCHED; PG8_LDA(At, 1, 0); PG8_STAGE(PG8_SA(0, 1), a2 + hstepA, PG8_OS(1));
;             PG8_WAIT_V(8); PG8_WAIT_L(0); PG8_BAR; PG8_MMA(0, 0, At, B0); PG8_MMA(0, 1, At, B1); PG8_BAR; PG8_SCHED;
;             PG8_LDA(At, 1, 1); PG8_STAGE(PG8_SB(1, 0), b3, voffB); PG8_STAGE(PG8_SB(1, 1), b3 + hstep, voffB); PG8_STAGE(PG8_SA(1, 0), a3, PG8_OS(0));
;             PG8_WAIT_V(8); PG8_WAIT_L(0); PG8_BAR; PG8_MMA(1, 0, At, B0); PG8_MMA(1, 1, At, B1); PG8_BAR; PG8_SCHED;
	s_add_i32 s28, s60, s49
	v_lshl_add_u64 v[176:177], v[176:177], 0, s[10:11]
	s_mov_b32 m0, s28
	ds_read_b128 v[188:191], v150 offset:49152
	ds_read_b128 v[192:195], v150 offset:50176
	ds_read_b128 v[196:199], v150 offset:51200
	ds_read_b128 v[200:203], v150 offset:52224
	ds_read_b128 v[204:207], v150 offset:53248
	ds_read_b128 v[208:211], v150 offset:54272
	ds_read_b128 v[212:215], v150 offset:55296
	ds_read_b128 v[216:219], v150 offset:56320
	global_load_lds_dwordx4 v[176:177], off
	s_add_i32 m0, s28, 0x2000
	s_add_u32 s26, s26, 0x20080
	v_lshl_add_u64 v[176:177], v[178:179], 0, s[10:11]
	s_addc_u32 s27, s27, 0
	s_add_i32 s28, s61, s49
	global_load_lds_dwordx4 v[176:177], off
	v_lshl_add_u64 v[176:177], s[26:27], 0, v[0:1]
	s_mov_b32 m0, s28
	s_nop 0
	global_load_lds_dwordx4 v[176:177], off
	v_lshl_add_u64 v[176:177], s[26:27], 0, v[130:131]
	s_add_i32 m0, s28, 0x2000
	s_nop 0
	global_load_lds_dwordx4 v[176:177], off
	v_lshl_add_u64 v[176:177], v[180:181], 0, s[10:11]
	s_mov_b32 m0, s52
	s_nop 0
	global_load_lds_dwordx4 v[176:177], off
	v_lshl_add_u64 v[176:177], v[182:183], 0, s[10:11]
	s_mov_b32 m0, s53
	s_nop 0
	global_load_lds_dwordx4 v[176:177], off
	s_waitcnt vmcnt(8)
	s_waitcnt lgkmcnt(0)
	v_mfma_f32_16x16x32_bf16 v[62:65], v[140:143], v[188:191], v[62:65]
	v_mfma_f32_16x16x32_bf16 v[58:61], v[156:159], v[188:191], v[58:61]
	v_mfma_f32_16x16x32_bf16 v[54:57], v[140:143], v[196:199], v[54:57]
	s_barrier
	s_setprio 1
	s_waitcnt lgkmcnt(0)
	v_mfma_f32_16x16x32_bf16 v[46:49], v[156:159], v[196:199], v[46:49]
	v_mfma_f32_16x16x32_bf16 v[38:41], v[140:143], v[204:207], v[38:41]
	v_mfma_f32_16x16x32_bf16 v[30:33], v[156:159], v[204:207], v[30:33]
	v_mfma_f32_16x16x32_bf16 v[22:25], v[140:143], v[212:215], v[22:25]
	v_mfma_f32_16x16x32_bf16 v[14:17], v[156:159], v[212:215], v[14:17]
	v_mfma_f32_16x16x32_bf16 v[62:65], v[152:155], v[192:195], v[62:65]
	v_mfma_f32_16x16x32_bf16 v[58:61], v[160:163], v[192:195], v[58:61]
	v_mfma_f32_16x16x32_bf16 v[54:57], v[152:155], v[200:203], v[54:57]
	v_mfma_f32_16x16x32_bf16 v[46:49], v[160:163], v[200:203], v[46:49]
	v_mfma_f32_16x16x32_bf16 v[38:41], v[152:155], v[208:211], v[38:41]
	v_mfma_f32_16x16x32_bf16 v[30:33], v[160:163], v[208:211], v[30:33]
	v_mfma_f32_16x16x32_bf16 v[22:25], v[152:155], v[216:219], v[22:25]
	v_mfma_f32_16x16x32_bf16 v[14:17], v[160:163], v[216:219], v[14:17]
	s_setprio 0
	s_setprio 1
	v_mfma_f32_16x16x32_bf16 v[50:53], v[164:167], v[188:191], v[50:53]
	v_mfma_f32_16x16x32_bf16 v[42:45], v[172:175], v[188:191], v[42:45]
	v_mfma_f32_16x16x32_bf16 v[34:37], v[164:167], v[196:199], v[34:37]
	v_mfma_f32_16x16x32_bf16 v[26:29], v[172:175], v[196:199], v[26:29]
	v_mfma_f32_16x16x32_bf16 v[18:21], v[164:167], v[204:207], v[18:21]
	v_mfma_f32_16x16x32_bf16 v[10:13], v[172:175], v[204:207], v[10:13]
	v_mfma_f32_16x16x32_bf16 v[6:9], v[164:167], v[212:215], v[6:9]
	v_mfma_f32_16x16x32_bf16 v[2:5], v[172:175], v[212:215], v[2:5]
	v_mfma_f32_16x16x32_bf16 v[50:53], v[168:171], v[192:195], v[50:53]
	v_mfma_f32_16x16x32_bf16 v[42:45], v[184:187], v[192:195], v[42:45]
	v_mfma_f32_16x16x32_bf16 v[34:37], v[168:171], v[200:203], v[34:37]
	v_mfma_f32_16x16x32_bf16 v[26:29], v[184:187], v[200:203], v[26:29]
	v_mfma_f32_16x16x32_bf16 v[18:21], v[168:171], v[208:211], v[18:21]
	v_mfma_f32_16x16x32_bf16 v[10:13], v[184:187], v[208:211], v[10:13]
	v_mfma_f32_16x16x32_bf16 v[6:9], v[168:171], v[216:219], v[6:9]
	v_mfma_f32_16x16x32_bf16 v[2:5], v[184:187], v[216:219], v[2:5]
	s_setprio 0
	s_barrier
	s_add_i32 s59, s59, 2
	s_add_u32 s24, s24, 0x100
	s_addc_u32 s25, s25, 0
	s_add_u32 s57, s57, 0x100
	s_addc_u32 s58, s58, 0
	s_cmp_gt_u32 s59, 5
	s_cbranch_scc0 .LBB0_1227
	s_and_b64 vcc, exec, s[8:9]
	s_cbranch_vccz .LBB0_1230
	s_barrier

; #define PG8_STAGE(bufoff, gbase, voff) do { _Pragma("unroll") for (int _i = 0; _i < 2; ++_i) \
;         __builtin_amdgcn_global_load_lds((const unsigned*)((const char*)(gbase) + (voff)[_i]), (PG8_LAS unsigned*)(lds + (bufoff) + ldsw + _i * 8192), 16, 0, 0); } while (0)
; #define PG8_LDA(dst, b, h) do { _Pragma("unroll") for (int m = 0; m < 4; ++m) _Pragma("unroll") for (int k = 0; k < 2; ++k) dst[m][k] = *(const PG8_LAS bf16x8*)(lds + PG8_SA(b, h) + aoff + m * 2048 + k * 1024); } while (0)
; #define PG8_LDB(dst, b, h) do { _Pragma("unroll") for (int n = 0; n < 2; ++n) _Pragma("unroll") for (int k = 0; k < 2; ++k) dst[n][k] = *(const PG8_LAS bf16x8*)(lds + PG8_SB(b, h) + boff + n * 2048 + k * 1024); } while (0)
; #define PG8_WAIT_V(n) asm volatile("s_waitcnt vmcnt(" #n ")" ::: "memory")
; #define PG8_WAIT_L(n) asm volatile("s_waitcnt lgkmcnt(" #n ")" ::: "memory")
; #define PG8_BAR __builtin_amdgcn_s_barrier()
; #define PG8_SCHED __builtin_amdgcn_sched_barrier(0)
; template <class Epi, class Sched, bool ALIGN_EPI = false, bool SP2 = false, bool GATHER = false>
; __device__ __forceinline__ void gemm_phase(PG8_LAS unsigned char* lds, const Gemm g, const Sched& S, const Epi& E, int tid_in, const int* rowsrc = nullptr, PG8_LAS int* idx_lds = nullptr) {
;     ...
;             PG8_LDB(B0, 0, 0); PG8_LDB(B1, 0, 1); PG8_SCHED; PG8_LDA(At, 0, 0); PG8_STAGE(PG8_SA(1, 1), a1 + hstepA, PG8_OA(1));
;             PG8_WAIT_V(8); PG8_WAIT_L(0); PG8_BAR; PG8_MMA(0, 0, At, B0); PG8_MMA(0, 1, At, B1); PG8_BAR; PG8_SCHED;
;             PG8_LDA(At, 0, 1); PG8_STAGE(PG8_SB(0, 0), b2, voffB); PG8_STAGE(PG8_SB(0, 1), b2 + hstep, voffB); PG8_STAGE(PG8_SA(0, 0), a2, PG8_OS(0));
;             PG8_WAIT_V(8); PG8_WAIT_L(0); PG8_BAR; PG8_MMA(1, 0, At, B0); PG8_MMA(1, 1, At, B1); PG8_BAR; PG8_SCHED;
;             PG8_LDB(B0, 1, 0); PG8_LDB(B1, 1, 1); PG8_SCHED; PG8_LDA(At, 1, 0); PG8_STAGE(PG8_SA(0, 1), a2 + hstepA, PG8_OS(1));
;             PG8_WAIT_V(8); PG8_WAIT_L(0); PG8_BAR; PG8_MMA(0, 0, At, B0); PG8_MMA(0, 1, At, B1); PG8_BAR; PG8_SCHED;
;             PG8_LDA(At, 1, 1); PG8_STAGE(PG8_SB(1, 0), b3, voffB); PG8_STAGE(PG8_SB(1, 1), b3 + hstep, voffB); PG8_STAGE(PG8_SA(1, 0), a3, PG8_OS(0));
;             PG8_WAIT_V(8); PG8_WAIT_L(0); PG8_BAR; PG8_MMA(1, 0, At, B0); PG8_MMA(1, 1, At, B1); PG8_BAR; PG8_SCHED;
.LBB0_1245:
	s_add_u32 s31, s24, s30
	s_addc_u32 s38, s25, 0
	s_add_u32 s36, s31, 0x100
	s_addc_u32 s37, s38, 0
	s_and_b64 s[34:35], s[28:29], exec
	s_cselect_b32 s35, s15, s37
	s_cselect_b32 s34, s61, s36
	s_add_u32 s30, s22, s30
	s_addc_u32 s36, s23, 0
	s_add_u32 s30, s30, 0x100
	s_addc_u32 s36, s36, 0
	s_add_i32 s71, 0, 0x10000
	s_and_b64 s[28:29], s[28:29], exec
	s_cselect_b32 s37, s13, s36
	s_cselect_b32 s36, s62, s30
	s_add_i32 s29, 0, 0x14000
	s_add_u32 s40, s31, 0x40080
	s_addc_u32 s41, s38, 0
	s_add_i32 s70, s71, s2
	s_add_i32 m0, s21, 0xc000
	s_add_i32 s73, s21, 0xe000
	s_add_i32 s67, s70, 0x2000
	v_add_u32_e32 v136, s71, v139
	s_add_u32 s38, s36, 0x10000
	ds_read_b128 v[142:145], v136
	ds_read_b128 v[148:151], v136 offset:1024
	ds_read_b128 v[152:155], v136 offset:2048
	ds_read_b128 v[156:159], v136 offset:3072
	v_add_u32_e32 v136, s29, v139
	s_addc_u32 s39, s37, 0
	s_add_i32 s69, s29, s2
	ds_read_b128 v[160:163], v136
	ds_read_b128 v[164:167], v136 offset:1024
	ds_read_b128 v[168:171], v136 offset:2048
	ds_read_b128 v[172:175], v136 offset:3072
	s_add_i32 s68, s69, 0x2000
	s_add_i32 s66, 0, 0x18000
	s_add_i32 s65, 0, 0x1c000
	s_add_u32 s30, s34, 0x40000
	s_addc_u32 s31, s35, 0
	s_add_i32 s64, s66, s2
	s_add_i32 s63, s64, 0x2000
	s_add_u32 s28, s36, 0x10080
	s_addc_u32 s29, s37, 0
	s_add_i32 s72, s65, s2
	s_add_i32 s71, s72, 0x2000
	v_lshl_add_u64 v[136:137], s[40:41], 0, v[134:135]
	ds_read_b128 v[184:187], v141
	ds_read_b128 v[188:191], v141 offset:1024
	ds_read_b128 v[192:195], v141 offset:2048
	ds_read_b128 v[196:199], v141 offset:3072
	ds_read_b128 v[200:203], v141 offset:4096
	ds_read_b128 v[204:207], v141 offset:5120
	ds_read_b128 v[208:211], v141 offset:6144
	ds_read_b128 v[212:215], v141 offset:7168
	global_load_lds_dwordx4 v[136:137], off
	v_lshl_add_u64 v[136:137], s[40:41], 0, v[132:133]
	s_mov_b32 m0, s73
	s_nop 0
	global_load_lds_dwordx4 v[136:137], off
	s_waitcnt vmcnt(8)
	s_waitcnt lgkmcnt(0)
	v_mfma_f32_16x16x32_bf16 v[126:129], v[142:145], v[184:187], v[126:129]
	v_mfma_f32_16x16x32_bf16 v[122:125], v[152:155], v[184:187], v[122:125]
	v_mfma_f32_16x16x32_bf16 v[118:121], v[142:145], v[192:195], v[118:121]
	s_barrier
	s_setprio 1
	s_waitcnt lgkmcnt(0)
	v_mfma_f32_16x16x32_bf16 v[110:113], v[152:155], v[192:195], v[110:113]
	v_mfma_f32_16x16x32_bf16 v[102:105], v[142:145], v[200:203], v[102:105]
	v_mfma_f32_16x16x32_bf16 v[94:97], v[152:155], v[200:203], v[94:97]
	v_mfma_f32_16x16x32_bf16 v[86:89], v[142:145], v[208:211], v[86:89]
	v_mfma_f32_16x16x32_bf16 v[78:81], v[152:155], v[208:211], v[78:81]
	v_mfma_f32_16x16x32_bf16 v[126:129], v[148:151], v[188:191], v[126:129]
	v_mfma_f32_16x16x32_bf16 v[122:125], v[156:159], v[188:191], v[122:125]
	v_mfma_f32_16x16x32_bf16 v[118:121], v[148:151], v[196:199], v[118:121]
	v_mfma_f32_16x16x32_bf16 v[110:113], v[156:159], v[196:199], v[110:113]
	v_mfma_f32_16x16x32_bf16 v[102:105], v[148:151], v[204:207], v[102:105]
	v_mfma_f32_16x16x32_bf16 v[94:97], v[156:159], v[204:207], v[94:97]
	v_mfma_f32_16x16x32_bf16 v[86:89], v[148:151], v[212:215], v[86:89]
	v_mfma_f32_16x16x32_bf16 v[78:81], v[156:159], v[212:215], v[78:81]
	s_setprio 0
	s_setprio 1
	v_mfma_f32_16x16x32_bf16 v[114:117], v[160:163], v[184:187], v[114:117]
	v_mfma_f32_16x16x32_bf16 v[106:109], v[168:171], v[184:187], v[106:109]
	v_mfma_f32_16x16x32_bf16 v[98:101], v[160:163], v[192:195], v[98:101]
	v_mfma_f32_16x16x32_bf16 v[90:93], v[168:171], v[192:195], v[90:93]
	v_mfma_f32_16x16x32_bf16 v[82:85], v[160:163], v[200:203], v[82:85]
	v_mfma_f32_16x16x32_bf16 v[74:77], v[168:171], v[200:203], v[74:77]
	v_mfma_f32_16x16x32_bf16 v[70:73], v[160:163], v[208:211], v[70:73]
	v_mfma_f32_16x16x32_bf16 v[66:69], v[168:171], v[208:211], v[66:69]
	v_mfma_f32_16x16x32_bf16 v[114:117], v[164:167], v[188:191], v[114:117]
	v_mfma_f32_16x16x32_bf16 v[106:109], v[172:175], v[188:191], v[106:109]
	v_mfma_f32_16x16x32_bf16 v[98:101], v[164:167], v[196:199], v[98:101]
	v_mfma_f32_16x16x32_bf16 v[90:93], v[172:175], v[196:199], v[90:93]
	v_mfma_f32_16x16x32_bf16 v[82:85], v[164:167], v[204:207], v[82:85]
	v_mfma_f32_16x16x32_bf16 v[74:77], v[172:175], v[204:207], v[74:77]
	v_mfma_f32_16x16x32_bf16 v[70:73], v[164:167], v[212:215], v[70:73]
	v_mfma_f32_16x16x32_bf16 v[66:69], v[172:175], v[212:215], v[66:69]
	s_setprio 0
	s_barrier
	s_mov_b32 m0, s70
	v_lshl_add_u64 v[136:137], s[36:37], 0, v[0:1]
	ds_read_b128 v[184:187], v141 offset:16384
	ds_read_b128 v[188:191], v141 offset:17408
	ds_read_b128 v[192:195], v141 offset:18432
	ds_read_b128 v[196:199], v141 offset:19456
	ds_read_b128 v[200:203], v141 offset:20480
	ds_read_b128 v[204:207], v141 offset:21504
	ds_read_b128 v[208:211], v141 offset:22528
	ds_read_b128 v[212:215], v141 offset:23552
	global_load_lds_dwordx4 v[136:137], off
	v_lshl_add_u64 v[176:177], s[36:37], 0, v[130:131]
	s_mov_b32 m0, s67
	v_lshl_add_u64 v[178:179], s[38:39], 0, v[0:1]
	global_load_lds_dwordx4 v[176:177], off
	s_mov_b32 m0, s69
	v_lshl_add_u64 v[180:181], s[34:35], 0, v[132:133]
	global_load_lds_dwordx4 v[178:179], off
	v_lshl_add_u64 v[178:179], s[38:39], 0, v[130:131]
	s_mov_b32 m0, s68
	s_nop 0
	global_load_lds_dwordx4 v[178:179], off
	v_lshl_add_u64 v[178:179], s[34:35], 0, v[134:135]
	s_mov_b32 m0, s21
	s_nop 0
	global_load_lds_dwordx4 v[178:179], off
	s_mov_b32 m0, s54
	s_nop 0
	global_load_lds_dwordx4 v[180:181], off
	s_waitcnt vmcnt(8)
	s_waitcnt lgkmcnt(0)
	v_mfma_f32_16x16x32_bf16 v[62:65], v[142:145], v[184:187], v[62:65]
	v_mfma_f32_16x16x32_bf16 v[58:61], v[152:155], v[184:187], v[58:61]
	v_mfma_f32_16x16x32_bf16 v[54:57], v[142:145], v[192:195], v[54:57]
	s_barrier
; #define PG8_STAGE(bufoff, gbase, voff) do { _Pragma("unroll") for (int _i = 0; _i < 2; ++_i) \
;         __builtin_amdgcn_global_load_lds((const unsigned*)((const char*)(gbase) + (voff)[_i]), (PG8_LAS unsigned*)(lds + (bufoff) + ldsw + _i * 8192), 16, 0, 0); } while (0)
; #define PG8_LDA(dst, b, h) do { _Pragma("unroll") for (int m = 0; m < 4; ++m) _Pragma("unroll") for (int k = 0; k < 2; ++k) dst[m][k] = *(const PG8_LAS bf16x8*)(lds + PG8_SA(b, h) + aoff + m * 2048 + k * 1024); } while (0)
; #define PG8_LDB(dst, b, h) do { _Pragma("unroll") for (int n = 0; n < 2; ++n) _Pragma("unroll") for (int k = 0; k < 2; ++k) dst[n][k] = *(const PG8_LAS bf16x8*)(lds + PG8_SB(b, h) + boff + n * 2048 + k * 1024); } while (0)
; #define PG8_WAIT_V(n) asm volatile("s_waitcnt vmcnt(" #n ")" ::: "memory")
; #define PG8_WAIT_L(n) asm volatile("s_waitcnt lgkmcnt(" #n ")" ::: "memory")
; #define PG8_BAR __builtin_amdgcn_s_barrier()
; #define PG8_SCHED __builtin_amdgcn_sched_barrier(0)
; template <class Epi, class Sched, bool ALIGN_EPI = false, bool SP2 = false, bool GATHER = false>
; __device__ __forceinline__ void gemm_phase(PG8_LAS unsigned char* lds, const Gemm g, const Sched& S, const Epi& E, int tid_in, const int* rowsrc = nullptr, PG8_LAS int* idx_lds = nullptr) {
;     ...
;             PG8_LDB(B0, 0, 0); PG8_LDB(B1, 0, 1); PG8_SCHED; PG8_LDA(At, 0, 0); PG8_STAGE(PG8_SA(1, 1), a1 + hstepA, PG8_OA(1));
;             PG8_WAIT_V(8); PG8_WAIT_L(0); PG8_BAR; PG8_MMA(0, 0, At, B0); PG8_MMA(0, 1, At, B1); PG8_BAR; PG8_SCHED;
;             PG8_LDA(At, 0, 1); PG8_STAGE(PG8_SB(0, 0), b2, voffB); PG8_STAGE(PG8_SB(0, 1), b2 + hstep, voffB); PG8_STAGE(PG8_SA(0, 0), a2, PG8_OS(0));
;             PG8_WAIT_V(8); PG8_WAIT_L(0); PG8_BAR; PG8_MMA(1, 0, At, B0); PG8_MMA(1, 1, At, B1); PG8_BAR; PG8_SCHED;
;             PG8_LDB(B0, 1, 0); PG8_LDB(B1, 1, 1); PG8_SCHED; PG8_LDA(At, 1, 0); PG8_STAGE(PG8_SA(0, 1), a2 + hstepA, PG8_OS(1));
;             PG8_WAIT_V(8); PG8_WAIT_L(0); PG8_BAR; PG8_MMA(0, 0, At, B0); PG8_MMA(0, 1, At, B1); PG8_BAR; PG8_SCHED;
;             PG8_LDA(At, 1, 1); PG8_STAGE(PG8_SB(1, 0), b3, voffB); PG8_STAGE(PG8_SB(1, 1), b3 + hstep, voffB); PG8_STAGE(PG8_SA(1, 0), a3, PG8_OS(0));
;             PG8_WAIT_V(8); PG8_WAIT_L(0); PG8_BAR; PG8_MMA(1, 0, At, B0); PG8_MMA(1, 1, At, B1); PG8_BAR; PG8_SCHED;
	s_setprio 1
	s_waitcnt lgkmcnt(0)
	v_mfma_f32_16x16x32_bf16 v[46:49], v[152:155], v[192:195], v[46:49]
	v_mfma_f32_16x16x32_bf16 v[38:41], v[142:145], v[200:203], v[38:41]
	v_mfma_f32_16x16x32_bf16 v[30:33], v[152:155], v[200:203], v[30:33]
	v_mfma_f32_16x16x32_bf16 v[22:25], v[142:145], v[208:211], v[22:25]
	v_mfma_f32_16x16x32_bf16 v[14:17], v[152:155], v[208:211], v[14:17]
	v_mfma_f32_16x16x32_bf16 v[62:65], v[148:151], v[188:191], v[62:65]
	v_mfma_f32_16x16x32_bf16 v[58:61], v[156:159], v[188:191], v[58:61]
	v_mfma_f32_16x16x32_bf16 v[54:57], v[148:151], v[196:199], v[54:57]
	v_mfma_f32_16x16x32_bf16 v[46:49], v[156:159], v[196:199], v[46:49]
	v_mfma_f32_16x16x32_bf16 v[38:41], v[148:151], v[204:207], v[38:41]
	v_mfma_f32_16x16x32_bf16 v[30:33], v[156:159], v[204:207], v[30:33]
	v_mfma_f32_16x16x32_bf16 v[22:25], v[148:151], v[212:215], v[22:25]
	v_mfma_f32_16x16x32_bf16 v[14:17], v[156:159], v[212:215], v[14:17]
	s_setprio 0
	s_setprio 1
	v_mfma_f32_16x16x32_bf16 v[50:53], v[160:163], v[184:187], v[50:53]
	v_mfma_f32_16x16x32_bf16 v[42:45], v[168:171], v[184:187], v[42:45]
	v_mfma_f32_16x16x32_bf16 v[34:37], v[160:163], v[192:195], v[34:37]
	v_mfma_f32_16x16x32_bf16 v[26:29], v[168:171], v[192:195], v[26:29]
	v_mfma_f32_16x16x32_bf16 v[18:21], v[160:163], v[200:203], v[18:21]
	v_mfma_f32_16x16x32_bf16 v[10:13], v[168:171], v[200:203], v[10:13]
	v_mfma_f32_16x16x32_bf16 v[6:9], v[160:163], v[208:211], v[6:9]
	v_mfma_f32_16x16x32_bf16 v[2:5], v[168:171], v[208:211], v[2:5]
	v_mfma_f32_16x16x32_bf16 v[50:53], v[164:167], v[188:191], v[50:53]
	v_mfma_f32_16x16x32_bf16 v[42:45], v[172:175], v[188:191], v[42:45]
	v_mfma_f32_16x16x32_bf16 v[34:37], v[164:167], v[196:199], v[34:37]
	v_mfma_f32_16x16x32_bf16 v[26:29], v[172:175], v[196:199], v[26:29]
	v_mfma_f32_16x16x32_bf16 v[18:21], v[164:167], v[204:207], v[18:21]
	v_mfma_f32_16x16x32_bf16 v[10:13], v[172:175], v[204:207], v[10:13]
	v_mfma_f32_16x16x32_bf16 v[6:9], v[164:167], v[212:215], v[6:9]
	v_mfma_f32_16x16x32_bf16 v[2:5], v[172:175], v[212:215], v[2:5]
	s_setprio 0
	s_barrier
	v_add_u32_e32 v156, s66, v139
	v_add_u32_e32 v172, s65, v139
	ds_read_b128 v[142:145], v156
	ds_read_b128 v[148:151], v156 offset:1024
	ds_read_b128 v[152:155], v156 offset:2048
	ds_read_b128 v[156:159], v156 offset:3072
	ds_read_b128 v[160:163], v172
	ds_read_b128 v[164:167], v172 offset:1024
	ds_read_b128 v[168:171], v172 offset:2048
	ds_read_b128 v[172:175], v172 offset:3072
	s_mov_b32 m0, s55
	v_lshl_add_u64 v[182:183], s[30:31], 0, v[134:135]
	ds_read_b128 v[184:187], v141 offset:32768
	ds_read_b128 v[188:191], v141 offset:33792
	ds_read_b128 v[192:195], v141 offset:34816
	ds_read_b128 v[196:199], v141 offset:35840
	ds_read_b128 v[200:203], v141 offset:36864
	ds_read_b128 v[204:207], v141 offset:37888
	ds_read_b128 v[208:211], v141 offset:38912
	ds_read_b128 v[212:215], v141 offset:39936
	global_load_lds_dwordx4 v[182:183], off
	v_lshl_add_u64 v[182:183], s[30:31], 0, v[132:133]
	s_mov_b32 m0, s56
	s_nop 0
	global_load_lds_dwordx4 v[182:183], off
	s_waitcnt vmcnt(8)
	s_waitcnt lgkmcnt(0)
	v_mfma_f32_16x16x32_bf16 v[126:129], v[142:145], v[184:187], v[126:129]
	v_mfma_f32_16x16x32_bf16 v[122:125], v[152:155], v[184:187], v[122:125]
	v_mfma_f32_16x16x32_bf16 v[118:121], v[142:145], v[192:195], v[118:121]
	s_barrier
	s_setprio 1
	s_waitcnt lgkmcnt(0)
	v_mfma_f32_16x16x32_bf16 v[110:113], v[152:155], v[192:195], v[110:113]
	v_mfma_f32_16x16x32_bf16 v[102:105], v[142:145], v[200:203], v[102:105]
	v_mfma_f32_16x16x32_bf16 v[94:97], v[152:155], v[200:203], v[94:97]
	v_mfma_f32_16x16x32_bf16 v[86:89], v[142:145], v[208:211], v[86:89]
	v_mfma_f32_16x16x32_bf16 v[78:81], v[152:155], v[208:211], v[78:81]
	v_mfma_f32_16x16x32_bf16 v[126:129], v[148:151], v[188:191], v[126:129]
	v_mfma_f32_16x16x32_bf16 v[122:125], v[156:159], v[188:191], v[122:125]
	v_mfma_f32_16x16x32_bf16 v[118:121], v[148:151], v[196:199], v[118:121]
	v_mfma_f32_16x16x32_bf16 v[110:113], v[156:159], v[196:199], v[110:113]
	v_mfma_f32_16x16x32_bf16 v[102:105], v[148:151], v[204:207], v[102:105]
	v_mfma_f32_16x16x32_bf16 v[94:97], v[156:159], v[204:207], v[94:97]
	v_mfma_f32_16x16x32_bf16 v[86:89], v[148:151], v[212:215], v[86:89]
	v_mfma_f32_16x16x32_bf16 v[78:81], v[156:159], v[212:215], v[78:81]
	s_setprio 0
	s_setprio 1
	v_mfma_f32_16x16x32_bf16 v[114:117], v[160:163], v[184:187], v[114:117]
	v_mfma_f32_16x16x32_bf16 v[106:109], v[168:171], v[184:187], v[106:109]
	v_mfma_f32_16x16x32_bf16 v[98:101], v[160:163], v[192:195], v[98:101]
	v_mfma_f32_16x16x32_bf16 v[90:93], v[168:171], v[192:195], v[90:93]
	v_mfma_f32_16x16x32_bf16 v[82:85], v[160:163], v[200:203], v[82:85]
	v_mfma_f32_16x16x32_bf16 v[74:77], v[168:171], v[200:203], v[74:77]
	v_mfma_f32_16x16x32_bf16 v[70:73], v[160:163], v[208:211], v[70:73]
	v_mfma_f32_16x16x32_bf16 v[66:69], v[168:171], v[208:211], v[66:69]
	v_mfma_f32_16x16x32_bf16 v[114:117], v[164:167], v[188:191], v[114:117]
	v_mfma_f32_16x16x32_bf16 v[106:109], v[172:175], v[188:191], v[106:109]
	v_mfma_f32_16x16x32_bf16 v[98:101], v[164:167], v[196:199], v[98:101]
	v_mfma_f32_16x16x32_bf16 v[90:93], v[172:175], v[196:199], v[90:93]
	v_mfma_f32_16x16x32_bf16 v[82:85], v[164:167], v[204:207], v[82:85]
	v_mfma_f32_16x16x32_bf16 v[74:77], v[172:175], v[204:207], v[74:77]
	v_mfma_f32_16x16x32_bf16 v[70:73], v[164:167], v[212:215], v[70:73]
	v_mfma_f32_16x16x32_bf16 v[66:69], v[172:175], v[212:215], v[66:69]
	s_setprio 0
	s_barrier
; #define PG8_STAGE(bufoff, gbase, voff) do { _Pragma("unroll") for (int _i = 0; _i < 2; ++_i) \
;         __builtin_amdgcn_global_load_lds((const unsigned*)((const char*)(gbase) + (voff)[_i]), (PG8_LAS unsigned*)(lds + (bufoff) + ldsw + _i * 8192), 16, 0, 0); } while (0)
; #define PG8_LDA(dst, b, h) do { _Pragma("unroll") for (int m = 0; m < 4; ++m) _Pragma("unroll") for (int k = 0; k < 2; ++k) dst[m][k] = *(const PG8_LAS bf16x8*)(lds + PG8_SA(b, h) + aoff + m * 2048 + k * 1024); } while (0)
; #define PG8_MMA(ai, bj, At, Bt) do { __builtin_amdgcn_s_setprio(1); _Pragma("unroll") for (int m = 0; m < 4; ++m) _Pragma("unroll") for (int n = 0; n < 2; ++n) _Pragma("unroll") for (int k = 0; k < 2; ++k) \
;         acc[ai][bj][m][n] = __builtin_amdgcn_mfma_f32_16x16x32_bf16(Bt[n][k], At[m][k], acc[ai][bj][m][n], 0, 0, 0); __builtin_amdgcn_s_setprio(0); } while (0)
; #define PG8_WAIT_V(n) asm volatile("s_waitcnt vmcnt(" #n ")" ::: "memory")
; #define PG8_WAIT_L(n) asm volatile("s_waitcnt lgkmcnt(" #n ")" ::: "memory")
; #define PG8_BAR __builtin_amdgcn_s_barrier()
; #define PG8_SCHED __builtin_amdgcn_sched_barrier(0)
; template <class Epi, class Sched, bool ALIGN_EPI = false, bool SP2 = false, bool GATHER = false>
; __device__ __forceinline__ void gemm_phase(PG8_LAS unsigned char* lds, const Gemm g, const Sched& S, const Epi& E, int tid_in, const int* rowsrc = nullptr, PG8_LAS int* idx_lds = nullptr) {
;     ...
;             PG8_LDA(At, 1, 1); PG8_STAGE(PG8_SB(1, 0), b3, voffB); PG8_STAGE(PG8_SB(1, 1), b3 + hstep, voffB); PG8_STAGE(PG8_SA(1, 0), a3, PG8_OS(0));
;             PG8_WAIT_V(8); PG8_WAIT_L(0); PG8_BAR; PG8_MMA(1, 0, At, B0); PG8_MMA(1, 1, At, B1); PG8_BAR; PG8_SCHED;
;     ...
;         if constexpr (ALIGN_EPI) { if (wr == 0) PG8_BAR; }
	s_mov_b32 m0, s64
	v_lshl_add_u64 v[136:137], v[136:137], 0, s[10:11]
	ds_read_b128 v[184:187], v141 offset:49152
	ds_read_b128 v[188:191], v141 offset:50176
	ds_read_b128 v[192:195], v141 offset:51200
	ds_read_b128 v[196:199], v141 offset:52224
	ds_read_b128 v[200:203], v141 offset:53248
	ds_read_b128 v[204:207], v141 offset:54272
	ds_read_b128 v[208:211], v141 offset:55296
	ds_read_b128 v[212:215], v141 offset:56320
	global_load_lds_dwordx4 v[136:137], off
	v_lshl_add_u64 v[136:137], v[176:177], 0, s[10:11]
	s_mov_b32 m0, s63
	s_nop 0
	global_load_lds_dwordx4 v[136:137], off
	v_lshl_add_u64 v[136:137], s[28:29], 0, v[0:1]
	s_mov_b32 m0, s72
	s_nop 0
	global_load_lds_dwordx4 v[136:137], off
	v_lshl_add_u64 v[136:137], s[28:29], 0, v[130:131]
	s_mov_b32 m0, s71
	s_nop 0
	global_load_lds_dwordx4 v[136:137], off
	v_lshl_add_u64 v[136:137], v[178:179], 0, s[10:11]
	s_mov_b32 m0, s57
	s_nop 0
	global_load_lds_dwordx4 v[136:137], off
	v_lshl_add_u64 v[136:137], v[180:181], 0, s[10:11]
	s_mov_b32 m0, s58
	s_nop 0
	global_load_lds_dwordx4 v[136:137], off
	s_waitcnt vmcnt(8)
	s_waitcnt lgkmcnt(0)
	v_mfma_f32_16x16x32_bf16 v[62:65], v[142:145], v[184:187], v[62:65]
	v_mfma_f32_16x16x32_bf16 v[58:61], v[152:155], v[184:187], v[58:61]
	v_mfma_f32_16x16x32_bf16 v[54:57], v[142:145], v[192:195], v[54:57]
	s_barrier
	s_setprio 1
	s_waitcnt lgkmcnt(0)
	v_mfma_f32_16x16x32_bf16 v[46:49], v[152:155], v[192:195], v[46:49]
	v_mfma_f32_16x16x32_bf16 v[38:41], v[142:145], v[200:203], v[38:41]
	v_mfma_f32_16x16x32_bf16 v[30:33], v[152:155], v[200:203], v[30:33]
	v_mfma_f32_16x16x32_bf16 v[22:25], v[142:145], v[208:211], v[22:25]
	v_mfma_f32_16x16x32_bf16 v[14:17], v[152:155], v[208:211], v[14:17]
	v_mfma_f32_16x16x32_bf16 v[62:65], v[148:151], v[188:191], v[62:65]
	v_mfma_f32_16x16x32_bf16 v[58:61], v[156:159], v[188:191], v[58:61]
	v_mfma_f32_16x16x32_bf16 v[54:57], v[148:151], v[196:199], v[54:57]
	v_mfma_f32_16x16x32_bf16 v[46:49], v[156:159], v[196:199], v[46:49]
	v_mfma_f32_16x16x32_bf16 v[38:41], v[148:151], v[204:207], v[38:41]
	v_mfma_f32_16x16x32_bf16 v[30:33], v[156:159], v[204:207], v[30:33]
	v_mfma_f32_16x16x32_bf16 v[22:25], v[148:151], v[212:215], v[22:25]
	v_mfma_f32_16x16x32_bf16 v[14:17], v[156:159], v[212:215], v[14:17]
	s_setprio 0
	s_setprio 1
	v_mfma_f32_16x16x32_bf16 v[50:53], v[160:163], v[184:187], v[50:53]
	v_mfma_f32_16x16x32_bf16 v[42:45], v[168:171], v[184:187], v[42:45]
	v_mfma_f32_16x16x32_bf16 v[34:37], v[160:163], v[192:195], v[34:37]
	v_mfma_f32_16x16x32_bf16 v[26:29], v[168:171], v[192:195], v[26:29]
	v_mfma_f32_16x16x32_bf16 v[18:21], v[160:163], v[200:203], v[18:21]
	v_mfma_f32_16x16x32_bf16 v[10:13], v[168:171], v[200:203], v[10:13]
	v_mfma_f32_16x16x32_bf16 v[6:9], v[160:163], v[208:211], v[6:9]
	v_mfma_f32_16x16x32_bf16 v[2:5], v[168:171], v[208:211], v[2:5]
	v_mfma_f32_16x16x32_bf16 v[50:53], v[164:167], v[188:191], v[50:53]
	v_mfma_f32_16x16x32_bf16 v[42:45], v[172:175], v[188:191], v[42:45]
	v_mfma_f32_16x16x32_bf16 v[34:37], v[164:167], v[196:199], v[34:37]
	v_mfma_f32_16x16x32_bf16 v[26:29], v[172:175], v[196:199], v[26:29]
	v_mfma_f32_16x16x32_bf16 v[18:21], v[164:167], v[204:207], v[18:21]
	v_mfma_f32_16x16x32_bf16 v[10:13], v[172:175], v[204:207], v[10:13]
	v_mfma_f32_16x16x32_bf16 v[6:9], v[164:167], v[212:215], v[6:9]
	v_mfma_f32_16x16x32_bf16 v[2:5], v[172:175], v[212:215], v[2:5]
	s_setprio 0
	s_barrier
	s_movk_i32 s30, 0x100
	s_andn2_b64 vcc, exec, s[26:27]
	s_mov_b64 s[28:29], -1
	s_mov_b64 s[26:27], 0
	s_cbranch_vccz .LBB0_1245
	s_and_b64 vcc, exec, s[8:9]
	s_cbranch_vccz .LBB0_1248
	s_barrier

; #define PG8_STAGE(bufoff, gbase, voff) do { _Pragma("unroll") for (int _i = 0; _i < 2; ++_i) \
;         __builtin_amdgcn_global_load_lds((const unsigned*)((const char*)(gbase) + (voff)[_i]), (PG8_LAS unsigned*)(lds + (bufoff) + ldsw + _i * 8192), 16, 0, 0); } while (0)
; #define PG8_LDA(dst, b, h) do { _Pragma("unroll") for (int m = 0; m < 4; ++m) _Pragma("unroll") for (int k = 0; k < 2; ++k) dst[m][k] = *(const PG8_LAS bf16x8*)(lds + PG8_SA(b, h) + aoff + m * 2048 + k * 1024); } while (0)
; #define PG8_LDB(dst, b, h) do { _Pragma("unroll") for (int n = 0; n < 2; ++n) _Pragma("unroll") for (int k = 0; k < 2; ++k) dst[n][k] = *(const PG8_LAS bf16x8*)(lds + PG8_SB(b, h) + boff + n * 2048 + k * 1024); } while (0)
; #define PG8_WAIT_V(n) asm volatile("s_waitcnt vmcnt(" #n ")" ::: "memory")
; #define PG8_WAIT_L(n) asm volatile("s_waitcnt lgkmcnt(" #n ")" ::: "memory")
; #define PG8_BAR __builtin_amdgcn_s_barrier()
; template <class Epi, class Sched, bool ALIGN_EPI = false, bool SP2 = false, bool GATHER = false>
; __device__ __forceinline__ void gemm_phase(PG8_LAS unsigned char* lds, const Gemm g, const Sched& S, const Epi& E, int tid_in, const int* rowsrc = nullptr, PG8_LAS int* idx_lds = nullptr) {
;     ...
;         for (int t = 0; t < nt; t += 2) {
;             const bool last = (t == nt - 2);
;             if constexpr (GATHER) {
; #pragma unroll
;                 for (int h_ = 0; h_ < 2; ++h_) { gS[h_][0] = last ? gN[h_][0] : gA[h_][0]; gS[h_][1] = last ? gN[h_][1] : gA[h_][1]; } }
;             const char* a1 = cA + (size_t)(t + 1) * kstep;
;             const char* a2 = last ? nA : cA + (size_t)(t + 2) * kstep; const char* b2 = last ? nB : cB + (size_t)(t + 2) * kstep;
;             const char* a3 = a2 + kstep; const char* b3 = b2 + kstep;
;             if (last && has_next) S.a_ready(nxt);
;             if constexpr (SP2) {
;             PG8_LDB(B0, 0, 0); PG8_LDB(B1, 0, 1); PG8_SCHED; PG8_LDA(At, 0, 0); PG8_STAGE(PG8_SA(1, 1), a1 + hstepA, PG8_OA(1));
;             PG8_WAIT_V(8); PG8_WAIT_L(0); PG8_BAR; PG8_MMA(0, 0, At, B0); PG8_MMA(0, 1, At, B1); PG8_BAR; PG8_SCHED;
;             PG8_LDA(At, 0, 1); PG8_STAGE(PG8_SB(0, 0), b2, voffB); PG8_STAGE(PG8_SB(0, 1), b2 + hstep, voffB); PG8_STAGE(PG8_SA(0, 0), a2, PG8_OS(0));
;             PG8_WAIT_V(8); PG8_WAIT_L(0); PG8_BAR; PG8_MMA(1, 0, At, B0); PG8_MMA(1, 1, At, B1); PG8_BAR; PG8_SCHED;
.LBB0_1618:
	s_add_u32 s22, s20, 0xfffc0080
	s_addc_u32 s23, s21, -1
	s_add_i32 s57, 0, 0x10000
	s_cmp_eq_u32 s56, 12
	s_cselect_b32 s25, s9, s23
	s_cselect_b32 s24, s17, s22
	s_cselect_b32 s23, s7, s55
	s_cselect_b32 s22, s19, s54
	s_add_i32 s60, 0, 0x14000
	v_add_u32_e32 v142, s57, v184
	v_add_u32_e32 v178, s60, v184
	ds_read_b128 v[122:125], v142
	ds_read_b128 v[126:129], v142 offset:1024
	ds_read_b128 v[134:137], v142 offset:2048
	ds_read_b128 v[142:145], v142 offset:3072
	ds_read_b128 v[174:177], v178
	ds_read_b128 v[188:191], v178 offset:1024
	ds_read_b128 v[192:195], v178 offset:2048
	ds_read_b128 v[196:199], v178 offset:3072
	v_lshl_add_u64 v[178:179], s[20:21], 0, v[170:171]
	s_add_i32 m0, s39, 0xc000
	ds_read_b128 v[200:203], v186
	ds_read_b128 v[204:207], v186 offset:1024
	ds_read_b128 v[208:211], v186 offset:2048
	ds_read_b128 v[212:215], v186 offset:3072
	ds_read_b128 v[216:219], v186 offset:4096
	ds_read_b128 v[220:223], v186 offset:5120
	ds_read_b128 v[224:227], v186 offset:6144
	ds_read_b128 v[228:231], v186 offset:7168
	global_load_lds_dwordx4 v[178:179], off
	v_lshl_add_u64 v[178:179], s[20:21], 0, v[172:173]
	s_add_i32 m0, s39, 0xe000
	s_nop 0
	global_load_lds_dwordx4 v[178:179], off
	s_waitcnt vmcnt(8)
	s_waitcnt lgkmcnt(0)
	v_mfma_f32_16x16x32_bf16 v[138:141], v[122:125], v[200:203], v[138:141]
	v_mfma_f32_16x16x32_bf16 v[130:133], v[134:137], v[200:203], v[130:133]
	v_mfma_f32_16x16x32_bf16 v[118:121], v[122:125], v[208:211], v[118:121]
	s_barrier
	s_setprio 1
	s_waitcnt lgkmcnt(0)
	v_mfma_f32_16x16x32_bf16 v[106:109], v[134:137], v[208:211], v[106:109]
	v_mfma_f32_16x16x32_bf16 v[102:105], v[122:125], v[216:219], v[102:105]
	v_mfma_f32_16x16x32_bf16 v[90:93], v[134:137], v[216:219], v[90:93]
	v_mfma_f32_16x16x32_bf16 v[86:89], v[122:125], v[224:227], v[86:89]
	v_mfma_f32_16x16x32_bf16 v[74:77], v[134:137], v[224:227], v[74:77]
	v_mfma_f32_16x16x32_bf16 v[138:141], v[126:129], v[204:207], v[138:141]
	v_mfma_f32_16x16x32_bf16 v[130:133], v[142:145], v[204:207], v[130:133]
	v_mfma_f32_16x16x32_bf16 v[118:121], v[126:129], v[212:215], v[118:121]
	v_mfma_f32_16x16x32_bf16 v[106:109], v[142:145], v[212:215], v[106:109]
	v_mfma_f32_16x16x32_bf16 v[102:105], v[126:129], v[220:223], v[102:105]
	v_mfma_f32_16x16x32_bf16 v[90:93], v[142:145], v[220:223], v[90:93]
	v_mfma_f32_16x16x32_bf16 v[86:89], v[126:129], v[228:231], v[86:89]
	v_mfma_f32_16x16x32_bf16 v[74:77], v[142:145], v[228:231], v[74:77]
	s_setprio 0
	s_setprio 1
	v_mfma_f32_16x16x32_bf16 v[114:117], v[174:177], v[200:203], v[114:117]
	v_mfma_f32_16x16x32_bf16 v[110:113], v[192:195], v[200:203], v[110:113]
	v_mfma_f32_16x16x32_bf16 v[98:101], v[174:177], v[208:211], v[98:101]
	v_mfma_f32_16x16x32_bf16 v[94:97], v[192:195], v[208:211], v[94:97]
	v_mfma_f32_16x16x32_bf16 v[82:85], v[174:177], v[216:219], v[82:85]
	v_mfma_f32_16x16x32_bf16 v[78:81], v[192:195], v[216:219], v[78:81]
	v_mfma_f32_16x16x32_bf16 v[70:73], v[174:177], v[224:227], v[70:73]
	v_mfma_f32_16x16x32_bf16 v[66:69], v[192:195], v[224:227], v[66:69]
	v_mfma_f32_16x16x32_bf16 v[114:117], v[188:191], v[204:207], v[114:117]
	v_mfma_f32_16x16x32_bf16 v[110:113], v[196:199], v[204:207], v[110:113]
	v_mfma_f32_16x16x32_bf16 v[98:101], v[188:191], v[212:215], v[98:101]
	v_mfma_f32_16x16x32_bf16 v[94:97], v[196:199], v[212:215], v[94:97]
	v_mfma_f32_16x16x32_bf16 v[82:85], v[188:191], v[220:223], v[82:85]
	v_mfma_f32_16x16x32_bf16 v[78:81], v[196:199], v[220:223], v[78:81]
	v_mfma_f32_16x16x32_bf16 v[70:73], v[188:191], v[228:231], v[70:73]
	v_mfma_f32_16x16x32_bf16 v[66:69], v[196:199], v[228:231], v[66:69]
	s_setprio 0
	s_barrier
	s_add_i32 s57, s57, s38
	v_lshl_add_u64 v[178:179], s[22:23], 0, v[0:1]
	s_mov_b32 m0, s57
	ds_read_b128 v[200:203], v186 offset:16384
	ds_read_b128 v[204:207], v186 offset:17408
	ds_read_b128 v[208:211], v186 offset:18432
	ds_read_b128 v[212:215], v186 offset:19456
	ds_read_b128 v[216:219], v186 offset:20480
	ds_read_b128 v[220:223], v186 offset:21504
	ds_read_b128 v[224:227], v186 offset:22528
	ds_read_b128 v[228:231], v186 offset:23552
	global_load_lds_dwordx4 v[178:179], off
	s_add_i32 m0, s57, 0x2000
	s_add_u32 s58, s22, 0x40000
	v_lshl_add_u64 v[180:181], s[22:23], 0, v[148:149]
	s_addc_u32 s59, s23, 0
	s_add_i32 s57, s60, s38
	global_load_lds_dwordx4 v[180:181], off
	v_lshl_add_u64 v[182:183], s[58:59], 0, v[0:1]
	s_mov_b32 m0, s57
	v_lshl_add_u64 v[232:233], s[24:25], 0, v[150:151]
	global_load_lds_dwordx4 v[182:183], off
	v_lshl_add_u64 v[182:183], s[58:59], 0, v[148:149]
	s_add_i32 m0, s57, 0x2000
	s_nop 0
	global_load_lds_dwordx4 v[182:183], off
	v_lshl_add_u64 v[182:183], s[24:25], 0, v[152:153]
	s_mov_b32 m0, s39
	s_nop 0
	global_load_lds_dwordx4 v[182:183], off
	s_mov_b32 m0, s40
	s_nop 0
	global_load_lds_dwordx4 v[232:233], off
	s_waitcnt vmcnt(8)
	s_waitcnt lgkmcnt(0)
	v_mfma_f32_16x16x32_bf16 v[62:65], v[122:125], v[200:203], v[62:65]
	v_mfma_f32_16x16x32_bf16 v[58:61], v[134:137], v[200:203], v[58:61]
	v_mfma_f32_16x16x32_bf16 v[54:57], v[122:125], v[208:211], v[54:57]
	s_barrier
; #define PG8_STAGE(bufoff, gbase, voff) do { _Pragma("unroll") for (int _i = 0; _i < 2; ++_i) \
;         __builtin_amdgcn_global_load_lds((const unsigned*)((const char*)(gbase) + (voff)[_i]), (PG8_LAS unsigned*)(lds + (bufoff) + ldsw + _i * 8192), 16, 0, 0); } while (0)
; #define PG8_LDA(dst, b, h) do { _Pragma("unroll") for (int m = 0; m < 4; ++m) _Pragma("unroll") for (int k = 0; k < 2; ++k) dst[m][k] = *(const PG8_LAS bf16x8*)(lds + PG8_SA(b, h) + aoff + m * 2048 + k * 1024); } while (0)
; #define PG8_LDB(dst, b, h) do { _Pragma("unroll") for (int n = 0; n < 2; ++n) _Pragma("unroll") for (int k = 0; k < 2; ++k) dst[n][k] = *(const PG8_LAS bf16x8*)(lds + PG8_SB(b, h) + boff + n * 2048 + k * 1024); } while (0)
; #define PG8_MMA(ai, bj, At, Bt) do { __builtin_amdgcn_s_setprio(1); _Pragma("unroll") for (int m = 0; m < 4; ++m) _Pragma("unroll") for (int n = 0; n < 2; ++n) _Pragma("unroll") for (int k = 0; k < 2; ++k) \
;         acc[ai][bj][m][n] = __builtin_amdgcn_mfma_f32_16x16x32_bf16(Bt[n][k], At[m][k], acc[ai][bj][m][n], 0, 0, 0); __builtin_amdgcn_s_setprio(0); } while (0)
; #define PG8_WAIT_V(n) asm volatile("s_waitcnt vmcnt(" #n ")" ::: "memory")
; #define PG8_WAIT_L(n) asm volatile("s_waitcnt lgkmcnt(" #n ")" ::: "memory")
; #define PG8_BAR __builtin_amdgcn_s_barrier()
; #define PG8_SCHED __builtin_amdgcn_sched_barrier(0)
; template <class Epi, class Sched, bool ALIGN_EPI = false, bool SP2 = false, bool GATHER = false>
; __device__ __forceinline__ void gemm_phase(PG8_LAS unsigned char* lds, const Gemm g, const Sched& S, const Epi& E, int tid_in, const int* rowsrc = nullptr, PG8_LAS int* idx_lds = nullptr) {
;     ...
;             PG8_WAIT_V(8); PG8_WAIT_L(0); PG8_BAR; PG8_MMA(1, 0, At, B0); PG8_MMA(1, 1, At, B1); PG8_BAR; PG8_SCHED;
;             PG8_LDB(B0, 1, 0); PG8_LDB(B1, 1, 1); PG8_SCHED; PG8_LDA(At, 1, 0); PG8_STAGE(PG8_SA(0, 1), a2 + hstepA, PG8_OS(1));
;             PG8_WAIT_V(8); PG8_WAIT_L(0); PG8_BAR; PG8_MMA(0, 0, At, B0); PG8_MMA(0, 1, At, B1); PG8_BAR; PG8_SCHED;
	s_setprio 1
	s_waitcnt lgkmcnt(0)
	v_mfma_f32_16x16x32_bf16 v[42:45], v[134:137], v[208:211], v[42:45]
	v_mfma_f32_16x16x32_bf16 v[38:41], v[122:125], v[216:219], v[38:41]
	v_mfma_f32_16x16x32_bf16 v[26:29], v[134:137], v[216:219], v[26:29]
	v_mfma_f32_16x16x32_bf16 v[22:25], v[122:125], v[224:227], v[22:25]
	v_mfma_f32_16x16x32_bf16 v[10:13], v[134:137], v[224:227], v[10:13]
	v_mfma_f32_16x16x32_bf16 v[62:65], v[126:129], v[204:207], v[62:65]
	v_mfma_f32_16x16x32_bf16 v[58:61], v[142:145], v[204:207], v[58:61]
	v_mfma_f32_16x16x32_bf16 v[54:57], v[126:129], v[212:215], v[54:57]
	v_mfma_f32_16x16x32_bf16 v[42:45], v[142:145], v[212:215], v[42:45]
	v_mfma_f32_16x16x32_bf16 v[38:41], v[126:129], v[220:223], v[38:41]
	v_mfma_f32_16x16x32_bf16 v[26:29], v[142:145], v[220:223], v[26:29]
	v_mfma_f32_16x16x32_bf16 v[22:25], v[126:129], v[228:231], v[22:25]
	v_mfma_f32_16x16x32_bf16 v[10:13], v[142:145], v[228:231], v[10:13]
	s_setprio 0
	s_setprio 1
	v_mfma_f32_16x16x32_bf16 v[50:53], v[174:177], v[200:203], v[50:53]
	v_mfma_f32_16x16x32_bf16 v[46:49], v[192:195], v[200:203], v[46:49]
	v_mfma_f32_16x16x32_bf16 v[34:37], v[174:177], v[208:211], v[34:37]
	v_mfma_f32_16x16x32_bf16 v[30:33], v[192:195], v[208:211], v[30:33]
	v_mfma_f32_16x16x32_bf16 v[18:21], v[174:177], v[216:219], v[18:21]
	v_mfma_f32_16x16x32_bf16 v[14:17], v[192:195], v[216:219], v[14:17]
	v_mfma_f32_16x16x32_bf16 v[6:9], v[174:177], v[224:227], v[6:9]
	v_mfma_f32_16x16x32_bf16 v[2:5], v[192:195], v[224:227], v[2:5]
	v_mfma_f32_16x16x32_bf16 v[50:53], v[188:191], v[204:207], v[50:53]
	v_mfma_f32_16x16x32_bf16 v[46:49], v[196:199], v[204:207], v[46:49]
	v_mfma_f32_16x16x32_bf16 v[34:37], v[188:191], v[212:215], v[34:37]
	v_mfma_f32_16x16x32_bf16 v[30:33], v[196:199], v[212:215], v[30:33]
	v_mfma_f32_16x16x32_bf16 v[18:21], v[188:191], v[220:223], v[18:21]
	v_mfma_f32_16x16x32_bf16 v[14:17], v[196:199], v[220:223], v[14:17]
	v_mfma_f32_16x16x32_bf16 v[6:9], v[188:191], v[228:231], v[6:9]
	v_mfma_f32_16x16x32_bf16 v[2:5], v[196:199], v[228:231], v[2:5]
	s_setprio 0
	s_barrier
	s_add_i32 s57, 0, 0x18000
	s_add_i32 s58, 0, 0x1c000
	v_add_u32_e32 v142, s57, v184
	v_add_u32_e32 v187, s58, v184
	ds_read_b128 v[122:125], v142
	ds_read_b128 v[126:129], v142 offset:1024
	ds_read_b128 v[134:137], v142 offset:2048
	ds_read_b128 v[142:145], v142 offset:3072
	ds_read_b128 v[174:177], v187
	ds_read_b128 v[188:191], v187 offset:1024
	ds_read_b128 v[192:195], v187 offset:2048
	ds_read_b128 v[196:199], v187 offset:3072
	s_add_u32 s24, s24, 0x40000
	s_addc_u32 s25, s25, 0
	s_mov_b32 m0, s41
	v_lshl_add_u64 v[234:235], s[24:25], 0, v[152:153]
	ds_read_b128 v[200:203], v186 offset:32768
	ds_read_b128 v[204:207], v186 offset:33792
	ds_read_b128 v[208:211], v186 offset:34816
	ds_read_b128 v[212:215], v186 offset:35840
	ds_read_b128 v[216:219], v186 offset:36864
	ds_read_b128 v[220:223], v186 offset:37888
	ds_read_b128 v[224:227], v186 offset:38912
	ds_read_b128 v[228:231], v186 offset:39936
	global_load_lds_dwordx4 v[234:235], off
	v_lshl_add_u64 v[234:235], s[24:25], 0, v[150:151]
	s_mov_b32 m0, s43
	s_nop 0
	global_load_lds_dwordx4 v[234:235], off
	s_waitcnt vmcnt(8)
	s_waitcnt lgkmcnt(0)
	v_mfma_f32_16x16x32_bf16 v[138:141], v[122:125], v[200:203], v[138:141]
	v_mfma_f32_16x16x32_bf16 v[130:133], v[134:137], v[200:203], v[130:133]
	v_mfma_f32_16x16x32_bf16 v[118:121], v[122:125], v[208:211], v[118:121]
	s_barrier
	s_setprio 1
	s_waitcnt lgkmcnt(0)
	v_mfma_f32_16x16x32_bf16 v[106:109], v[134:137], v[208:211], v[106:109]
	v_mfma_f32_16x16x32_bf16 v[102:105], v[122:125], v[216:219], v[102:105]
	v_mfma_f32_16x16x32_bf16 v[90:93], v[134:137], v[216:219], v[90:93]
	v_mfma_f32_16x16x32_bf16 v[86:89], v[122:125], v[224:227], v[86:89]
	v_mfma_f32_16x16x32_bf16 v[74:77], v[134:137], v[224:227], v[74:77]
	v_mfma_f32_16x16x32_bf16 v[138:141], v[126:129], v[204:207], v[138:141]
	v_mfma_f32_16x16x32_bf16 v[130:133], v[142:145], v[204:207], v[130:133]
	v_mfma_f32_16x16x32_bf16 v[118:121], v[126:129], v[212:215], v[118:121]
	v_mfma_f32_16x16x32_bf16 v[106:109], v[142:145], v[212:215], v[106:109]
	v_mfma_f32_16x16x32_bf16 v[102:105], v[126:129], v[220:223], v[102:105]
	v_mfma_f32_16x16x32_bf16 v[90:93], v[142:145], v[220:223], v[90:93]
	v_mfma_f32_16x16x32_bf16 v[86:89], v[126:129], v[228:231], v[86:89]
	v_mfma_f32_16x16x32_bf16 v[74:77], v[142:145], v[228:231], v[74:77]
	s_setprio 0
	s_setprio 1
	v_mfma_f32_16x16x32_bf16 v[114:117], v[174:177], v[200:203], v[114:117]
	v_mfma_f32_16x16x32_bf16 v[110:113], v[192:195], v[200:203], v[110:113]
	v_mfma_f32_16x16x32_bf16 v[98:101], v[174:177], v[208:211], v[98:101]
	v_mfma_f32_16x16x32_bf16 v[94:97], v[192:195], v[208:211], v[94:97]
	v_mfma_f32_16x16x32_bf16 v[82:85], v[174:177], v[216:219], v[82:85]
	v_mfma_f32_16x16x32_bf16 v[78:81], v[192:195], v[216:219], v[78:81]
	v_mfma_f32_16x16x32_bf16 v[70:73], v[174:177], v[224:227], v[70:73]
	v_mfma_f32_16x16x32_bf16 v[66:69], v[192:195], v[224:227], v[66:69]
	v_mfma_f32_16x16x32_bf16 v[114:117], v[188:191], v[204:207], v[114:117]
	v_mfma_f32_16x16x32_bf16 v[110:113], v[196:199], v[204:207], v[110:113]
	v_mfma_f32_16x16x32_bf16 v[98:101], v[188:191], v[212:215], v[98:101]
	v_mfma_f32_16x16x32_bf16 v[94:97], v[196:199], v[212:215], v[94:97]
	v_mfma_f32_16x16x32_bf16 v[82:85], v[188:191], v[220:223], v[82:85]
	v_mfma_f32_16x16x32_bf16 v[78:81], v[196:199], v[220:223], v[78:81]
	v_mfma_f32_16x16x32_bf16 v[70:73], v[188:191], v[228:231], v[70:73]
	v_mfma_f32_16x16x32_bf16 v[66:69], v[196:199], v[228:231], v[66:69]
	s_setprio 0
	s_barrier
; #define PG8_STAGE(bufoff, gbase, voff) do { _Pragma("unroll") for (int _i = 0; _i < 2; ++_i) \
;         __builtin_amdgcn_global_load_lds((const unsigned*)((const char*)(gbase) + (voff)[_i]), (PG8_LAS unsigned*)(lds + (bufoff) + ldsw + _i * 8192), 16, 0, 0); } while (0)
; #define PG8_LDA(dst, b, h) do { _Pragma("unroll") for (int m = 0; m < 4; ++m) _Pragma("unroll") for (int k = 0; k < 2; ++k) dst[m][k] = *(const PG8_LAS bf16x8*)(lds + PG8_SA(b, h) + aoff + m * 2048 + k * 1024); } while (0)
; #define PG8_MMA(ai, bj, At, Bt) do { __builtin_amdgcn_s_setprio(1); _Pragma("unroll") for (int m = 0; m < 4; ++m) _Pragma("unroll") for (int n = 0; n < 2; ++n) _Pragma("unroll") for (int k = 0; k < 2; ++k) \
;         acc[ai][bj][m][n] = __builtin_amdgcn_mfma_f32_16x16x32_bf16(Bt[n][k], At[m][k], acc[ai][bj][m][n], 0, 0, 0); __builtin_amdgcn_s_setprio(0); } while (0)
; #define PG8_WAIT_V(n) asm volatile("s_waitcnt vmcnt(" #n ")" ::: "memory")
; #define PG8_WAIT_L(n) asm volatile("s_waitcnt lgkmcnt(" #n ")" ::: "memory")
; #define PG8_BAR __builtin_amdgcn_s_barrier()
; #define PG8_SCHED __builtin_amdgcn_sched_barrier(0)
; template <class Epi, class Sched, bool ALIGN_EPI = false, bool SP2 = false, bool GATHER = false>
; __device__ __forceinline__ void gemm_phase(PG8_LAS unsigned char* lds, const Gemm g, const Sched& S, const Epi& E, int tid_in, const int* rowsrc = nullptr, PG8_LAS int* idx_lds = nullptr) {
;     ...
;             PG8_LDA(At, 1, 1); PG8_STAGE(PG8_SB(1, 0), b3, voffB); PG8_STAGE(PG8_SB(1, 1), b3 + hstep, voffB); PG8_STAGE(PG8_SA(1, 0), a3, PG8_OS(0));
;             PG8_WAIT_V(8); PG8_WAIT_L(0); PG8_BAR; PG8_MMA(1, 0, At, B0); PG8_MMA(1, 1, At, B1); PG8_BAR; PG8_SCHED;
;     ...
;         if constexpr (ALIGN_EPI) { if (wr == 0) PG8_BAR; }
	s_add_i32 s24, s57, s38
	v_lshl_add_u64 v[178:179], v[178:179], 0, s[10:11]
	s_mov_b32 m0, s24
	ds_read_b128 v[200:203], v186 offset:49152
	ds_read_b128 v[204:207], v186 offset:50176
	ds_read_b128 v[208:211], v186 offset:51200
	ds_read_b128 v[212:215], v186 offset:52224
	ds_read_b128 v[216:219], v186 offset:53248
	ds_read_b128 v[220:223], v186 offset:54272
	ds_read_b128 v[224:227], v186 offset:55296
	ds_read_b128 v[228:231], v186 offset:56320
	global_load_lds_dwordx4 v[178:179], off
	s_add_i32 m0, s24, 0x2000
	s_add_u32 s22, s22, 0x40080
	v_lshl_add_u64 v[178:179], v[180:181], 0, s[10:11]
	s_addc_u32 s23, s23, 0
	s_add_i32 s24, s58, s38
	global_load_lds_dwordx4 v[178:179], off
	v_lshl_add_u64 v[178:179], s[22:23], 0, v[0:1]
	s_mov_b32 m0, s24
	s_nop 0
	global_load_lds_dwordx4 v[178:179], off
	v_lshl_add_u64 v[178:179], s[22:23], 0, v[148:149]
	s_add_i32 m0, s24, 0x2000
	s_nop 0
	global_load_lds_dwordx4 v[178:179], off
	v_lshl_add_u64 v[178:179], v[182:183], 0, s[10:11]
	s_mov_b32 m0, s51
	s_nop 0
	global_load_lds_dwordx4 v[178:179], off
	v_lshl_add_u64 v[178:179], v[232:233], 0, s[10:11]
	s_mov_b32 m0, s52
	s_nop 0
	global_load_lds_dwordx4 v[178:179], off
	s_waitcnt vmcnt(8)
	s_waitcnt lgkmcnt(0)
	v_mfma_f32_16x16x32_bf16 v[62:65], v[122:125], v[200:203], v[62:65]
	v_mfma_f32_16x16x32_bf16 v[58:61], v[134:137], v[200:203], v[58:61]
	v_mfma_f32_16x16x32_bf16 v[54:57], v[122:125], v[208:211], v[54:57]
	s_barrier
	s_setprio 1
	s_waitcnt lgkmcnt(0)
	v_mfma_f32_16x16x32_bf16 v[42:45], v[134:137], v[208:211], v[42:45]
	v_mfma_f32_16x16x32_bf16 v[38:41], v[122:125], v[216:219], v[38:41]
	v_mfma_f32_16x16x32_bf16 v[26:29], v[134:137], v[216:219], v[26:29]
	v_mfma_f32_16x16x32_bf16 v[22:25], v[122:125], v[224:227], v[22:25]
	v_mfma_f32_16x16x32_bf16 v[10:13], v[134:137], v[224:227], v[10:13]
	v_mfma_f32_16x16x32_bf16 v[62:65], v[126:129], v[204:207], v[62:65]
	v_mfma_f32_16x16x32_bf16 v[58:61], v[142:145], v[204:207], v[58:61]
	v_mfma_f32_16x16x32_bf16 v[54:57], v[126:129], v[212:215], v[54:57]
	v_mfma_f32_16x16x32_bf16 v[42:45], v[142:145], v[212:215], v[42:45]
	v_mfma_f32_16x16x32_bf16 v[38:41], v[126:129], v[220:223], v[38:41]
	v_mfma_f32_16x16x32_bf16 v[26:29], v[142:145], v[220:223], v[26:29]
	v_mfma_f32_16x16x32_bf16 v[22:25], v[126:129], v[228:231], v[22:25]
	v_mfma_f32_16x16x32_bf16 v[10:13], v[142:145], v[228:231], v[10:13]
	s_setprio 0
	s_setprio 1
	v_mfma_f32_16x16x32_bf16 v[50:53], v[174:177], v[200:203], v[50:53]
	v_mfma_f32_16x16x32_bf16 v[46:49], v[192:195], v[200:203], v[46:49]
	v_mfma_f32_16x16x32_bf16 v[34:37], v[174:177], v[208:211], v[34:37]
	v_mfma_f32_16x16x32_bf16 v[30:33], v[192:195], v[208:211], v[30:33]
	v_mfma_f32_16x16x32_bf16 v[18:21], v[174:177], v[216:219], v[18:21]
	v_mfma_f32_16x16x32_bf16 v[14:17], v[192:195], v[216:219], v[14:17]
	v_mfma_f32_16x16x32_bf16 v[6:9], v[174:177], v[224:227], v[6:9]
	v_mfma_f32_16x16x32_bf16 v[2:5], v[192:195], v[224:227], v[2:5]
	v_mfma_f32_16x16x32_bf16 v[50:53], v[188:191], v[204:207], v[50:53]
	v_mfma_f32_16x16x32_bf16 v[46:49], v[196:199], v[204:207], v[46:49]
	v_mfma_f32_16x16x32_bf16 v[34:37], v[188:191], v[212:215], v[34:37]
	v_mfma_f32_16x16x32_bf16 v[30:33], v[196:199], v[212:215], v[30:33]
	v_mfma_f32_16x16x32_bf16 v[18:21], v[188:191], v[220:223], v[18:21]
	v_mfma_f32_16x16x32_bf16 v[14:17], v[196:199], v[220:223], v[14:17]
	v_mfma_f32_16x16x32_bf16 v[6:9], v[188:191], v[228:231], v[6:9]
	v_mfma_f32_16x16x32_bf16 v[2:5], v[196:199], v[228:231], v[2:5]
	s_setprio 0
	s_barrier
	s_add_i32 s56, s56, 2
	s_add_u32 s20, s20, 0x100
	s_addc_u32 s21, s21, 0
	s_add_u32 s54, s54, 0x100
	s_addc_u32 s55, s55, 0
	s_cmp_gt_u32 s56, 13
	s_cbranch_scc0 .LBB0_1618
	s_and_b64 vcc, exec, s[4:5]
	s_cbranch_vccz .LBB0_1621
	s_barrier

;     __device__ bool next(int i, Unit& u) const { const int L = i * G + c; if (L >= nwg) return false; u.pm = L & 7; u.pn = L; return true; }
;     __device__ bool next(int i, Unit& u) const {
;         const int L = i * G + c; if (L >= nwg) return false;
;         const int per = nrt * nct, e = L / per, r = L % per, j = r / nrt, rt = r % nrt;
;         u.pm = e * 17 + rt; u.pn = e * nct + j; return true;
; template <class Epi, class Sched, bool ALIGN_EPI = false, bool SP2 = false, bool GATHER = false>
; __device__ __forceinline__ void gemm_phase(PG8_LAS unsigned char* lds, const Gemm g, const Sched& S, const Epi& E, int tid_in, const int* rowsrc = nullptr, PG8_LAS int* idx_lds = nullptr) {
;     ...
;         Unit u_; for (int i = 0; S.next(i, u_); ++i) if (tid < 256) idx_lds[i * 256 + tid] = rowsrc[u_.pm * BM + tid];
.LBB0_1917:
	s_and_saveexec_b64 s[6:7], vcc
	s_cbranch_execz .LBB0_1916
	s_abs_i32 s21, s19
	s_mul_hi_u32 s22, s21, s16
	s_mul_i32 s23, s22, s14
	s_ashr_i32 s20, s19, 31
	s_sub_i32 s21, s21, s23
	s_xor_b32 s20, s20, s9
	s_add_i32 s23, s22, 1
	s_sub_i32 s24, s21, s14
	s_cmp_ge_u32 s21, s14
	s_cselect_b32 s22, s23, s22
	s_cselect_b32 s21, s24, s21
	s_add_i32 s23, s22, 1
	s_cmp_ge_u32 s21, s14
	s_cselect_b32 s21, s23, s22
	s_xor_b32 s21, s21, s20
	s_sub_i32 s20, s21, s20
	s_mul_i32 s21, s20, s31
	s_sub_i32 s19, s19, s21
	s_ashr_i32 s21, s19, 31
	s_abs_i32 s19, s19
	s_mul_hi_u32 s22, s19, s17
	s_mul_i32 s22, s22, s29
	s_sub_i32 s19, s19, s22
	s_sub_i32 s22, s19, s29
	s_cmp_ge_u32 s19, s29
	s_cselect_b32 s19, s22, s19
	s_sub_i32 s22, s19, s29
	s_cmp_ge_u32 s19, s29
	s_cselect_b32 s19, s22, s19
	s_xor_b32 s19, s19, s21
	s_sub_i32 s19, s19, s21
	s_mul_i32 s20, s20, 17
	s_add_i32 s20, s20, s19
	v_lshl_add_u32 v4, s20, 8, v0
	v_ashrrev_i32_e32 v5, 31, v4
	v_lshl_add_u64 v[4:5], v[4:5], 2, s[4:5]
	v_readfirstlane_b32 s24, v2
	s_mov_b32 m0, s24
	s_nop 0
	global_load_lds_dword v[4:5], off
	s_branch .LBB0_1916

; #define PG8_STAGE(bufoff, gbase, voff) do { _Pragma("unroll") for (int _i = 0; _i < 2; ++_i) \
;         __builtin_amdgcn_global_load_lds((const unsigned*)((const char*)(gbase) + (voff)[_i]), (PG8_LAS unsigned*)(lds + (bufoff) + ldsw + _i * 8192), 16, 0, 0); } while (0)
; #define PG8_LDA(dst, b, h) do { _Pragma("unroll") for (int m = 0; m < 4; ++m) _Pragma("unroll") for (int k = 0; k < 2; ++k) dst[m][k] = *(const PG8_LAS bf16x8*)(lds + PG8_SA(b, h) + aoff + m * 2048 + k * 1024); } while (0)
; #define PG8_LDB(dst, b, h) do { _Pragma("unroll") for (int n = 0; n < 2; ++n) _Pragma("unroll") for (int k = 0; k < 2; ++k) dst[n][k] = *(const PG8_LAS bf16x8*)(lds + PG8_SB(b, h) + boff + n * 2048 + k * 1024); } while (0)
; #define PG8_WAIT_V(n) asm volatile("s_waitcnt vmcnt(" #n ")" ::: "memory")
; #define PG8_WAIT_L(n) asm volatile("s_waitcnt lgkmcnt(" #n ")" ::: "memory")
; #define PG8_BAR __builtin_amdgcn_s_barrier()
; template <class Epi, class Sched, bool ALIGN_EPI = false, bool SP2 = false, bool GATHER = false>
; __device__ __forceinline__ void gemm_phase(PG8_LAS unsigned char* lds, const Gemm g, const Sched& S, const Epi& E, int tid_in, const int* rowsrc = nullptr, PG8_LAS int* idx_lds = nullptr) {
;     ...
;         for (int t = 0; t < nt; t += 2) {
;             const bool last = (t == nt - 2);
;             if constexpr (GATHER) {
; #pragma unroll
;                 for (int h_ = 0; h_ < 2; ++h_) { gS[h_][0] = last ? gN[h_][0] : gA[h_][0]; gS[h_][1] = last ? gN[h_][1] : gA[h_][1]; } }
;             const char* a1 = cA + (size_t)(t + 1) * kstep;
;             const char* a2 = last ? nA : cA + (size_t)(t + 2) * kstep; const char* b2 = last ? nB : cB + (size_t)(t + 2) * kstep;
;             const char* a3 = a2 + kstep; const char* b3 = b2 + kstep;
;             if (last && has_next) S.a_ready(nxt);
;             if constexpr (SP2) {
;             PG8_LDB(B0, 0, 0); PG8_LDB(B1, 0, 1); PG8_SCHED; PG8_LDA(At, 0, 0); PG8_STAGE(PG8_SA(1, 1), a1 + hstepA, PG8_OA(1));
;             PG8_WAIT_V(8); PG8_WAIT_L(0); PG8_BAR; PG8_MMA(0, 0, At, B0); PG8_MMA(0, 1, At, B1); PG8_BAR; PG8_SCHED;
;             PG8_LDA(At, 0, 1); PG8_STAGE(PG8_SB(0, 0), b2, voffB); PG8_STAGE(PG8_SB(0, 1), b2 + hstep, voffB); PG8_STAGE(PG8_SA(0, 0), a2, PG8_OS(0));
;             PG8_WAIT_V(8); PG8_WAIT_L(0); PG8_BAR; PG8_MMA(1, 0, At, B0); PG8_MMA(1, 1, At, B1); PG8_BAR; PG8_SCHED;
.LBB0_1930:
	s_add_u32 s22, s27, s20
	s_addc_u32 s23, s28, s21
	s_add_u32 s24, s22, 0x9000100
	s_addc_u32 s25, s23, 0
	s_add_u32 s56, s53, s20
	s_addc_u32 s57, s54, s21
	s_add_i32 s58, 0, 0x10000
	s_cmpk_eq_i32 s20, 0x700
	s_cselect_b64 vcc, -1, 0
	s_and_b64 s[22:23], vcc, exec
	s_cselect_b32 s25, s1, s25
	s_cselect_b32 s24, s0, s24
	v_add_u32_e32 v141, s58, v153
	s_cselect_b32 s23, s15, s57
	s_cselect_b32 s22, s43, s56
	s_add_i32 s59, 0, 0x14000
	ds_read_b128 v[160:163], v141
	ds_read_b128 v[164:167], v141 offset:1024
	ds_read_b128 v[168:171], v141 offset:2048
	ds_read_b128 v[172:175], v141 offset:3072
	v_add_u32_e32 v141, s59, v153
	ds_read_b128 v[176:179], v141
	ds_read_b128 v[180:183], v141 offset:1024
	ds_read_b128 v[184:187], v141 offset:2048
	ds_read_b128 v[188:191], v141 offset:3072
	v_cndmask_b32_e32 v0, v134, v158, vcc
	v_cndmask_b32_e32 v224, v136, v157, vcc
	v_cndmask_b32_e32 v135, v138, v156, vcc
	v_cndmask_b32_e32 v139, v140, v155, vcc
	v_lshl_add_u64 v[226:227], v[144:145], 0, s[20:21]
	s_add_i32 m0, s45, 0xc000
	ds_read_b128 v[192:195], v154
	ds_read_b128 v[196:199], v154 offset:1024
	ds_read_b128 v[200:203], v154 offset:2048
	ds_read_b128 v[204:207], v154 offset:3072
	ds_read_b128 v[208:211], v154 offset:4096
	ds_read_b128 v[212:215], v154 offset:5120
	ds_read_b128 v[216:219], v154 offset:6144
	ds_read_b128 v[220:223], v154 offset:7168
	global_load_lds_dwordx4 v[226:227], off
	v_lshl_add_u64 v[226:227], v[142:143], 0, s[20:21]
	s_add_i32 m0, s45, 0xe000
	s_nop 0
	global_load_lds_dwordx4 v[226:227], off
	s_waitcnt vmcnt(8)
	s_waitcnt lgkmcnt(0)
	v_mfma_f32_16x16x32_bf16 v[126:129], v[160:163], v[192:195], v[126:129]
	v_mfma_f32_16x16x32_bf16 v[118:121], v[168:171], v[192:195], v[118:121]
	v_mfma_f32_16x16x32_bf16 v[110:113], v[160:163], v[200:203], v[110:113]
	s_barrier
	s_setprio 1
	s_waitcnt lgkmcnt(0)
	v_mfma_f32_16x16x32_bf16 v[102:105], v[168:171], v[200:203], v[102:105]
	v_mfma_f32_16x16x32_bf16 v[94:97], v[160:163], v[208:211], v[94:97]
	v_mfma_f32_16x16x32_bf16 v[86:89], v[168:171], v[208:211], v[86:89]
	v_mfma_f32_16x16x32_bf16 v[78:81], v[160:163], v[216:219], v[78:81]
	v_mfma_f32_16x16x32_bf16 v[70:73], v[168:171], v[216:219], v[70:73]
	v_mfma_f32_16x16x32_bf16 v[126:129], v[164:167], v[196:199], v[126:129]
	v_mfma_f32_16x16x32_bf16 v[118:121], v[172:175], v[196:199], v[118:121]
	v_mfma_f32_16x16x32_bf16 v[110:113], v[164:167], v[204:207], v[110:113]
	v_mfma_f32_16x16x32_bf16 v[102:105], v[172:175], v[204:207], v[102:105]
	v_mfma_f32_16x16x32_bf16 v[94:97], v[164:167], v[212:215], v[94:97]
	v_mfma_f32_16x16x32_bf16 v[86:89], v[172:175], v[212:215], v[86:89]
	v_mfma_f32_16x16x32_bf16 v[78:81], v[164:167], v[220:223], v[78:81]
	v_mfma_f32_16x16x32_bf16 v[70:73], v[172:175], v[220:223], v[70:73]
	s_setprio 0
	s_setprio 1
	v_mfma_f32_16x16x32_bf16 v[122:125], v[176:179], v[192:195], v[122:125]
	v_mfma_f32_16x16x32_bf16 v[114:117], v[184:187], v[192:195], v[114:117]
	v_mfma_f32_16x16x32_bf16 v[106:109], v[176:179], v[200:203], v[106:109]
	v_mfma_f32_16x16x32_bf16 v[98:101], v[184:187], v[200:203], v[98:101]
	v_mfma_f32_16x16x32_bf16 v[90:93], v[176:179], v[208:211], v[90:93]
	v_mfma_f32_16x16x32_bf16 v[82:85], v[184:187], v[208:211], v[82:85]
	v_mfma_f32_16x16x32_bf16 v[74:77], v[176:179], v[216:219], v[74:77]
	v_mfma_f32_16x16x32_bf16 v[66:69], v[184:187], v[216:219], v[66:69]
	v_mfma_f32_16x16x32_bf16 v[122:125], v[180:183], v[196:199], v[122:125]
	v_mfma_f32_16x16x32_bf16 v[114:117], v[188:191], v[196:199], v[114:117]
	v_mfma_f32_16x16x32_bf16 v[106:109], v[180:183], v[204:207], v[106:109]
	v_mfma_f32_16x16x32_bf16 v[98:101], v[188:191], v[204:207], v[98:101]
	v_mfma_f32_16x16x32_bf16 v[90:93], v[180:183], v[212:215], v[90:93]
	v_mfma_f32_16x16x32_bf16 v[82:85], v[188:191], v[212:215], v[82:85]
	v_mfma_f32_16x16x32_bf16 v[74:77], v[180:183], v[220:223], v[74:77]
	v_mfma_f32_16x16x32_bf16 v[66:69], v[188:191], v[220:223], v[66:69]
	s_setprio 0
	s_barrier
	s_add_i32 s56, s58, s36
	v_lshl_add_u64 v[226:227], s[22:23], 0, v[130:131]
	s_mov_b32 m0, s56
	ds_read_b128 v[192:195], v154 offset:16384
	ds_read_b128 v[196:199], v154 offset:17408
	ds_read_b128 v[200:203], v154 offset:18432
	ds_read_b128 v[204:207], v154 offset:19456
	ds_read_b128 v[208:211], v154 offset:20480
	ds_read_b128 v[212:215], v154 offset:21504
	ds_read_b128 v[216:219], v154 offset:22528
	ds_read_b128 v[220:223], v154 offset:23552
	global_load_lds_dwordx4 v[226:227], off
	s_add_i32 m0, s56, 0x2000
	s_add_u32 s56, s22, 0x40000
	v_lshl_add_u64 v[228:229], s[22:23], 0, v[132:133]
	s_addc_u32 s57, s23, 0
	s_add_i32 s58, s59, s36
	global_load_lds_dwordx4 v[228:229], off
	v_lshl_add_u64 v[230:231], s[56:57], 0, v[130:131]
	s_mov_b32 m0, s58
	v_mov_b32_e32 v225, v1
	global_load_lds_dwordx4 v[230:231], off
	v_lshl_add_u64 v[230:231], s[56:57], 0, v[132:133]
	s_add_i32 m0, s58, 0x2000
	s_nop 0
	global_load_lds_dwordx4 v[230:231], off
	s_mov_b32 m0, s45
	v_lshl_add_u64 v[230:231], s[24:25], 0, v[0:1]
	global_load_lds_dwordx4 v0, s[24:25]
	s_mov_b32 m0, s46
	s_nop 0
	global_load_lds_dwordx4 v224, s[24:25]
	s_waitcnt vmcnt(8)
	s_waitcnt lgkmcnt(0)
	v_lshl_add_u64 v[224:225], s[24:25], 0, v[224:225]
	s_barrier
; #define PG8_STAGE(bufoff, gbase, voff) do { _Pragma("unroll") for (int _i = 0; _i < 2; ++_i) \
;         __builtin_amdgcn_global_load_lds((const unsigned*)((const char*)(gbase) + (voff)[_i]), (PG8_LAS unsigned*)(lds + (bufoff) + ldsw + _i * 8192), 16, 0, 0); } while (0)
; #define PG8_LDA(dst, b, h) do { _Pragma("unroll") for (int m = 0; m < 4; ++m) _Pragma("unroll") for (int k = 0; k < 2; ++k) dst[m][k] = *(const PG8_LAS bf16x8*)(lds + PG8_SA(b, h) + aoff + m * 2048 + k * 1024); } while (0)
; #define PG8_LDB(dst, b, h) do { _Pragma("unroll") for (int n = 0; n < 2; ++n) _Pragma("unroll") for (int k = 0; k < 2; ++k) dst[n][k] = *(const PG8_LAS bf16x8*)(lds + PG8_SB(b, h) + boff + n * 2048 + k * 1024); } while (0)
; #define PG8_MMA(ai, bj, At, Bt) do { __builtin_amdgcn_s_setprio(1); _Pragma("unroll") for (int m = 0; m < 4; ++m) _Pragma("unroll") for (int n = 0; n < 2; ++n) _Pragma("unroll") for (int k = 0; k < 2; ++k) \
;         acc[ai][bj][m][n] = __builtin_amdgcn_mfma_f32_16x16x32_bf16(Bt[n][k], At[m][k], acc[ai][bj][m][n], 0, 0, 0); __builtin_amdgcn_s_setprio(0); } while (0)
; #define PG8_WAIT_V(n) asm volatile("s_waitcnt vmcnt(" #n ")" ::: "memory")
; #define PG8_WAIT_L(n) asm volatile("s_waitcnt lgkmcnt(" #n ")" ::: "memory")
; #define PG8_BAR __builtin_amdgcn_s_barrier()
; #define PG8_SCHED __builtin_amdgcn_sched_barrier(0)
; template <class Epi, class Sched, bool ALIGN_EPI = false, bool SP2 = false, bool GATHER = false>
; __device__ __forceinline__ void gemm_phase(PG8_LAS unsigned char* lds, const Gemm g, const Sched& S, const Epi& E, int tid_in, const int* rowsrc = nullptr, PG8_LAS int* idx_lds = nullptr) {
;     ...
;             PG8_WAIT_V(8); PG8_WAIT_L(0); PG8_BAR; PG8_MMA(1, 0, At, B0); PG8_MMA(1, 1, At, B1); PG8_BAR; PG8_SCHED;
;             PG8_LDB(B0, 1, 0); PG8_LDB(B1, 1, 1); PG8_SCHED; PG8_LDA(At, 1, 0); PG8_STAGE(PG8_SA(0, 1), a2 + hstepA, PG8_OS(1));
;             PG8_WAIT_V(8); PG8_WAIT_L(0); PG8_BAR; PG8_MMA(0, 0, At, B0); PG8_MMA(0, 1, At, B1); PG8_BAR; PG8_SCHED;
	s_setprio 1
	s_waitcnt lgkmcnt(0)
	v_mfma_f32_16x16x32_bf16 v[62:65], v[160:163], v[192:195], v[62:65]
	v_mfma_f32_16x16x32_bf16 v[54:57], v[168:171], v[192:195], v[54:57]
	v_mfma_f32_16x16x32_bf16 v[46:49], v[160:163], v[200:203], v[46:49]
	v_mfma_f32_16x16x32_bf16 v[38:41], v[168:171], v[200:203], v[38:41]
	v_mfma_f32_16x16x32_bf16 v[30:33], v[160:163], v[208:211], v[30:33]
	v_mfma_f32_16x16x32_bf16 v[22:25], v[168:171], v[208:211], v[22:25]
	v_mfma_f32_16x16x32_bf16 v[14:17], v[160:163], v[216:219], v[14:17]
	v_mfma_f32_16x16x32_bf16 v[6:9], v[168:171], v[216:219], v[6:9]
	v_mfma_f32_16x16x32_bf16 v[62:65], v[164:167], v[196:199], v[62:65]
	v_mfma_f32_16x16x32_bf16 v[54:57], v[172:175], v[196:199], v[54:57]
	v_mfma_f32_16x16x32_bf16 v[46:49], v[164:167], v[204:207], v[46:49]
	v_mfma_f32_16x16x32_bf16 v[38:41], v[172:175], v[204:207], v[38:41]
	v_mfma_f32_16x16x32_bf16 v[30:33], v[164:167], v[212:215], v[30:33]
	v_mfma_f32_16x16x32_bf16 v[22:25], v[172:175], v[212:215], v[22:25]
	v_mfma_f32_16x16x32_bf16 v[14:17], v[164:167], v[220:223], v[14:17]
	v_mfma_f32_16x16x32_bf16 v[6:9], v[172:175], v[220:223], v[6:9]
	s_setprio 0
	s_setprio 1
	v_mfma_f32_16x16x32_bf16 v[58:61], v[176:179], v[192:195], v[58:61]
	v_mfma_f32_16x16x32_bf16 v[50:53], v[184:187], v[192:195], v[50:53]
	v_mfma_f32_16x16x32_bf16 v[42:45], v[176:179], v[200:203], v[42:45]
	v_mfma_f32_16x16x32_bf16 v[34:37], v[184:187], v[200:203], v[34:37]
	v_mfma_f32_16x16x32_bf16 v[26:29], v[176:179], v[208:211], v[26:29]
	v_mfma_f32_16x16x32_bf16 v[18:21], v[184:187], v[208:211], v[18:21]
	v_mfma_f32_16x16x32_bf16 v[10:13], v[176:179], v[216:219], v[10:13]
	v_mfma_f32_16x16x32_bf16 v[2:5], v[184:187], v[216:219], v[2:5]
	v_mfma_f32_16x16x32_bf16 v[58:61], v[180:183], v[196:199], v[58:61]
	v_mfma_f32_16x16x32_bf16 v[50:53], v[188:191], v[196:199], v[50:53]
	v_mfma_f32_16x16x32_bf16 v[42:45], v[180:183], v[204:207], v[42:45]
	v_mfma_f32_16x16x32_bf16 v[34:37], v[188:191], v[204:207], v[34:37]
	v_mfma_f32_16x16x32_bf16 v[26:29], v[180:183], v[212:215], v[26:29]
	v_mfma_f32_16x16x32_bf16 v[18:21], v[188:191], v[212:215], v[18:21]
	v_mfma_f32_16x16x32_bf16 v[10:13], v[180:183], v[220:223], v[10:13]
	v_mfma_f32_16x16x32_bf16 v[2:5], v[188:191], v[220:223], v[2:5]
	s_setprio 0
	s_barrier
	s_add_i32 s56, 0, 0x18000
	v_add_u32_e32 v0, s56, v153
	s_add_i32 s57, 0, 0x1c000
	ds_read_b128 v[160:163], v0
	ds_read_b128 v[164:167], v0 offset:1024
	ds_read_b128 v[168:171], v0 offset:2048
	ds_read_b128 v[172:175], v0 offset:3072
	v_add_u32_e32 v0, s57, v153
	ds_read_b128 v[176:179], v0
	ds_read_b128 v[180:183], v0 offset:1024
	ds_read_b128 v[184:187], v0 offset:2048
	ds_read_b128 v[188:191], v0 offset:3072
	s_mov_b32 m0, s47
	ds_read_b128 v[192:195], v154 offset:32768
	ds_read_b128 v[196:199], v154 offset:33792
	ds_read_b128 v[200:203], v154 offset:34816
	ds_read_b128 v[204:207], v154 offset:35840
	ds_read_b128 v[208:211], v154 offset:36864
	ds_read_b128 v[212:215], v154 offset:37888
	ds_read_b128 v[216:219], v154 offset:38912
	ds_read_b128 v[220:223], v154 offset:39936
	global_load_lds_dwordx4 v135, s[24:25]
	s_mov_b32 m0, s48
	s_nop 0
	global_load_lds_dwordx4 v139, s[24:25]
	s_waitcnt vmcnt(8)
	s_waitcnt lgkmcnt(0)
	v_mfma_f32_16x16x32_bf16 v[126:129], v[160:163], v[192:195], v[126:129]
	v_mfma_f32_16x16x32_bf16 v[118:121], v[168:171], v[192:195], v[118:121]
	v_mfma_f32_16x16x32_bf16 v[110:113], v[160:163], v[200:203], v[110:113]
	s_barrier
	s_setprio 1
	s_waitcnt lgkmcnt(0)
	v_mfma_f32_16x16x32_bf16 v[102:105], v[168:171], v[200:203], v[102:105]
	v_mfma_f32_16x16x32_bf16 v[94:97], v[160:163], v[208:211], v[94:97]
	v_mfma_f32_16x16x32_bf16 v[86:89], v[168:171], v[208:211], v[86:89]
	v_mfma_f32_16x16x32_bf16 v[78:81], v[160:163], v[216:219], v[78:81]
	v_mfma_f32_16x16x32_bf16 v[70:73], v[168:171], v[216:219], v[70:73]
	v_mfma_f32_16x16x32_bf16 v[126:129], v[164:167], v[196:199], v[126:129]
	v_mfma_f32_16x16x32_bf16 v[118:121], v[172:175], v[196:199], v[118:121]
	v_mfma_f32_16x16x32_bf16 v[110:113], v[164:167], v[204:207], v[110:113]
	v_mfma_f32_16x16x32_bf16 v[102:105], v[172:175], v[204:207], v[102:105]
	v_mfma_f32_16x16x32_bf16 v[94:97], v[164:167], v[212:215], v[94:97]
	v_mfma_f32_16x16x32_bf16 v[86:89], v[172:175], v[212:215], v[86:89]
	v_mfma_f32_16x16x32_bf16 v[78:81], v[164:167], v[220:223], v[78:81]
	v_mfma_f32_16x16x32_bf16 v[70:73], v[172:175], v[220:223], v[70:73]
	s_setprio 0
	s_setprio 1
	v_mfma_f32_16x16x32_bf16 v[122:125], v[176:179], v[192:195], v[122:125]
	v_mfma_f32_16x16x32_bf16 v[114:117], v[184:187], v[192:195], v[114:117]
	v_mfma_f32_16x16x32_bf16 v[106:109], v[176:179], v[200:203], v[106:109]
	v_mfma_f32_16x16x32_bf16 v[98:101], v[184:187], v[200:203], v[98:101]
	v_mfma_f32_16x16x32_bf16 v[90:93], v[176:179], v[208:211], v[90:93]
	v_mfma_f32_16x16x32_bf16 v[82:85], v[184:187], v[208:211], v[82:85]
	v_mfma_f32_16x16x32_bf16 v[74:77], v[176:179], v[216:219], v[74:77]
	v_mfma_f32_16x16x32_bf16 v[66:69], v[184:187], v[216:219], v[66:69]
	v_mfma_f32_16x16x32_bf16 v[122:125], v[180:183], v[196:199], v[122:125]
	v_mfma_f32_16x16x32_bf16 v[114:117], v[188:191], v[196:199], v[114:117]
	v_mfma_f32_16x16x32_bf16 v[106:109], v[180:183], v[204:207], v[106:109]
	v_mfma_f32_16x16x32_bf16 v[98:101], v[188:191], v[204:207], v[98:101]
	v_mfma_f32_16x16x32_bf16 v[90:93], v[180:183], v[212:215], v[90:93]
	v_mfma_f32_16x16x32_bf16 v[82:85], v[188:191], v[212:215], v[82:85]
	v_mfma_f32_16x16x32_bf16 v[74:77], v[180:183], v[220:223], v[74:77]
	v_mfma_f32_16x16x32_bf16 v[66:69], v[188:191], v[220:223], v[66:69]
	s_setprio 0
	s_barrier
; #define PG8_STAGE(bufoff, gbase, voff) do { _Pragma("unroll") for (int _i = 0; _i < 2; ++_i) \
;         __builtin_amdgcn_global_load_lds((const unsigned*)((const char*)(gbase) + (voff)[_i]), (PG8_LAS unsigned*)(lds + (bufoff) + ldsw + _i * 8192), 16, 0, 0); } while (0)
; #define PG8_LDA(dst, b, h) do { _Pragma("unroll") for (int m = 0; m < 4; ++m) _Pragma("unroll") for (int k = 0; k < 2; ++k) dst[m][k] = *(const PG8_LAS bf16x8*)(lds + PG8_SA(b, h) + aoff + m * 2048 + k * 1024); } while (0)
; #define PG8_MMA(ai, bj, At, Bt) do { __builtin_amdgcn_s_setprio(1); _Pragma("unroll") for (int m = 0; m < 4; ++m) _Pragma("unroll") for (int n = 0; n < 2; ++n) _Pragma("unroll") for (int k = 0; k < 2; ++k) \
;         acc[ai][bj][m][n] = __builtin_amdgcn_mfma_f32_16x16x32_bf16(Bt[n][k], At[m][k], acc[ai][bj][m][n], 0, 0, 0); __builtin_amdgcn_s_setprio(0); } while (0)
; #define PG8_WAIT_V(n) asm volatile("s_waitcnt vmcnt(" #n ")" ::: "memory")
; #define PG8_WAIT_L(n) asm volatile("s_waitcnt lgkmcnt(" #n ")" ::: "memory")
; #define PG8_BAR __builtin_amdgcn_s_barrier()
; #define PG8_SCHED __builtin_amdgcn_sched_barrier(0)
; template <class Epi, class Sched, bool ALIGN_EPI = false, bool SP2 = false, bool GATHER = false>
; __device__ __forceinline__ void gemm_phase(PG8_LAS unsigned char* lds, const Gemm g, const Sched& S, const Epi& E, int tid_in, const int* rowsrc = nullptr, PG8_LAS int* idx_lds = nullptr) {
;     ...
;             PG8_LDA(At, 1, 1); PG8_STAGE(PG8_SB(1, 0), b3, voffB); PG8_STAGE(PG8_SB(1, 1), b3 + hstep, voffB); PG8_STAGE(PG8_SA(1, 0), a3, PG8_OS(0));
;             PG8_WAIT_V(8); PG8_WAIT_L(0); PG8_BAR; PG8_MMA(1, 0, At, B0); PG8_MMA(1, 1, At, B1); PG8_BAR; PG8_SCHED;
;     ...
;         if constexpr (ALIGN_EPI) { if (wr == 0) PG8_BAR; }
	s_add_i32 s24, s56, s36
	v_lshl_add_u64 v[226:227], v[226:227], 0, s[10:11]
	s_mov_b32 m0, s24
	ds_read_b128 v[192:195], v154 offset:49152
	ds_read_b128 v[196:199], v154 offset:50176
	ds_read_b128 v[200:203], v154 offset:51200
	ds_read_b128 v[204:207], v154 offset:52224
	ds_read_b128 v[208:211], v154 offset:53248
	ds_read_b128 v[212:215], v154 offset:54272
	ds_read_b128 v[216:219], v154 offset:55296
	ds_read_b128 v[220:223], v154 offset:56320
	global_load_lds_dwordx4 v[226:227], off
	s_add_i32 m0, s24, 0x2000
	s_add_u32 s22, s22, 0x40080
	v_lshl_add_u64 v[226:227], v[228:229], 0, s[10:11]
	s_addc_u32 s23, s23, 0
	s_add_i32 s24, s57, s36
	global_load_lds_dwordx4 v[226:227], off
	v_lshl_add_u64 v[226:227], s[22:23], 0, v[130:131]
	s_mov_b32 m0, s24
	v_lshl_add_u64 v[224:225], v[224:225], 0, s[10:11]
	global_load_lds_dwordx4 v[226:227], off
	v_lshl_add_u64 v[226:227], s[22:23], 0, v[132:133]
	s_add_i32 m0, s24, 0x2000
	s_nop 0
	global_load_lds_dwordx4 v[226:227], off
	v_lshl_add_u64 v[226:227], v[230:231], 0, s[10:11]
	s_mov_b32 m0, s49
	s_nop 0
	global_load_lds_dwordx4 v[226:227], off
	s_mov_b32 m0, s50
	s_nop 0
	global_load_lds_dwordx4 v[224:225], off
	s_waitcnt vmcnt(8)
	s_waitcnt lgkmcnt(0)
	v_mfma_f32_16x16x32_bf16 v[62:65], v[160:163], v[192:195], v[62:65]
	v_mfma_f32_16x16x32_bf16 v[54:57], v[168:171], v[192:195], v[54:57]
	v_mfma_f32_16x16x32_bf16 v[46:49], v[160:163], v[200:203], v[46:49]
	s_barrier
	s_setprio 1
	s_waitcnt lgkmcnt(0)
	v_mfma_f32_16x16x32_bf16 v[38:41], v[168:171], v[200:203], v[38:41]
	v_mfma_f32_16x16x32_bf16 v[30:33], v[160:163], v[208:211], v[30:33]
	v_mfma_f32_16x16x32_bf16 v[22:25], v[168:171], v[208:211], v[22:25]
	v_mfma_f32_16x16x32_bf16 v[14:17], v[160:163], v[216:219], v[14:17]
	v_mfma_f32_16x16x32_bf16 v[6:9], v[168:171], v[216:219], v[6:9]
	v_mfma_f32_16x16x32_bf16 v[62:65], v[164:167], v[196:199], v[62:65]
	v_mfma_f32_16x16x32_bf16 v[54:57], v[172:175], v[196:199], v[54:57]
	v_mfma_f32_16x16x32_bf16 v[46:49], v[164:167], v[204:207], v[46:49]
	v_mfma_f32_16x16x32_bf16 v[38:41], v[172:175], v[204:207], v[38:41]
	v_mfma_f32_16x16x32_bf16 v[30:33], v[164:167], v[212:215], v[30:33]
	v_mfma_f32_16x16x32_bf16 v[22:25], v[172:175], v[212:215], v[22:25]
	v_mfma_f32_16x16x32_bf16 v[14:17], v[164:167], v[220:223], v[14:17]
	v_mfma_f32_16x16x32_bf16 v[6:9], v[172:175], v[220:223], v[6:9]
	s_setprio 0
	s_setprio 1
	v_mfma_f32_16x16x32_bf16 v[58:61], v[176:179], v[192:195], v[58:61]
	v_mfma_f32_16x16x32_bf16 v[50:53], v[184:187], v[192:195], v[50:53]
	v_mfma_f32_16x16x32_bf16 v[42:45], v[176:179], v[200:203], v[42:45]
	v_mfma_f32_16x16x32_bf16 v[34:37], v[184:187], v[200:203], v[34:37]
	v_mfma_f32_16x16x32_bf16 v[26:29], v[176:179], v[208:211], v[26:29]
	v_mfma_f32_16x16x32_bf16 v[18:21], v[184:187], v[208:211], v[18:21]
	v_mfma_f32_16x16x32_bf16 v[10:13], v[176:179], v[216:219], v[10:13]
	v_mfma_f32_16x16x32_bf16 v[2:5], v[184:187], v[216:219], v[2:5]
	v_mfma_f32_16x16x32_bf16 v[58:61], v[180:183], v[196:199], v[58:61]
	v_mfma_f32_16x16x32_bf16 v[50:53], v[188:191], v[196:199], v[50:53]
	v_mfma_f32_16x16x32_bf16 v[42:45], v[180:183], v[204:207], v[42:45]
	v_mfma_f32_16x16x32_bf16 v[34:37], v[188:191], v[204:207], v[34:37]
	v_mfma_f32_16x16x32_bf16 v[26:29], v[180:183], v[212:215], v[26:29]
	v_mfma_f32_16x16x32_bf16 v[18:21], v[188:191], v[212:215], v[18:21]
	v_mfma_f32_16x16x32_bf16 v[10:13], v[180:183], v[220:223], v[10:13]
	v_mfma_f32_16x16x32_bf16 v[2:5], v[188:191], v[220:223], v[2:5]
	s_setprio 0
	s_barrier
	s_add_i32 s55, s55, 2
	s_add_u32 s20, s20, 0x100
	s_addc_u32 s21, s21, 0
	s_cmp_gt_u32 s55, 13
	s_cbranch_scc0 .LBB0_1930
	s_and_b64 vcc, exec, s[8:9]
	s_cbranch_vccz .LBB0_1933
	s_barrier

; #define PG8_STAGE(bufoff, gbase, voff) do { _Pragma("unroll") for (int _i = 0; _i < 2; ++_i) \
;         __builtin_amdgcn_global_load_lds((const unsigned*)((const char*)(gbase) + (voff)[_i]), (PG8_LAS unsigned*)(lds + (bufoff) + ldsw + _i * 8192), 16, 0, 0); } while (0)
; #define PG8_LDA(dst, b, h) do { _Pragma("unroll") for (int m = 0; m < 4; ++m) _Pragma("unroll") for (int k = 0; k < 2; ++k) dst[m][k] = *(const PG8_LAS bf16x8*)(lds + PG8_SA(b, h) + aoff + m * 2048 + k * 1024); } while (0)
; #define PG8_LDB(dst, b, h) do { _Pragma("unroll") for (int n = 0; n < 2; ++n) _Pragma("unroll") for (int k = 0; k < 2; ++k) dst[n][k] = *(const PG8_LAS bf16x8*)(lds + PG8_SB(b, h) + boff + n * 2048 + k * 1024); } while (0)
; #define PG8_WAIT_V(n) asm volatile("s_waitcnt vmcnt(" #n ")" ::: "memory")
; #define PG8_WAIT_L(n) asm volatile("s_waitcnt lgkmcnt(" #n ")" ::: "memory")
; #define PG8_BAR __builtin_amdgcn_s_barrier()
; template <class Epi, class Sched, bool ALIGN_EPI = false, bool SP2 = false, bool GATHER = false>
; __device__ __forceinline__ void gemm_phase(PG8_LAS unsigned char* lds, const Gemm g, const Sched& S, const Epi& E, int tid_in, const int* rowsrc = nullptr, PG8_LAS int* idx_lds = nullptr) {
;     ...
;         for (int t = 0; t < nt; t += 2) {
;             const bool last = (t == nt - 2);
;             if constexpr (GATHER) {
; #pragma unroll
;                 for (int h_ = 0; h_ < 2; ++h_) { gS[h_][0] = last ? gN[h_][0] : gA[h_][0]; gS[h_][1] = last ? gN[h_][1] : gA[h_][1]; } }
;             const char* a1 = cA + (size_t)(t + 1) * kstep;
;             const char* a2 = last ? nA : cA + (size_t)(t + 2) * kstep; const char* b2 = last ? nB : cB + (size_t)(t + 2) * kstep;
;             const char* a3 = a2 + kstep; const char* b3 = b2 + kstep;
;             if (last && has_next) S.a_ready(nxt);
;             if constexpr (SP2) {
;             PG8_LDB(B0, 0, 0); PG8_LDB(B1, 0, 1); PG8_SCHED; PG8_LDA(At, 0, 0); PG8_STAGE(PG8_SA(1, 1), a1 + hstepA, PG8_OA(1));
;             PG8_WAIT_V(8); PG8_WAIT_L(0); PG8_BAR; PG8_MMA(0, 0, At, B0); PG8_MMA(0, 1, At, B1); PG8_BAR; PG8_SCHED;
;             PG8_LDA(At, 0, 1); PG8_STAGE(PG8_SB(0, 0), b2, voffB); PG8_STAGE(PG8_SB(0, 1), b2 + hstep, voffB); PG8_STAGE(PG8_SA(0, 0), a2, PG8_OS(0));
;             PG8_WAIT_V(8); PG8_WAIT_L(0); PG8_BAR; PG8_MMA(1, 0, At, B0); PG8_MMA(1, 1, At, B1); PG8_BAR; PG8_SCHED;
.LBB0_2005:
	s_add_u32 s28, s26, 0xfffc0080
	s_addc_u32 s29, s27, -1
	s_add_i32 s58, 0, 0x10000
	s_cmp_eq_u32 s57, 12
	s_cselect_b32 s31, s13, s29
	s_cselect_b32 s30, s23, s28
	v_add_u32_e32 v0, s58, v151
	s_cselect_b32 s29, s15, s56
	s_cselect_b32 s28, s43, s55
	s_add_i32 s60, 0, 0x14000
	ds_read_b128 v[142:145], v0
	ds_read_b128 v[154:157], v0 offset:1024
	ds_read_b128 v[158:161], v0 offset:2048
	ds_read_b128 v[162:165], v0 offset:3072
	v_add_u32_e32 v0, s60, v151
	ds_read_b128 v[166:169], v0
	ds_read_b128 v[170:173], v0 offset:1024
	ds_read_b128 v[174:177], v0 offset:2048
	ds_read_b128 v[178:181], v0 offset:3072
	v_lshl_add_u64 v[148:149], s[26:27], 0, v[138:139]
	s_add_i32 m0, s25, 0xc000
	ds_read_b128 v[182:185], v153
	ds_read_b128 v[186:189], v153 offset:1024
	ds_read_b128 v[190:193], v153 offset:2048
	ds_read_b128 v[194:197], v153 offset:3072
	ds_read_b128 v[198:201], v153 offset:4096
	ds_read_b128 v[202:205], v153 offset:5120
	ds_read_b128 v[206:209], v153 offset:6144
	ds_read_b128 v[210:213], v153 offset:7168
	global_load_lds_dwordx4 v[148:149], off
	v_lshl_add_u64 v[148:149], s[26:27], 0, v[140:141]
	s_add_i32 m0, s25, 0xe000
	s_nop 0
	global_load_lds_dwordx4 v[148:149], off
	s_waitcnt vmcnt(8)
	s_waitcnt lgkmcnt(0)
	v_mfma_f32_16x16x32_bf16 v[126:129], v[142:145], v[182:185], v[126:129]
	v_mfma_f32_16x16x32_bf16 v[122:125], v[158:161], v[182:185], v[122:125]
	v_mfma_f32_16x16x32_bf16 v[110:113], v[142:145], v[190:193], v[110:113]
	s_barrier
	s_setprio 1
	s_waitcnt lgkmcnt(0)
	v_mfma_f32_16x16x32_bf16 v[106:109], v[158:161], v[190:193], v[106:109]
	v_mfma_f32_16x16x32_bf16 v[94:97], v[142:145], v[198:201], v[94:97]
	v_mfma_f32_16x16x32_bf16 v[90:93], v[158:161], v[198:201], v[90:93]
	v_mfma_f32_16x16x32_bf16 v[78:81], v[142:145], v[206:209], v[78:81]
	v_mfma_f32_16x16x32_bf16 v[74:77], v[158:161], v[206:209], v[74:77]
	v_mfma_f32_16x16x32_bf16 v[126:129], v[154:157], v[186:189], v[126:129]
	v_mfma_f32_16x16x32_bf16 v[122:125], v[162:165], v[186:189], v[122:125]
	v_mfma_f32_16x16x32_bf16 v[110:113], v[154:157], v[194:197], v[110:113]
	v_mfma_f32_16x16x32_bf16 v[106:109], v[162:165], v[194:197], v[106:109]
	v_mfma_f32_16x16x32_bf16 v[94:97], v[154:157], v[202:205], v[94:97]
	v_mfma_f32_16x16x32_bf16 v[90:93], v[162:165], v[202:205], v[90:93]
	v_mfma_f32_16x16x32_bf16 v[78:81], v[154:157], v[210:213], v[78:81]
	v_mfma_f32_16x16x32_bf16 v[74:77], v[162:165], v[210:213], v[74:77]
	s_setprio 0
	s_setprio 1
	v_mfma_f32_16x16x32_bf16 v[118:121], v[166:169], v[182:185], v[118:121]
	v_mfma_f32_16x16x32_bf16 v[114:117], v[174:177], v[182:185], v[114:117]
	v_mfma_f32_16x16x32_bf16 v[102:105], v[166:169], v[190:193], v[102:105]
	v_mfma_f32_16x16x32_bf16 v[98:101], v[174:177], v[190:193], v[98:101]
	v_mfma_f32_16x16x32_bf16 v[86:89], v[166:169], v[198:201], v[86:89]
	v_mfma_f32_16x16x32_bf16 v[82:85], v[174:177], v[198:201], v[82:85]
	v_mfma_f32_16x16x32_bf16 v[70:73], v[166:169], v[206:209], v[70:73]
	v_mfma_f32_16x16x32_bf16 v[66:69], v[174:177], v[206:209], v[66:69]
	v_mfma_f32_16x16x32_bf16 v[118:121], v[170:173], v[186:189], v[118:121]
	v_mfma_f32_16x16x32_bf16 v[114:117], v[178:181], v[186:189], v[114:117]
	v_mfma_f32_16x16x32_bf16 v[102:105], v[170:173], v[194:197], v[102:105]
	v_mfma_f32_16x16x32_bf16 v[98:101], v[178:181], v[194:197], v[98:101]
	v_mfma_f32_16x16x32_bf16 v[86:89], v[170:173], v[202:205], v[86:89]
	v_mfma_f32_16x16x32_bf16 v[82:85], v[178:181], v[202:205], v[82:85]
	v_mfma_f32_16x16x32_bf16 v[70:73], v[170:173], v[210:213], v[70:73]
	v_mfma_f32_16x16x32_bf16 v[66:69], v[178:181], v[210:213], v[66:69]
	s_setprio 0
	s_barrier
	s_add_i32 s58, s58, s44
	v_lshl_add_u64 v[148:149], s[28:29], 0, v[134:135]
	s_mov_b32 m0, s58
	ds_read_b128 v[182:185], v153 offset:16384
	ds_read_b128 v[186:189], v153 offset:17408
	ds_read_b128 v[190:193], v153 offset:18432
	ds_read_b128 v[194:197], v153 offset:19456
	ds_read_b128 v[198:201], v153 offset:20480
	ds_read_b128 v[202:205], v153 offset:21504
	ds_read_b128 v[206:209], v153 offset:22528
	ds_read_b128 v[210:213], v153 offset:23552
	global_load_lds_dwordx4 v[148:149], off
	s_add_i32 m0, s58, 0x2000
	s_add_u32 s58, s28, 0x40000
	v_lshl_add_u64 v[214:215], s[28:29], 0, v[130:131]
	s_addc_u32 s59, s29, 0
	s_add_i32 s60, s60, s44
	global_load_lds_dwordx4 v[214:215], off
	v_lshl_add_u64 v[216:217], s[58:59], 0, v[134:135]
	s_mov_b32 m0, s60
	v_lshl_add_u64 v[218:219], s[30:31], 0, v[132:133]
	global_load_lds_dwordx4 v[216:217], off
	v_lshl_add_u64 v[216:217], s[58:59], 0, v[130:131]
	s_add_i32 m0, s60, 0x2000
	s_nop 0
	global_load_lds_dwordx4 v[216:217], off
	v_lshl_add_u64 v[216:217], s[30:31], 0, v[136:137]
	s_mov_b32 m0, s25
	s_nop 0
	global_load_lds_dwordx4 v[216:217], off
	s_mov_b32 m0, s48
	s_nop 0
	global_load_lds_dwordx4 v[218:219], off
	s_waitcnt vmcnt(8)
	s_waitcnt lgkmcnt(0)
	v_mfma_f32_16x16x32_bf16 v[62:65], v[142:145], v[182:185], v[62:65]
	v_mfma_f32_16x16x32_bf16 v[58:61], v[158:161], v[182:185], v[58:61]
	v_mfma_f32_16x16x32_bf16 v[46:49], v[142:145], v[190:193], v[46:49]
	s_barrier
; #define PG8_STAGE(bufoff, gbase, voff) do { _Pragma("unroll") for (int _i = 0; _i < 2; ++_i) \
;         __builtin_amdgcn_global_load_lds((const unsigned*)((const char*)(gbase) + (voff)[_i]), (PG8_LAS unsigned*)(lds + (bufoff) + ldsw + _i * 8192), 16, 0, 0); } while (0)
; #define PG8_LDA(dst, b, h) do { _Pragma("unroll") for (int m = 0; m < 4; ++m) _Pragma("unroll") for (int k = 0; k < 2; ++k) dst[m][k] = *(const PG8_LAS bf16x8*)(lds + PG8_SA(b, h) + aoff + m * 2048 + k * 1024); } while (0)
; #define PG8_LDB(dst, b, h) do { _Pragma("unroll") for (int n = 0; n < 2; ++n) _Pragma("unroll") for (int k = 0; k < 2; ++k) dst[n][k] = *(const PG8_LAS bf16x8*)(lds + PG8_SB(b, h) + boff + n * 2048 + k * 1024); } while (0)
; #define PG8_MMA(ai, bj, At, Bt) do { __builtin_amdgcn_s_setprio(1); _Pragma("unroll") for (int m = 0; m < 4; ++m) _Pragma("unroll") for (int n = 0; n < 2; ++n) _Pragma("unroll") for (int k = 0; k < 2; ++k) \
;         acc[ai][bj][m][n] = __builtin_amdgcn_mfma_f32_16x16x32_bf16(Bt[n][k], At[m][k], acc[ai][bj][m][n], 0, 0, 0); __builtin_amdgcn_s_setprio(0); } while (0)
; #define PG8_WAIT_V(n) asm volatile("s_waitcnt vmcnt(" #n ")" ::: "memory")
; #define PG8_WAIT_L(n) asm volatile("s_waitcnt lgkmcnt(" #n ")" ::: "memory")
; #define PG8_BAR __builtin_amdgcn_s_barrier()
; #define PG8_SCHED __builtin_amdgcn_sched_barrier(0)
; template <class Epi, class Sched, bool ALIGN_EPI = false, bool SP2 = false, bool GATHER = false>
; __device__ __forceinline__ void gemm_phase(PG8_LAS unsigned char* lds, const Gemm g, const Sched& S, const Epi& E, int tid_in, const int* rowsrc = nullptr, PG8_LAS int* idx_lds = nullptr) {
;     ...
;             PG8_WAIT_V(8); PG8_WAIT_L(0); PG8_BAR; PG8_MMA(1, 0, At, B0); PG8_MMA(1, 1, At, B1); PG8_BAR; PG8_SCHED;
;             PG8_LDB(B0, 1, 0); PG8_LDB(B1, 1, 1); PG8_SCHED; PG8_LDA(At, 1, 0); PG8_STAGE(PG8_SA(0, 1), a2 + hstepA, PG8_OS(1));
;             PG8_WAIT_V(8); PG8_WAIT_L(0); PG8_BAR; PG8_MMA(0, 0, At, B0); PG8_MMA(0, 1, At, B1); PG8_BAR; PG8_SCHED;
	s_setprio 1
	s_waitcnt lgkmcnt(0)
	v_mfma_f32_16x16x32_bf16 v[42:45], v[158:161], v[190:193], v[42:45]
	v_mfma_f32_16x16x32_bf16 v[30:33], v[142:145], v[198:201], v[30:33]
	v_mfma_f32_16x16x32_bf16 v[26:29], v[158:161], v[198:201], v[26:29]
	v_mfma_f32_16x16x32_bf16 v[14:17], v[142:145], v[206:209], v[14:17]
	v_mfma_f32_16x16x32_bf16 v[10:13], v[158:161], v[206:209], v[10:13]
	v_mfma_f32_16x16x32_bf16 v[62:65], v[154:157], v[186:189], v[62:65]
	v_mfma_f32_16x16x32_bf16 v[58:61], v[162:165], v[186:189], v[58:61]
	v_mfma_f32_16x16x32_bf16 v[46:49], v[154:157], v[194:197], v[46:49]
	v_mfma_f32_16x16x32_bf16 v[42:45], v[162:165], v[194:197], v[42:45]
	v_mfma_f32_16x16x32_bf16 v[30:33], v[154:157], v[202:205], v[30:33]
	v_mfma_f32_16x16x32_bf16 v[26:29], v[162:165], v[202:205], v[26:29]
	v_mfma_f32_16x16x32_bf16 v[14:17], v[154:157], v[210:213], v[14:17]
	v_mfma_f32_16x16x32_bf16 v[10:13], v[162:165], v[210:213], v[10:13]
	s_setprio 0
	s_setprio 1
	v_mfma_f32_16x16x32_bf16 v[54:57], v[166:169], v[182:185], v[54:57]
	v_mfma_f32_16x16x32_bf16 v[50:53], v[174:177], v[182:185], v[50:53]
	v_mfma_f32_16x16x32_bf16 v[38:41], v[166:169], v[190:193], v[38:41]
	v_mfma_f32_16x16x32_bf16 v[34:37], v[174:177], v[190:193], v[34:37]
	v_mfma_f32_16x16x32_bf16 v[22:25], v[166:169], v[198:201], v[22:25]
	v_mfma_f32_16x16x32_bf16 v[18:21], v[174:177], v[198:201], v[18:21]
	v_mfma_f32_16x16x32_bf16 v[6:9], v[166:169], v[206:209], v[6:9]
	v_mfma_f32_16x16x32_bf16 v[2:5], v[174:177], v[206:209], v[2:5]
	v_mfma_f32_16x16x32_bf16 v[54:57], v[170:173], v[186:189], v[54:57]
	v_mfma_f32_16x16x32_bf16 v[50:53], v[178:181], v[186:189], v[50:53]
	v_mfma_f32_16x16x32_bf16 v[38:41], v[170:173], v[194:197], v[38:41]
	v_mfma_f32_16x16x32_bf16 v[34:37], v[178:181], v[194:197], v[34:37]
	v_mfma_f32_16x16x32_bf16 v[22:25], v[170:173], v[202:205], v[22:25]
	v_mfma_f32_16x16x32_bf16 v[18:21], v[178:181], v[202:205], v[18:21]
	v_mfma_f32_16x16x32_bf16 v[6:9], v[170:173], v[210:213], v[6:9]
	v_mfma_f32_16x16x32_bf16 v[2:5], v[178:181], v[210:213], v[2:5]
	s_setprio 0
	s_barrier
	s_add_i32 s58, 0, 0x18000
	v_add_u32_e32 v0, s58, v151
	s_add_i32 s59, 0, 0x1c000
	ds_read_b128 v[142:145], v0
	ds_read_b128 v[154:157], v0 offset:1024
	ds_read_b128 v[158:161], v0 offset:2048
	ds_read_b128 v[162:165], v0 offset:3072
	v_add_u32_e32 v0, s59, v151
	ds_read_b128 v[166:169], v0
	ds_read_b128 v[170:173], v0 offset:1024
	ds_read_b128 v[174:177], v0 offset:2048
	ds_read_b128 v[178:181], v0 offset:3072
	s_add_u32 s30, s30, 0x40000
	s_addc_u32 s31, s31, 0
	s_mov_b32 m0, s49
	v_lshl_add_u64 v[220:221], s[30:31], 0, v[136:137]
	ds_read_b128 v[182:185], v153 offset:32768
	ds_read_b128 v[186:189], v153 offset:33792
	ds_read_b128 v[190:193], v153 offset:34816
	ds_read_b128 v[194:197], v153 offset:35840
	ds_read_b128 v[198:201], v153 offset:36864
	ds_read_b128 v[202:205], v153 offset:37888
	ds_read_b128 v[206:209], v153 offset:38912
	ds_read_b128 v[210:213], v153 offset:39936
	global_load_lds_dwordx4 v[220:221], off
	v_lshl_add_u64 v[220:221], s[30:31], 0, v[132:133]
	s_mov_b32 m0, s50
	s_nop 0
	global_load_lds_dwordx4 v[220:221], off
	s_waitcnt vmcnt(8)
	s_waitcnt lgkmcnt(0)
	v_mfma_f32_16x16x32_bf16 v[126:129], v[142:145], v[182:185], v[126:129]
	v_mfma_f32_16x16x32_bf16 v[122:125], v[158:161], v[182:185], v[122:125]
	v_mfma_f32_16x16x32_bf16 v[110:113], v[142:145], v[190:193], v[110:113]
	s_barrier
	s_setprio 1
	s_waitcnt lgkmcnt(0)
	v_mfma_f32_16x16x32_bf16 v[106:109], v[158:161], v[190:193], v[106:109]
	v_mfma_f32_16x16x32_bf16 v[94:97], v[142:145], v[198:201], v[94:97]
	v_mfma_f32_16x16x32_bf16 v[90:93], v[158:161], v[198:201], v[90:93]
	v_mfma_f32_16x16x32_bf16 v[78:81], v[142:145], v[206:209], v[78:81]
	v_mfma_f32_16x16x32_bf16 v[74:77], v[158:161], v[206:209], v[74:77]
	v_mfma_f32_16x16x32_bf16 v[126:129], v[154:157], v[186:189], v[126:129]
	v_mfma_f32_16x16x32_bf16 v[122:125], v[162:165], v[186:189], v[122:125]
	v_mfma_f32_16x16x32_bf16 v[110:113], v[154:157], v[194:197], v[110:113]
	v_mfma_f32_16x16x32_bf16 v[106:109], v[162:165], v[194:197], v[106:109]
	v_mfma_f32_16x16x32_bf16 v[94:97], v[154:157], v[202:205], v[94:97]
	v_mfma_f32_16x16x32_bf16 v[90:93], v[162:165], v[202:205], v[90:93]
	v_mfma_f32_16x16x32_bf16 v[78:81], v[154:157], v[210:213], v[78:81]
	v_mfma_f32_16x16x32_bf16 v[74:77], v[162:165], v[210:213], v[74:77]
	s_setprio 0
	s_setprio 1
	v_mfma_f32_16x16x32_bf16 v[118:121], v[166:169], v[182:185], v[118:121]
	v_mfma_f32_16x16x32_bf16 v[114:117], v[174:177], v[182:185], v[114:117]
	v_mfma_f32_16x16x32_bf16 v[102:105], v[166:169], v[190:193], v[102:105]
	v_mfma_f32_16x16x32_bf16 v[98:101], v[174:177], v[190:193], v[98:101]
	v_mfma_f32_16x16x32_bf16 v[86:89], v[166:169], v[198:201], v[86:89]
	v_mfma_f32_16x16x32_bf16 v[82:85], v[174:177], v[198:201], v[82:85]
	v_mfma_f32_16x16x32_bf16 v[70:73], v[166:169], v[206:209], v[70:73]
	v_mfma_f32_16x16x32_bf16 v[66:69], v[174:177], v[206:209], v[66:69]
	v_mfma_f32_16x16x32_bf16 v[118:121], v[170:173], v[186:189], v[118:121]
	v_mfma_f32_16x16x32_bf16 v[114:117], v[178:181], v[186:189], v[114:117]
	v_mfma_f32_16x16x32_bf16 v[102:105], v[170:173], v[194:197], v[102:105]
	v_mfma_f32_16x16x32_bf16 v[98:101], v[178:181], v[194:197], v[98:101]
	v_mfma_f32_16x16x32_bf16 v[86:89], v[170:173], v[202:205], v[86:89]
	v_mfma_f32_16x16x32_bf16 v[82:85], v[178:181], v[202:205], v[82:85]
	v_mfma_f32_16x16x32_bf16 v[70:73], v[170:173], v[210:213], v[70:73]
	v_mfma_f32_16x16x32_bf16 v[66:69], v[178:181], v[210:213], v[66:69]
	s_setprio 0
	s_barrier
; #define PG8_STAGE(bufoff, gbase, voff) do { _Pragma("unroll") for (int _i = 0; _i < 2; ++_i) \
;         __builtin_amdgcn_global_load_lds((const unsigned*)((const char*)(gbase) + (voff)[_i]), (PG8_LAS unsigned*)(lds + (bufoff) + ldsw + _i * 8192), 16, 0, 0); } while (0)
; #define PG8_LDA(dst, b, h) do { _Pragma("unroll") for (int m = 0; m < 4; ++m) _Pragma("unroll") for (int k = 0; k < 2; ++k) dst[m][k] = *(const PG8_LAS bf16x8*)(lds + PG8_SA(b, h) + aoff + m * 2048 + k * 1024); } while (0)
; #define PG8_MMA(ai, bj, At, Bt) do { __builtin_amdgcn_s_setprio(1); _Pragma("unroll") for (int m = 0; m < 4; ++m) _Pragma("unroll") for (int n = 0; n < 2; ++n) _Pragma("unroll") for (int k = 0; k < 2; ++k) \
;         acc[ai][bj][m][n] = __builtin_amdgcn_mfma_f32_16x16x32_bf16(Bt[n][k], At[m][k], acc[ai][bj][m][n], 0, 0, 0); __builtin_amdgcn_s_setprio(0); } while (0)
; #define PG8_WAIT_V(n) asm volatile("s_waitcnt vmcnt(" #n ")" ::: "memory")
; #define PG8_WAIT_L(n) asm volatile("s_waitcnt lgkmcnt(" #n ")" ::: "memory")
; #define PG8_BAR __builtin_amdgcn_s_barrier()
; #define PG8_SCHED __builtin_amdgcn_sched_barrier(0)
; template <class Epi, class Sched, bool ALIGN_EPI = false, bool SP2 = false, bool GATHER = false>
; __device__ __forceinline__ void gemm_phase(PG8_LAS unsigned char* lds, const Gemm g, const Sched& S, const Epi& E, int tid_in, const int* rowsrc = nullptr, PG8_LAS int* idx_lds = nullptr) {
;     ...
;             PG8_LDA(At, 1, 1); PG8_STAGE(PG8_SB(1, 0), b3, voffB); PG8_STAGE(PG8_SB(1, 1), b3 + hstep, voffB); PG8_STAGE(PG8_SA(1, 0), a3, PG8_OS(0));
;             PG8_WAIT_V(8); PG8_WAIT_L(0); PG8_BAR; PG8_MMA(1, 0, At, B0); PG8_MMA(1, 1, At, B1); PG8_BAR; PG8_SCHED;
;     ...
;         if constexpr (ALIGN_EPI) { if (wr == 0) PG8_BAR; }
	s_add_i32 s30, s58, s44
	v_lshl_add_u64 v[148:149], v[148:149], 0, s[10:11]
	s_mov_b32 m0, s30
	ds_read_b128 v[182:185], v153 offset:49152
	ds_read_b128 v[186:189], v153 offset:50176
	ds_read_b128 v[190:193], v153 offset:51200
	ds_read_b128 v[194:197], v153 offset:52224
	ds_read_b128 v[198:201], v153 offset:53248
	ds_read_b128 v[202:205], v153 offset:54272
	ds_read_b128 v[206:209], v153 offset:55296
	ds_read_b128 v[210:213], v153 offset:56320
	global_load_lds_dwordx4 v[148:149], off
	s_add_i32 m0, s30, 0x2000
	s_add_u32 s28, s28, 0x40080
	v_lshl_add_u64 v[148:149], v[214:215], 0, s[10:11]
	s_addc_u32 s29, s29, 0
	s_add_i32 s30, s59, s44
	global_load_lds_dwordx4 v[148:149], off
	v_lshl_add_u64 v[148:149], s[28:29], 0, v[134:135]
	s_mov_b32 m0, s30
	s_nop 0
	global_load_lds_dwordx4 v[148:149], off
	v_lshl_add_u64 v[148:149], s[28:29], 0, v[130:131]
	s_add_i32 m0, s30, 0x2000
	s_nop 0
	global_load_lds_dwordx4 v[148:149], off
	v_lshl_add_u64 v[148:149], v[216:217], 0, s[10:11]
	s_mov_b32 m0, s51
	s_nop 0
	global_load_lds_dwordx4 v[148:149], off
	v_lshl_add_u64 v[148:149], v[218:219], 0, s[10:11]
	s_mov_b32 m0, s52
	s_nop 0
	global_load_lds_dwordx4 v[148:149], off
	s_waitcnt vmcnt(8)
	s_waitcnt lgkmcnt(0)
	v_mfma_f32_16x16x32_bf16 v[62:65], v[142:145], v[182:185], v[62:65]
	v_mfma_f32_16x16x32_bf16 v[58:61], v[158:161], v[182:185], v[58:61]
	v_mfma_f32_16x16x32_bf16 v[46:49], v[142:145], v[190:193], v[46:49]
	s_barrier
	s_setprio 1
	s_waitcnt lgkmcnt(0)
	v_mfma_f32_16x16x32_bf16 v[42:45], v[158:161], v[190:193], v[42:45]
	v_mfma_f32_16x16x32_bf16 v[30:33], v[142:145], v[198:201], v[30:33]
	v_mfma_f32_16x16x32_bf16 v[26:29], v[158:161], v[198:201], v[26:29]
	v_mfma_f32_16x16x32_bf16 v[14:17], v[142:145], v[206:209], v[14:17]
	v_mfma_f32_16x16x32_bf16 v[10:13], v[158:161], v[206:209], v[10:13]
	v_mfma_f32_16x16x32_bf16 v[62:65], v[154:157], v[186:189], v[62:65]
	v_mfma_f32_16x16x32_bf16 v[58:61], v[162:165], v[186:189], v[58:61]
	v_mfma_f32_16x16x32_bf16 v[46:49], v[154:157], v[194:197], v[46:49]
	v_mfma_f32_16x16x32_bf16 v[42:45], v[162:165], v[194:197], v[42:45]
	v_mfma_f32_16x16x32_bf16 v[30:33], v[154:157], v[202:205], v[30:33]
	v_mfma_f32_16x16x32_bf16 v[26:29], v[162:165], v[202:205], v[26:29]
	v_mfma_f32_16x16x32_bf16 v[14:17], v[154:157], v[210:213], v[14:17]
	v_mfma_f32_16x16x32_bf16 v[10:13], v[162:165], v[210:213], v[10:13]
	s_setprio 0
	s_setprio 1
	v_mfma_f32_16x16x32_bf16 v[54:57], v[166:169], v[182:185], v[54:57]
	v_mfma_f32_16x16x32_bf16 v[50:53], v[174:177], v[182:185], v[50:53]
	v_mfma_f32_16x16x32_bf16 v[38:41], v[166:169], v[190:193], v[38:41]
	v_mfma_f32_16x16x32_bf16 v[34:37], v[174:177], v[190:193], v[34:37]
	v_mfma_f32_16x16x32_bf16 v[22:25], v[166:169], v[198:201], v[22:25]
	v_mfma_f32_16x16x32_bf16 v[18:21], v[174:177], v[198:201], v[18:21]
	v_mfma_f32_16x16x32_bf16 v[6:9], v[166:169], v[206:209], v[6:9]
	v_mfma_f32_16x16x32_bf16 v[2:5], v[174:177], v[206:209], v[2:5]
	v_mfma_f32_16x16x32_bf16 v[54:57], v[170:173], v[186:189], v[54:57]
	v_mfma_f32_16x16x32_bf16 v[50:53], v[178:181], v[186:189], v[50:53]
	v_mfma_f32_16x16x32_bf16 v[38:41], v[170:173], v[194:197], v[38:41]
	v_mfma_f32_16x16x32_bf16 v[34:37], v[178:181], v[194:197], v[34:37]
	v_mfma_f32_16x16x32_bf16 v[22:25], v[170:173], v[202:205], v[22:25]
	v_mfma_f32_16x16x32_bf16 v[18:21], v[178:181], v[202:205], v[18:21]
	v_mfma_f32_16x16x32_bf16 v[6:9], v[170:173], v[210:213], v[6:9]
	v_mfma_f32_16x16x32_bf16 v[2:5], v[178:181], v[210:213], v[2:5]
	s_setprio 0
	s_barrier
	s_add_i32 s57, s57, 2
	s_add_u32 s26, s26, 0x100
	s_addc_u32 s27, s27, 0
	s_add_u32 s55, s55, 0x100
	s_addc_u32 s56, s56, 0
	s_cmp_gt_u32 s57, 13
	s_cbranch_scc0 .LBB0_2005
	s_and_b64 vcc, exec, s[8:9]
	s_cbranch_vccz .LBB0_2008
	s_barrier
